# topk half-merge lane exchange via v_permlane32_swap (self swap) instead of ds_bpermute
# baseline (speedup 1.0000x reference)
.LBB0_704:
	v_cndmask_b32_e64 v0, 0, 1, s[6:7]
	s_lshl_b32 s36, s8, 8
	v_cmp_ne_u32_e32 vcc, 1, v0
	v_lshl_add_u64 v[0:1], v[178:179], 0, s[36:37]
	global_load_dwordx4 v[44:47], v[0:1], off
	global_load_dwordx4 v[40:43], v[0:1], off offset:32
	global_load_dwordx4 v[36:39], v[0:1], off offset:64
	global_load_dwordx4 v[32:35], v[0:1], off offset:96
	global_load_dwordx4 v[28:31], v[0:1], off offset:128
	global_load_dwordx4 v[24:27], v[0:1], off offset:160
	global_load_dwordx4 v[20:23], v[0:1], off offset:192
	global_load_dwordx4 v[16:19], v[0:1], off offset:224
	v_lshl_or_b32 v180, s8, 7, v209
	v_ashrrev_i32_e32 v181, 31, v180
	v_lshlrev_b64 v[0:1], 8, v[180:181]
	v_lshl_add_u64 v[60:61], v[64:65], 0, v[0:1]
	global_load_dwordx4 v[0:3], v[60:61], off
	global_load_dwordx4 v[48:51], v[60:61], off offset:32
	global_load_dwordx4 v[52:55], v[60:61], off offset:64
	global_load_dwordx4 v[56:59], v[60:61], off offset:96
	s_nop 15
	s_nop 15
	s_waitcnt vmcnt(0)
	v_mfma_f32_32x32x16_bf16 v[0:15], v[0:3], v[44:47], 0
	v_mfma_f32_32x32x16_bf16 v[0:15], v[48:51], v[40:43], v[0:15]
	v_mfma_f32_32x32x16_bf16 v[0:15], v[52:55], v[36:39], v[0:15]
	v_mfma_f32_32x32x16_bf16 v[0:15], v[56:59], v[32:35], v[0:15]
	s_nop 15
	s_nop 15
	global_load_dwordx4 v[48:51], v[60:61], off offset:128
	global_load_dwordx4 v[52:55], v[60:61], off offset:160
	global_load_dwordx4 v[56:59], v[60:61], off offset:192
	s_nop 0
	global_load_dwordx4 v[60:63], v[60:61], off offset:224
	s_nop 15
	s_nop 15
	s_waitcnt vmcnt(3)
	v_mfma_f32_32x32x16_bf16 v[0:15], v[48:51], v[28:31], v[0:15]
	s_waitcnt vmcnt(2)
	v_mfma_f32_32x32x16_bf16 v[0:15], v[52:55], v[24:27], v[0:15]
	s_waitcnt vmcnt(1)
	v_mfma_f32_32x32x16_bf16 v[0:15], v[56:59], v[20:23], v[0:15]
	s_waitcnt vmcnt(0)
	v_mfma_f32_32x32x16_bf16 v[0:15], v[60:63], v[16:19], v[0:15]
	s_nop 15
	s_nop 15
	v_or_b32_e32 v49, 1, v66
	v_xor_b32_e32 v51, 0x7e, v66
	s_nop 9
	v_cmp_gt_i32_e64 s[6:7], 0, v1
	v_xor_b32_e32 v48, 0x7f, v66
	v_and_b32_e32 v1, 0xffffff80, v1
	v_cndmask_b32_e64 v49, v51, v49, s[6:7]
	v_cmp_gt_i32_e64 s[6:7], 0, v0
	v_and_b32_e32 v0, 0xffffff80, v0
	v_or_b32_e32 v210, v49, v1
	v_cndmask_b32_e64 v48, v48, v66, s[6:7]
	v_or_b32_e32 v211, v48, v0
	v_or_b32_e32 v48, 32, v180
	v_ashrrev_i32_e32 v49, 31, v48
	v_lshlrev_b64 v[48:49], 8, v[48:49]
	v_lshl_add_u64 v[182:183], v[64:65], 0, v[48:49]
	global_load_dwordx4 v[60:63], v[182:183], off
	global_load_dwordx4 v[56:59], v[182:183], off offset:32
	global_load_dwordx4 v[52:55], v[182:183], off offset:64
	global_load_dwordx4 v[48:51], v[182:183], off offset:96
	v_or_b32_e32 v1, 3, v66
	v_xor_b32_e32 v173, 0x7c, v66
	v_cmp_gt_i32_e64 s[6:7], 0, v3
	v_or_b32_e32 v0, 2, v66
	v_xor_b32_e32 v190, 0x7d, v66
	v_cndmask_b32_e64 v1, v173, v1, s[6:7]
	v_cmp_gt_i32_e64 s[6:7], 0, v2
	v_and_b32_e32 v3, 0xffffff80, v3
	v_and_b32_e32 v2, 0xffffff80, v2
	v_cndmask_b32_e64 v0, v190, v0, s[6:7]
	v_or_b32_e32 v173, v1, v3
	v_or_b32_e32 v1, 9, v66
	v_xor_b32_e32 v3, 0x76, v66
	v_cmp_gt_i32_e64 s[6:7], 0, v5
	v_or_b32_e32 v212, v0, v2
	v_or_b32_e32 v0, 8, v66
	v_cndmask_b32_e64 v1, v3, v1, s[6:7]
	v_xor_b32_e32 v2, 0x77, v66
	v_cmp_gt_i32_e64 s[6:7], 0, v4
	v_and_b32_e32 v3, 0xffffff80, v4
	s_nop 0
	v_cndmask_b32_e64 v0, v2, v0, s[6:7]
	v_and_b32_e32 v2, 0xffffff80, v5
	v_or_b32_e32 v213, v1, v2
	v_or_b32_e32 v214, v0, v3
	v_or_b32_e32 v1, 11, v66
	v_xor_b32_e32 v3, 0x74, v66
	v_cmp_gt_i32_e64 s[6:7], 0, v7
	v_or_b32_e32 v0, 10, v66
	v_xor_b32_e32 v2, 0x75, v66
	v_cndmask_b32_e64 v1, v3, v1, s[6:7]
	v_cmp_gt_i32_e64 s[6:7], 0, v6
	v_and_b32_e32 v3, 0xffffff80, v6
	s_nop 0
	v_cndmask_b32_e64 v0, v2, v0, s[6:7]
	v_and_b32_e32 v2, 0xffffff80, v7
	v_or_b32_e32 v215, v1, v2
	v_or_b32_e32 v216, v0, v3
	v_or_b32_e32 v1, 17, v66
	v_xor_b32_e32 v3, 0x6e, v66
	v_cmp_gt_i32_e64 s[6:7], 0, v9
	v_or_b32_e32 v0, 16, v66
	v_xor_b32_e32 v2, 0x6f, v66
	v_cndmask_b32_e64 v1, v3, v1, s[6:7]
	v_cmp_gt_i32_e64 s[6:7], 0, v8
	v_and_b32_e32 v3, 0xffffff80, v8
	s_nop 0
	v_cndmask_b32_e64 v0, v2, v0, s[6:7]
	v_and_b32_e32 v2, 0xffffff80, v9
	v_or_b32_e32 v217, v1, v2
	v_or_b32_e32 v218, v0, v3
	v_or_b32_e32 v1, 19, v66
	v_xor_b32_e32 v3, 0x6c, v66
	v_cmp_gt_i32_e64 s[6:7], 0, v11
	v_or_b32_e32 v0, 18, v66
	v_xor_b32_e32 v2, 0x6d, v66
	v_cndmask_b32_e64 v1, v3, v1, s[6:7]
	v_cmp_gt_i32_e64 s[6:7], 0, v10
	v_and_b32_e32 v3, 0xffffff80, v10
	s_nop 0
	v_cndmask_b32_e64 v0, v2, v0, s[6:7]
	v_and_b32_e32 v2, 0xffffff80, v11
	v_or_b32_e32 v219, v1, v2
	v_or_b32_e32 v220, v0, v3
	v_or_b32_e32 v1, 25, v66
	v_xor_b32_e32 v3, 0x66, v66
	v_cmp_gt_i32_e64 s[6:7], 0, v13
	v_or_b32_e32 v0, 24, v66
	v_xor_b32_e32 v2, 0x67, v66
	v_cndmask_b32_e64 v1, v3, v1, s[6:7]
	v_cmp_gt_i32_e64 s[6:7], 0, v12
	v_and_b32_e32 v3, 0xffffff80, v12
	s_nop 0
	v_cndmask_b32_e64 v0, v2, v0, s[6:7]
	v_and_b32_e32 v2, 0xffffff80, v13
	v_or_b32_e32 v221, v1, v2
	v_or_b32_e32 v1, 27, v66
	v_cmp_gt_i32_e64 s[6:7], 0, v15
	v_or_b32_e32 v222, v0, v3
	v_and_b32_e32 v2, 0xffffff80, v15
	v_cndmask_b32_e64 v0, v67, v1, s[6:7]
	v_cmp_gt_i32_e64 s[6:7], 0, v14
	v_and_b32_e32 v3, 0xffffff80, v14
	v_or_b32_e32 v223, v0, v2
	v_cndmask_b32_e64 v1, v70, v68, s[6:7]
	v_or_b32_e32 v224, v1, v3
	s_nop 15
	s_nop 15
	s_waitcnt vmcnt(3)
	v_mfma_f32_32x32x16_bf16 v[0:15], v[60:63], v[44:47], 0
	s_waitcnt vmcnt(2)
	v_mfma_f32_32x32x16_bf16 v[0:15], v[56:59], v[40:43], v[0:15]
	s_waitcnt vmcnt(1)
	v_mfma_f32_32x32x16_bf16 v[0:15], v[52:55], v[36:39], v[0:15]
	s_waitcnt vmcnt(0)
	v_mfma_f32_32x32x16_bf16 v[0:15], v[48:51], v[32:35], v[0:15]
	s_nop 15
	s_nop 15
	global_load_dwordx4 v[48:51], v[182:183], off offset:128
	global_load_dwordx4 v[52:55], v[182:183], off offset:160
	global_load_dwordx4 v[56:59], v[182:183], off offset:192
	global_load_dwordx4 v[60:63], v[182:183], off offset:224
	s_nop 15
	s_nop 15
	s_waitcnt vmcnt(3)
	v_mfma_f32_32x32x16_bf16 v[0:15], v[48:51], v[28:31], v[0:15]
	s_waitcnt vmcnt(2)
	v_mfma_f32_32x32x16_bf16 v[0:15], v[52:55], v[24:27], v[0:15]
	s_waitcnt vmcnt(1)
	v_mfma_f32_32x32x16_bf16 v[0:15], v[56:59], v[20:23], v[0:15]
	s_waitcnt vmcnt(0)
	v_mfma_f32_32x32x16_bf16 v[0:15], v[60:63], v[16:19], v[0:15]
	s_nop 15
	s_nop 15
	v_or_b32_e32 v48, 64, v180
	v_ashrrev_i32_e32 v49, 31, v48
	v_lshlrev_b64 v[48:49], 8, v[48:49]
	v_lshl_add_u64 v[182:183], v[64:65], 0, v[48:49]
	global_load_dwordx4 v[60:63], v[182:183], off
	global_load_dwordx4 v[56:59], v[182:183], off offset:32
	global_load_dwordx4 v[52:55], v[182:183], off offset:64
	global_load_dwordx4 v[48:51], v[182:183], off offset:96
	s_nop 3
	v_cmp_gt_i32_e64 s[6:7], 0, v1
	v_and_b32_e32 v1, 0xffffff80, v1
	s_nop 0
	v_cndmask_b32_e64 v181, v71, v69, s[6:7]
	v_cmp_gt_i32_e64 s[6:7], 0, v0
	v_and_b32_e32 v0, 0xffffff80, v0
	v_or_b32_e32 v225, v181, v1
	v_cndmask_b32_e64 v190, v74, v72, s[6:7]
	v_cmp_gt_i32_e64 s[6:7], 0, v3
	v_or_b32_e32 v226, v190, v0
	v_and_b32_e32 v3, 0xffffff80, v3
	v_cndmask_b32_e64 v0, v75, v73, s[6:7]
	v_cmp_gt_i32_e64 s[6:7], 0, v2
	v_and_b32_e32 v2, 0xffffff80, v2
	v_or_b32_e32 v227, v0, v3
	v_cndmask_b32_e64 v1, v78, v76, s[6:7]
	v_cmp_gt_i32_e64 s[6:7], 0, v5
	v_or_b32_e32 v228, v1, v2
	v_and_b32_e32 v2, 0xffffff80, v5
	v_cndmask_b32_e64 v0, v79, v77, s[6:7]
	v_cmp_gt_i32_e64 s[6:7], 0, v4
	v_and_b32_e32 v3, 0xffffff80, v4
	v_or_b32_e32 v229, v0, v2
	v_cndmask_b32_e64 v1, v82, v80, s[6:7]
	v_cmp_gt_i32_e64 s[6:7], 0, v7
	v_or_b32_e32 v230, v1, v3
	v_and_b32_e32 v2, 0xffffff80, v7
	v_cndmask_b32_e64 v0, v83, v81, s[6:7]
	v_cmp_gt_i32_e64 s[6:7], 0, v6
	v_and_b32_e32 v3, 0xffffff80, v6
	v_or_b32_e32 v231, v0, v2
	v_cndmask_b32_e64 v1, v86, v84, s[6:7]
	v_cmp_gt_i32_e64 s[6:7], 0, v9
	v_or_b32_e32 v232, v1, v3
	v_and_b32_e32 v2, 0xffffff80, v9
	v_cndmask_b32_e64 v0, v87, v85, s[6:7]
	v_cmp_gt_i32_e64 s[6:7], 0, v8
	v_and_b32_e32 v3, 0xffffff80, v8
	v_or_b32_e32 v233, v0, v2
	v_cndmask_b32_e64 v1, v90, v88, s[6:7]
	v_cmp_gt_i32_e64 s[6:7], 0, v11
	v_or_b32_e32 v234, v1, v3
	v_and_b32_e32 v2, 0xffffff80, v11
	v_cndmask_b32_e64 v0, v91, v89, s[6:7]
	v_cmp_gt_i32_e64 s[6:7], 0, v10
	v_and_b32_e32 v3, 0xffffff80, v10
	v_or_b32_e32 v235, v0, v2
	v_cndmask_b32_e64 v1, v94, v92, s[6:7]
	v_cmp_gt_i32_e64 s[6:7], 0, v13
	v_or_b32_e32 v236, v1, v3
	v_and_b32_e32 v2, 0xffffff80, v13
	v_cndmask_b32_e64 v0, v95, v93, s[6:7]
	v_cmp_gt_i32_e64 s[6:7], 0, v12
	v_and_b32_e32 v3, 0xffffff80, v12
	v_or_b32_e32 v237, v0, v2
	v_cndmask_b32_e64 v1, v98, v96, s[6:7]
	v_cmp_gt_i32_e64 s[6:7], 0, v15
	v_or_b32_e32 v238, v1, v3
	v_and_b32_e32 v2, 0xffffff80, v15
	v_cndmask_b32_e64 v0, v99, v97, s[6:7]
	v_cmp_gt_i32_e64 s[6:7], 0, v14
	v_and_b32_e32 v3, 0xffffff80, v14
	v_or_b32_e32 v239, v0, v2
	v_cndmask_b32_e64 v1, v102, v100, s[6:7]
	v_or_b32_e32 v240, v1, v3
	s_nop 15
	s_nop 15
	s_waitcnt vmcnt(3)
	v_mfma_f32_32x32x16_bf16 v[0:15], v[60:63], v[44:47], 0
	s_waitcnt vmcnt(2)
	v_mfma_f32_32x32x16_bf16 v[0:15], v[56:59], v[40:43], v[0:15]
	s_waitcnt vmcnt(1)
	v_mfma_f32_32x32x16_bf16 v[0:15], v[52:55], v[36:39], v[0:15]
	s_waitcnt vmcnt(0)
	v_mfma_f32_32x32x16_bf16 v[0:15], v[48:51], v[32:35], v[0:15]
	s_nop 15
	s_nop 15
	global_load_dwordx4 v[48:51], v[182:183], off offset:128
	global_load_dwordx4 v[52:55], v[182:183], off offset:160
	global_load_dwordx4 v[56:59], v[182:183], off offset:192
	global_load_dwordx4 v[60:63], v[182:183], off offset:224
	s_nop 15
	s_nop 15
	s_waitcnt vmcnt(3)
	v_mfma_f32_32x32x16_bf16 v[0:15], v[48:51], v[28:31], v[0:15]
	s_waitcnt vmcnt(2)
	v_mfma_f32_32x32x16_bf16 v[0:15], v[52:55], v[24:27], v[0:15]
	s_waitcnt vmcnt(1)
	v_mfma_f32_32x32x16_bf16 v[0:15], v[56:59], v[20:23], v[0:15]
	s_waitcnt vmcnt(0)
	v_mfma_f32_32x32x16_bf16 v[0:15], v[60:63], v[16:19], v[0:15]
	s_nop 15
	s_nop 15
	v_or_b32_e32 v48, 0x60, v180
	v_ashrrev_i32_e32 v49, 31, v48
	v_lshlrev_b64 v[48:49], 8, v[48:49]
	v_lshl_add_u64 v[180:181], v[64:65], 0, v[48:49]
	global_load_dwordx4 v[60:63], v[180:181], off
	global_load_dwordx4 v[56:59], v[180:181], off offset:32
	global_load_dwordx4 v[52:55], v[180:181], off offset:64
	global_load_dwordx4 v[48:51], v[180:181], off offset:96
	s_nop 3
	v_cmp_gt_i32_e64 s[6:7], 0, v1
	v_and_b32_e32 v1, 0xffffff80, v1
	s_nop 0
	v_cndmask_b32_e64 v182, v103, v101, s[6:7]
	v_cmp_gt_i32_e64 s[6:7], 0, v0
	v_and_b32_e32 v0, 0xffffff80, v0
	v_or_b32_e32 v182, v182, v1
	v_cndmask_b32_e64 v183, v106, v104, s[6:7]
	v_cmp_gt_i32_e64 s[6:7], 0, v3
	v_or_b32_e32 v183, v183, v0
	v_and_b32_e32 v3, 0xffffff80, v3
	v_cndmask_b32_e64 v0, v107, v105, s[6:7]
	v_cmp_gt_i32_e64 s[6:7], 0, v2
	v_and_b32_e32 v2, 0xffffff80, v2
	v_or_b32_e32 v241, v0, v3
	v_cndmask_b32_e64 v1, v110, v108, s[6:7]
	v_cmp_gt_i32_e64 s[6:7], 0, v5
	v_or_b32_e32 v242, v1, v2
	v_and_b32_e32 v2, 0xffffff80, v5
	v_cndmask_b32_e64 v0, v111, v109, s[6:7]
	v_cmp_gt_i32_e64 s[6:7], 0, v4
	v_and_b32_e32 v3, 0xffffff80, v4
	v_or_b32_e32 v243, v0, v2
	v_cndmask_b32_e64 v1, v114, v112, s[6:7]
	v_cmp_gt_i32_e64 s[6:7], 0, v7
	v_or_b32_e32 v244, v1, v3
	v_and_b32_e32 v2, 0xffffff80, v7
	v_cndmask_b32_e64 v0, v115, v113, s[6:7]
	v_cmp_gt_i32_e64 s[6:7], 0, v6
	v_and_b32_e32 v3, 0xffffff80, v6
	v_or_b32_e32 v245, v0, v2
	v_cndmask_b32_e64 v1, v118, v116, s[6:7]
	v_cmp_gt_i32_e64 s[6:7], 0, v9
	v_or_b32_e32 v246, v1, v3
	v_and_b32_e32 v2, 0xffffff80, v9
	v_cndmask_b32_e64 v0, v119, v117, s[6:7]
	v_cmp_gt_i32_e64 s[6:7], 0, v8
	v_and_b32_e32 v3, 0xffffff80, v8
	v_or_b32_e32 v247, v0, v2
	v_cndmask_b32_e64 v1, v122, v120, s[6:7]
	v_cmp_gt_i32_e64 s[6:7], 0, v11
	v_or_b32_e32 v248, v1, v3
	v_and_b32_e32 v2, 0xffffff80, v11
	v_cndmask_b32_e64 v0, v123, v121, s[6:7]
	v_cmp_gt_i32_e64 s[6:7], 0, v10
	v_and_b32_e32 v3, 0xffffff80, v10
	v_or_b32_e32 v249, v0, v2
	v_cndmask_b32_e64 v1, v126, v124, s[6:7]
	v_cmp_gt_i32_e64 s[6:7], 0, v13
	v_or_b32_e32 v250, v1, v3
	v_and_b32_e32 v2, 0xffffff80, v13
	v_cndmask_b32_e64 v0, v127, v125, s[6:7]
	v_cmp_gt_i32_e64 s[6:7], 0, v12
	v_and_b32_e32 v3, 0xffffff80, v12
	v_or_b32_e32 v251, v0, v2
	v_cndmask_b32_e64 v1, v130, v128, s[6:7]
	v_cmp_gt_i32_e64 s[6:7], 0, v15
	v_or_b32_e32 v252, v1, v3
	v_and_b32_e32 v2, 0xffffff80, v15
	v_cndmask_b32_e64 v0, v131, v129, s[6:7]
	v_cmp_gt_i32_e64 s[6:7], 0, v14
	v_and_b32_e32 v3, 0xffffff80, v14
	v_or_b32_e32 v190, v0, v2
	v_cndmask_b32_e64 v1, v134, v132, s[6:7]
	v_or_b32_e32 v195, v1, v3
	s_nop 15
	s_nop 15
	s_waitcnt vmcnt(3)
	v_mfma_f32_32x32x16_bf16 v[0:15], v[60:63], v[44:47], 0
	s_waitcnt vmcnt(2)
	v_mfma_f32_32x32x16_bf16 v[0:15], v[56:59], v[40:43], v[0:15]
	s_waitcnt vmcnt(1)
	v_mfma_f32_32x32x16_bf16 v[0:15], v[52:55], v[36:39], v[0:15]
	s_waitcnt vmcnt(0)
	v_mfma_f32_32x32x16_bf16 v[0:15], v[48:51], v[32:35], v[0:15]
	s_nop 15
	s_nop 15
	global_load_dwordx4 v[32:35], v[180:181], off offset:128
	global_load_dwordx4 v[36:39], v[180:181], off offset:160
	global_load_dwordx4 v[40:43], v[180:181], off offset:192
	global_load_dwordx4 v[44:47], v[180:181], off offset:224
	s_nop 15
	s_nop 15
	s_waitcnt vmcnt(3)
	v_mfma_f32_32x32x16_bf16 v[0:15], v[32:35], v[28:31], v[0:15]
	s_waitcnt vmcnt(2)
	v_mfma_f32_32x32x16_bf16 v[0:15], v[36:39], v[24:27], v[0:15]
	s_waitcnt vmcnt(1)
	v_mfma_f32_32x32x16_bf16 v[0:15], v[40:43], v[20:23], v[0:15]
	s_waitcnt vmcnt(0)
	v_mfma_f32_32x32x16_bf16 v[0:15], v[44:47], v[16:19], v[0:15]
	s_nop 15
	s_nop 15
	s_nop 11
	v_cmp_gt_i32_e64 s[6:7], 0, v1
	v_and_b32_e32 v1, 0xffffff80, v1
	v_and_b32_e32 v18, 0xffffff80, v0
	v_cndmask_b32_e64 v16, v135, v133, s[6:7]
	v_cmp_gt_i32_e64 s[6:7], 0, v0
	v_or_b32_e32 v0, v16, v1
	s_nop 0
	v_cndmask_b32_e64 v17, v138, v136, s[6:7]
	v_cmp_gt_i32_e64 s[6:7], 0, v3
	v_or_b32_e32 v1, v17, v18
	v_and_b32_e32 v3, 0xffffff80, v3
	v_cndmask_b32_e64 v16, v139, v137, s[6:7]
	v_cmp_gt_i32_e64 s[6:7], 0, v2
	v_and_b32_e32 v18, 0xffffff80, v2
	v_or_b32_e32 v2, v16, v3
	v_cndmask_b32_e64 v17, v142, v140, s[6:7]
	v_cmp_gt_i32_e64 s[6:7], 0, v5
	v_or_b32_e32 v3, v17, v18
	v_and_b32_e32 v5, 0xffffff80, v5
	v_cndmask_b32_e64 v16, v143, v141, s[6:7]
	v_cmp_gt_i32_e64 s[6:7], 0, v4
	v_and_b32_e32 v18, 0xffffff80, v4
	v_or_b32_e32 v4, v16, v5
	v_cndmask_b32_e64 v17, v154, v152, s[6:7]
	v_cmp_gt_i32_e64 s[6:7], 0, v7
	v_or_b32_e32 v5, v17, v18
	v_and_b32_e32 v7, 0xffffff80, v7
	v_cndmask_b32_e64 v16, v155, v153, s[6:7]
	v_cmp_gt_i32_e64 s[6:7], 0, v6
	v_and_b32_e32 v18, 0xffffff80, v6
	v_or_b32_e32 v6, v16, v7
	v_cndmask_b32_e64 v17, v158, v156, s[6:7]
	v_cmp_gt_i32_e64 s[6:7], 0, v9
	v_or_b32_e32 v7, v17, v18
	v_and_b32_e32 v9, 0xffffff80, v9
	v_cndmask_b32_e64 v16, v159, v157, s[6:7]
	v_cmp_gt_i32_e64 s[6:7], 0, v8
	v_and_b32_e32 v18, 0xffffff80, v8
	v_or_b32_e32 v8, v16, v9
	v_cndmask_b32_e64 v17, v162, v160, s[6:7]
	v_cmp_gt_i32_e64 s[6:7], 0, v11
	v_or_b32_e32 v9, v17, v18
	v_and_b32_e32 v11, 0xffffff80, v11
	v_cndmask_b32_e64 v16, v163, v161, s[6:7]
	v_cmp_gt_i32_e64 s[6:7], 0, v10
	v_and_b32_e32 v18, 0xffffff80, v10
	v_or_b32_e32 v10, v16, v11
	v_cndmask_b32_e64 v17, v166, v164, s[6:7]
	v_cmp_gt_i32_e64 s[6:7], 0, v13
	v_or_b32_e32 v11, v17, v18
	v_and_b32_e32 v13, 0xffffff80, v13
	v_cndmask_b32_e64 v16, v167, v165, s[6:7]
	v_cmp_gt_i32_e64 s[6:7], 0, v12
	v_and_b32_e32 v18, 0xffffff80, v12
	v_or_b32_e32 v12, v16, v13
	v_cndmask_b32_e64 v17, v170, v168, s[6:7]
	v_cmp_gt_i32_e64 s[6:7], 0, v15
	v_or_b32_e32 v16, v17, v18
	v_and_b32_e32 v15, 0xffffff80, v15
	v_cndmask_b32_e64 v13, v171, v169, s[6:7]
	v_cmp_gt_i32_e64 s[6:7], 0, v14
	v_and_b32_e32 v14, 0xffffff80, v14
	v_or_b32_e32 v25, v13, v15
	v_cndmask_b32_e64 v17, v174, v172, s[6:7]
	v_or_b32_e32 v28, v17, v14
	v_max_f32_e32 v13, v211, v210
	v_min_f32_e32 v14, v211, v210
	v_min_f32_e32 v15, v212, v173
	v_max_f32_e32 v17, v212, v173
	v_max_f32_e32 v18, v214, v213
	v_min_f32_e32 v19, v214, v213
	v_min_f32_e32 v20, v216, v215
	v_max_f32_e32 v21, v216, v215
	v_max_f32_e32 v22, v218, v217
	v_min_f32_e32 v23, v218, v217
	v_min_f32_e32 v24, v220, v219
	v_max_f32_e32 v26, v220, v219
	v_max_f32_e32 v27, v222, v221
	v_min_f32_e32 v29, v222, v221
	v_min_f32_e32 v30, v224, v223
	v_max_f32_e32 v31, v224, v223
	v_max_f32_e32 v32, v13, v15
	v_min_f32_e32 v13, v13, v15
	v_max_f32_e32 v15, v14, v17
	v_min_f32_e32 v14, v14, v17
	v_min_f32_e32 v17, v18, v20
	v_max_f32_e32 v18, v18, v20
	v_min_f32_e32 v20, v19, v21
	v_max_f32_e32 v19, v19, v21
	v_max_f32_e32 v21, v22, v24
	v_min_f32_e32 v22, v22, v24
	v_max_f32_e32 v24, v23, v26
	v_min_f32_e32 v23, v23, v26
	v_min_f32_e32 v26, v27, v30
	v_max_f32_e32 v27, v27, v30
	v_min_f32_e32 v30, v29, v31
	v_max_f32_e32 v29, v29, v31
	v_max_f32_e32 v31, v32, v15
	v_min_f32_e32 v15, v32, v15
	v_max_f32_e32 v32, v13, v14
	v_min_f32_e32 v13, v13, v14
	v_min_f32_e32 v14, v17, v20
	v_max_f32_e32 v17, v17, v20
	v_min_f32_e32 v20, v18, v19
	v_max_f32_e32 v18, v18, v19
	v_max_f32_e32 v19, v21, v24
	v_min_f32_e32 v21, v21, v24
	v_max_f32_e32 v24, v22, v23
	v_min_f32_e32 v22, v22, v23
	v_min_f32_e32 v23, v26, v30
	v_max_f32_e32 v26, v26, v30
	v_min_f32_e32 v30, v27, v29
	v_max_f32_e32 v27, v27, v29
	v_max_f32_e32 v29, v31, v14
	v_min_f32_e32 v14, v31, v14
	v_max_f32_e32 v31, v15, v17
	v_min_f32_e32 v15, v15, v17
	v_max_f32_e32 v17, v32, v20
	v_min_f32_e32 v20, v32, v20
	v_max_f32_e32 v32, v13, v18
	v_min_f32_e32 v13, v13, v18
	v_min_f32_e32 v18, v19, v23
	v_max_f32_e32 v19, v19, v23
	v_min_f32_e32 v23, v21, v26
	v_max_f32_e32 v21, v21, v26
	v_min_f32_e32 v26, v24, v30
	v_max_f32_e32 v24, v24, v30
	v_min_f32_e32 v30, v22, v27
	v_max_f32_e32 v22, v22, v27
	v_max_f32_e32 v27, v29, v17
	v_min_f32_e32 v17, v29, v17
	v_max_f32_e32 v29, v31, v32
	v_min_f32_e32 v31, v31, v32
	v_max_f32_e32 v32, v14, v20
	v_min_f32_e32 v14, v14, v20
	v_max_f32_e32 v20, v15, v13
	v_min_f32_e32 v13, v15, v13
	v_min_f32_e32 v15, v18, v26
	v_max_f32_e32 v18, v18, v26
	v_min_f32_e32 v26, v23, v30
	v_max_f32_e32 v23, v23, v30
	v_min_f32_e32 v30, v19, v24
	v_max_f32_e32 v19, v19, v24
	v_min_f32_e32 v24, v21, v22
	v_max_f32_e32 v21, v21, v22
	v_max_f32_e32 v22, v27, v29
	v_min_f32_e32 v27, v27, v29
	v_max_f32_e32 v29, v17, v31
	v_min_f32_e32 v17, v17, v31
	v_max_f32_e32 v31, v32, v20
	v_min_f32_e32 v20, v32, v20
	v_max_f32_e32 v32, v14, v13
	v_min_f32_e32 v13, v14, v13
	v_min_f32_e32 v14, v15, v26
	v_max_f32_e32 v15, v15, v26
	v_min_f32_e32 v26, v18, v23
	v_max_f32_e32 v18, v18, v23
	v_min_f32_e32 v23, v30, v24
	v_max_f32_e32 v24, v30, v24
	v_min_f32_e32 v30, v19, v21
	v_max_f32_e32 v19, v19, v21
	v_max_f32_e32 v21, v22, v14
	v_min_f32_e32 v14, v22, v14
	v_max_f32_e32 v22, v27, v15
	v_min_f32_e32 v15, v27, v15
	v_max_f32_e32 v27, v29, v26
	v_min_f32_e32 v26, v29, v26
	v_max_f32_e32 v29, v17, v18
	v_min_f32_e32 v17, v17, v18
	v_max_f32_e32 v18, v31, v23
	v_min_f32_e32 v23, v31, v23
	v_max_f32_e32 v31, v20, v24
	v_min_f32_e32 v20, v20, v24
	v_max_f32_e32 v24, v32, v30
	v_min_f32_e32 v30, v32, v30
	v_max_f32_e32 v32, v13, v19
	v_min_f32_e32 v13, v13, v19
	v_max_f32_e32 v19, v21, v18
	v_min_f32_e32 v18, v21, v18
	v_max_f32_e32 v21, v22, v31
	v_min_f32_e32 v22, v22, v31
	v_max_f32_e32 v31, v27, v24
	v_min_f32_e32 v24, v27, v24
	v_max_f32_e32 v27, v29, v32
	v_min_f32_e32 v29, v29, v32
	v_max_f32_e32 v32, v14, v23
	v_min_f32_e32 v14, v14, v23
	v_max_f32_e32 v23, v15, v20
	v_min_f32_e32 v15, v15, v20
	v_max_f32_e32 v20, v26, v30
	v_min_f32_e32 v26, v26, v30
	v_max_f32_e32 v30, v17, v13
	v_min_f32_e32 v13, v17, v13
	v_max_f32_e32 v17, v19, v31
	v_min_f32_e32 v19, v19, v31
	v_max_f32_e32 v33, v21, v27
	v_min_f32_e32 v21, v21, v27
	v_max_f32_e32 v34, v18, v24
	v_min_f32_e32 v18, v18, v24
	v_max_f32_e32 v24, v22, v29
	v_min_f32_e32 v22, v22, v29
	v_max_f32_e32 v35, v32, v20
	v_min_f32_e32 v32, v32, v20
	v_max_f32_e32 v20, v23, v30
	v_min_f32_e32 v36, v23, v30
	v_max_f32_e32 v37, v14, v26
	v_min_f32_e32 v38, v14, v26
	v_max_f32_e32 v14, v15, v13
	v_min_f32_e32 v13, v15, v13
	v_max_f32_e32 v31, v17, v33
	v_min_f32_e32 v29, v17, v33
	v_max_f32_e32 v30, v19, v21
	v_min_f32_e32 v26, v19, v21
	v_max_f32_e32 v27, v34, v24
	v_min_f32_e32 v23, v34, v24
	v_max_f32_e32 v24, v18, v22
	v_min_f32_e32 v21, v18, v22
	v_max_f32_e32 v22, v35, v20
	v_min_f32_e32 v19, v35, v20
	v_max_f32_e32 v20, v32, v36
	v_min_f32_e32 v17, v32, v36
	v_max_f32_e32 v18, v37, v14
	v_min_f32_e32 v14, v37, v14
	v_max_f32_e32 v15, v38, v13
	v_min_f32_e32 v13, v38, v13
	v_max_f32_e32 v32, v226, v225
	v_min_f32_e32 v33, v226, v225
	v_min_f32_e32 v34, v228, v227
	v_max_f32_e32 v35, v228, v227
	v_max_f32_e32 v36, v230, v229
	v_min_f32_e32 v37, v230, v229
	v_min_f32_e32 v38, v232, v231
	v_max_f32_e32 v39, v232, v231
	v_max_f32_e32 v40, v234, v233
	v_min_f32_e32 v41, v234, v233
	v_min_f32_e32 v42, v236, v235
	v_max_f32_e32 v43, v236, v235
	v_max_f32_e32 v44, v238, v237
	v_min_f32_e32 v45, v238, v237
	v_min_f32_e32 v46, v240, v239
	v_max_f32_e32 v47, v240, v239
	v_max_f32_e32 v48, v32, v34
	v_min_f32_e32 v32, v32, v34
	v_max_f32_e32 v34, v33, v35
	v_min_f32_e32 v33, v33, v35
	v_min_f32_e32 v35, v36, v38
	v_max_f32_e32 v36, v36, v38
	v_min_f32_e32 v38, v37, v39
	v_max_f32_e32 v37, v37, v39
	v_max_f32_e32 v39, v40, v42
	v_min_f32_e32 v40, v40, v42
	v_max_f32_e32 v42, v41, v43
	v_min_f32_e32 v41, v41, v43
	v_min_f32_e32 v43, v44, v46
	v_max_f32_e32 v44, v44, v46
	v_min_f32_e32 v46, v45, v47
	v_max_f32_e32 v45, v45, v47
	v_max_f32_e32 v47, v48, v34
	v_min_f32_e32 v34, v48, v34
	v_max_f32_e32 v48, v32, v33
	v_min_f32_e32 v32, v32, v33
	v_min_f32_e32 v33, v35, v38
	v_max_f32_e32 v35, v35, v38
	v_min_f32_e32 v38, v36, v37
	v_max_f32_e32 v36, v36, v37
	v_max_f32_e32 v37, v39, v42
	v_min_f32_e32 v39, v39, v42
	v_max_f32_e32 v42, v40, v41
	v_min_f32_e32 v40, v40, v41
	v_min_f32_e32 v41, v43, v46
	v_max_f32_e32 v43, v43, v46
	v_min_f32_e32 v46, v44, v45
	v_max_f32_e32 v44, v44, v45
	v_max_f32_e32 v45, v47, v33
	v_min_f32_e32 v33, v47, v33
	v_max_f32_e32 v47, v34, v35
	v_min_f32_e32 v34, v34, v35
	v_max_f32_e32 v35, v48, v38
	v_min_f32_e32 v38, v48, v38
	v_max_f32_e32 v48, v32, v36
	v_min_f32_e32 v32, v32, v36
	v_min_f32_e32 v36, v37, v41
	v_max_f32_e32 v37, v37, v41
	v_min_f32_e32 v41, v39, v43
	v_max_f32_e32 v39, v39, v43
	v_min_f32_e32 v43, v42, v46
	v_max_f32_e32 v42, v42, v46
	v_min_f32_e32 v46, v40, v44
	v_max_f32_e32 v40, v40, v44
	v_max_f32_e32 v44, v45, v35
	v_min_f32_e32 v35, v45, v35
	v_max_f32_e32 v45, v47, v48
	v_min_f32_e32 v47, v47, v48
	v_max_f32_e32 v48, v33, v38
	v_min_f32_e32 v33, v33, v38
	v_max_f32_e32 v38, v34, v32
	v_min_f32_e32 v32, v34, v32
	v_min_f32_e32 v34, v36, v43
	v_max_f32_e32 v36, v36, v43
	v_min_f32_e32 v43, v41, v46
	v_max_f32_e32 v41, v41, v46
	v_min_f32_e32 v46, v37, v42
	v_max_f32_e32 v37, v37, v42
	v_min_f32_e32 v42, v39, v40
	v_max_f32_e32 v39, v39, v40
	v_max_f32_e32 v40, v44, v45
	v_min_f32_e32 v44, v44, v45
	v_max_f32_e32 v45, v35, v47
	v_min_f32_e32 v35, v35, v47
	v_max_f32_e32 v47, v48, v38
	v_min_f32_e32 v38, v48, v38
	v_max_f32_e32 v48, v33, v32
	v_min_f32_e32 v32, v33, v32
	v_min_f32_e32 v33, v34, v43
	v_max_f32_e32 v34, v34, v43
	v_min_f32_e32 v43, v36, v41
	v_max_f32_e32 v36, v36, v41
	v_min_f32_e32 v41, v46, v42
	v_max_f32_e32 v42, v46, v42
	v_min_f32_e32 v46, v37, v39
	v_max_f32_e32 v37, v37, v39
	v_max_f32_e32 v39, v40, v33
	v_min_f32_e32 v33, v40, v33
	v_max_f32_e32 v40, v44, v34
	v_min_f32_e32 v34, v44, v34
	v_max_f32_e32 v44, v45, v43
	v_min_f32_e32 v43, v45, v43
	v_max_f32_e32 v45, v35, v36
	v_min_f32_e32 v35, v35, v36
	v_max_f32_e32 v36, v47, v41
	v_min_f32_e32 v41, v47, v41
	v_max_f32_e32 v47, v38, v42
	v_min_f32_e32 v38, v38, v42
	v_max_f32_e32 v42, v48, v46
	v_min_f32_e32 v46, v48, v46
	v_max_f32_e32 v48, v32, v37
	v_min_f32_e32 v32, v32, v37
	v_max_f32_e32 v37, v39, v36
	v_min_f32_e32 v36, v39, v36
	v_max_f32_e32 v39, v40, v47
	v_min_f32_e32 v40, v40, v47
	v_max_f32_e32 v47, v44, v42
	v_min_f32_e32 v42, v44, v42
	v_max_f32_e32 v44, v45, v48
	v_min_f32_e32 v45, v45, v48
	v_max_f32_e32 v48, v33, v41
	v_min_f32_e32 v33, v33, v41
	v_max_f32_e32 v41, v34, v38
	v_min_f32_e32 v34, v34, v38
	v_max_f32_e32 v38, v43, v46
	v_min_f32_e32 v43, v43, v46
	v_max_f32_e32 v46, v35, v32
	v_min_f32_e32 v32, v35, v32
	v_max_f32_e32 v35, v37, v47
	v_min_f32_e32 v37, v37, v47
	v_max_f32_e32 v47, v39, v44
	v_min_f32_e32 v39, v39, v44
	v_max_f32_e32 v44, v36, v42
	v_min_f32_e32 v42, v36, v42
	v_max_f32_e32 v49, v40, v45
	v_min_f32_e32 v40, v40, v45
	v_max_f32_e32 v45, v48, v38
	v_min_f32_e32 v48, v48, v38
	v_max_f32_e32 v50, v41, v46
	v_min_f32_e32 v41, v41, v46
	v_max_f32_e32 v46, v33, v43
	v_min_f32_e32 v43, v33, v43
	v_max_f32_e32 v51, v34, v32
	v_min_f32_e32 v52, v34, v32
	v_max_f32_e32 v32, v35, v47
	v_min_f32_e32 v33, v35, v47
	v_max_f32_e32 v34, v37, v39
	v_min_f32_e32 v35, v37, v39
	v_max_f32_e32 v36, v44, v49
	v_min_f32_e32 v37, v44, v49
	v_max_f32_e32 v38, v42, v40
	v_min_f32_e32 v39, v42, v40
	v_max_f32_e32 v40, v45, v50
	v_min_f32_e32 v42, v45, v50
	v_max_f32_e32 v44, v48, v41
	v_min_f32_e32 v41, v48, v41
	v_max_f32_e32 v45, v46, v51
	v_min_f32_e32 v46, v46, v51
	v_max_f32_e32 v47, v43, v52
	v_min_f32_e32 v43, v43, v52
	v_max_f32_e32 v48, v183, v182
	v_min_f32_e32 v49, v183, v182
	v_min_f32_e32 v50, v242, v241
	v_max_f32_e32 v51, v242, v241
	v_max_f32_e32 v52, v244, v243
	v_min_f32_e32 v53, v244, v243
	v_min_f32_e32 v54, v246, v245
	v_max_f32_e32 v55, v246, v245
	v_max_f32_e32 v56, v248, v247
	v_min_f32_e32 v57, v248, v247
	v_min_f32_e32 v58, v250, v249
	v_max_f32_e32 v59, v250, v249
	v_max_f32_e32 v60, v252, v251
	v_min_f32_e32 v61, v252, v251
	v_min_f32_e32 v62, v195, v190
	v_max_f32_e32 v63, v195, v190
	v_max_f32_e32 v173, v48, v50
	v_min_f32_e32 v48, v48, v50
	v_max_f32_e32 v50, v49, v51
	v_min_f32_e32 v49, v49, v51
	v_min_f32_e32 v51, v52, v54
	v_max_f32_e32 v52, v52, v54
	v_min_f32_e32 v54, v53, v55
	v_max_f32_e32 v53, v53, v55
	v_max_f32_e32 v55, v56, v58
	v_min_f32_e32 v56, v56, v58
	v_max_f32_e32 v58, v57, v59
	v_min_f32_e32 v57, v57, v59
	v_min_f32_e32 v59, v60, v62
	v_max_f32_e32 v60, v60, v62
	v_min_f32_e32 v62, v61, v63
	v_max_f32_e32 v61, v61, v63
	v_max_f32_e32 v63, v173, v50
	v_min_f32_e32 v50, v173, v50
	v_max_f32_e32 v173, v48, v49
	v_min_f32_e32 v48, v48, v49
	v_min_f32_e32 v49, v51, v54
	v_max_f32_e32 v51, v51, v54
	v_min_f32_e32 v54, v52, v53
	v_max_f32_e32 v52, v52, v53
	v_max_f32_e32 v53, v55, v58
	v_min_f32_e32 v55, v55, v58
	v_max_f32_e32 v58, v56, v57
	v_min_f32_e32 v56, v56, v57
	v_min_f32_e32 v57, v59, v62
	v_max_f32_e32 v59, v59, v62
	v_min_f32_e32 v62, v60, v61
	v_max_f32_e32 v60, v60, v61
	v_max_f32_e32 v61, v63, v49
	v_min_f32_e32 v49, v63, v49
	v_max_f32_e32 v63, v50, v51
	v_min_f32_e32 v50, v50, v51
	v_max_f32_e32 v51, v173, v54
	v_min_f32_e32 v54, v173, v54
	v_max_f32_e32 v173, v48, v52
	v_min_f32_e32 v48, v48, v52
	v_min_f32_e32 v52, v53, v57
	v_max_f32_e32 v53, v53, v57
	v_min_f32_e32 v57, v55, v59
	v_max_f32_e32 v55, v55, v59
	v_min_f32_e32 v59, v58, v62
	v_max_f32_e32 v58, v58, v62
	v_min_f32_e32 v62, v56, v60
	v_max_f32_e32 v56, v56, v60
	v_max_f32_e32 v60, v61, v51
	v_min_f32_e32 v51, v61, v51
	v_max_f32_e32 v61, v63, v173
	v_min_f32_e32 v63, v63, v173
	v_max_f32_e32 v173, v49, v54
	v_min_f32_e32 v49, v49, v54
	v_max_f32_e32 v54, v50, v48
	v_min_f32_e32 v48, v50, v48
	v_min_f32_e32 v50, v52, v59
	v_max_f32_e32 v52, v52, v59
	v_min_f32_e32 v59, v57, v62
	v_max_f32_e32 v57, v57, v62
	v_min_f32_e32 v62, v53, v58
	v_max_f32_e32 v53, v53, v58
	v_min_f32_e32 v58, v55, v56
	v_max_f32_e32 v55, v55, v56
	v_max_f32_e32 v56, v60, v61
	v_min_f32_e32 v60, v60, v61
	v_max_f32_e32 v61, v51, v63
	v_min_f32_e32 v51, v51, v63
	v_max_f32_e32 v63, v173, v54
	v_min_f32_e32 v54, v173, v54
	v_max_f32_e32 v173, v49, v48
	v_min_f32_e32 v48, v49, v48
	v_min_f32_e32 v49, v50, v59
	v_max_f32_e32 v50, v50, v59
	v_min_f32_e32 v59, v52, v57
	v_max_f32_e32 v52, v52, v57
	v_min_f32_e32 v57, v62, v58
	v_max_f32_e32 v58, v62, v58
	v_min_f32_e32 v62, v53, v55
	v_max_f32_e32 v53, v53, v55
	v_max_f32_e32 v55, v56, v49
	v_min_f32_e32 v49, v56, v49
	v_max_f32_e32 v56, v60, v50
	v_min_f32_e32 v50, v60, v50
	v_max_f32_e32 v60, v61, v59
	v_min_f32_e32 v59, v61, v59
	v_max_f32_e32 v61, v51, v52
	v_min_f32_e32 v51, v51, v52
	v_max_f32_e32 v52, v63, v57
	v_min_f32_e32 v57, v63, v57
	v_max_f32_e32 v63, v54, v58
	v_min_f32_e32 v54, v54, v58
	v_max_f32_e32 v58, v173, v62
	v_min_f32_e32 v62, v173, v62
	v_max_f32_e32 v173, v48, v53
	v_min_f32_e32 v48, v48, v53
	v_max_f32_e32 v53, v55, v52
	v_min_f32_e32 v52, v55, v52
	v_max_f32_e32 v55, v56, v63
	v_min_f32_e32 v56, v56, v63
	v_max_f32_e32 v63, v60, v58
	v_min_f32_e32 v58, v60, v58
	v_max_f32_e32 v60, v61, v173
	v_min_f32_e32 v61, v61, v173
	v_max_f32_e32 v173, v49, v57
	v_min_f32_e32 v49, v49, v57
	v_max_f32_e32 v57, v50, v54
	v_min_f32_e32 v50, v50, v54
	v_max_f32_e32 v54, v59, v62
	v_min_f32_e32 v59, v59, v62
	v_max_f32_e32 v62, v51, v48
	v_min_f32_e32 v48, v51, v48
	v_max_f32_e32 v51, v53, v63
	v_min_f32_e32 v53, v53, v63
	v_max_f32_e32 v63, v55, v60
	v_min_f32_e32 v55, v55, v60
	v_max_f32_e32 v60, v52, v58
	v_min_f32_e32 v52, v52, v58
	v_max_f32_e32 v58, v56, v61
	v_min_f32_e32 v56, v56, v61
	v_max_f32_e32 v61, v173, v54
	v_min_f32_e32 v54, v173, v54
	v_max_f32_e32 v173, v57, v62
	v_min_f32_e32 v57, v57, v62
	v_max_f32_e32 v62, v49, v59
	v_min_f32_e32 v49, v49, v59
	v_max_f32_e32 v59, v50, v48
	v_min_f32_e32 v48, v50, v48
	v_max_f32_e32 v50, v51, v63
	v_min_f32_e32 v51, v51, v63
	v_max_f32_e32 v63, v53, v55
	v_min_f32_e32 v53, v53, v55
	v_max_f32_e32 v55, v60, v58
	v_min_f32_e32 v58, v60, v58
	v_max_f32_e32 v60, v52, v56
	v_min_f32_e32 v52, v52, v56
	v_max_f32_e32 v56, v61, v173
	v_min_f32_e32 v61, v61, v173
	v_max_f32_e32 v173, v54, v57
	v_min_f32_e32 v54, v54, v57
	v_max_f32_e32 v57, v62, v59
	v_min_f32_e32 v59, v62, v59
	v_max_f32_e32 v62, v49, v48
	v_min_f32_e32 v48, v49, v48
	v_max_f32_e32 v49, v1, v0
	v_min_f32_e32 v0, v1, v0
	v_min_f32_e32 v1, v3, v2
	v_max_f32_e32 v2, v3, v2
	v_max_f32_e32 v3, v5, v4
	v_min_f32_e32 v4, v5, v4
	v_min_f32_e32 v5, v7, v6
	v_max_f32_e32 v6, v7, v6
	v_max_f32_e32 v7, v9, v8
	v_min_f32_e32 v8, v9, v8
	v_min_f32_e32 v9, v11, v10
	v_max_f32_e32 v10, v11, v10
	v_max_f32_e32 v11, v16, v12
	v_min_f32_e32 v12, v16, v12
	v_min_f32_e32 v16, v28, v25
	v_max_f32_e32 v25, v28, v25
	v_max_f32_e32 v28, v49, v1
	v_min_f32_e32 v1, v49, v1
	v_max_f32_e32 v49, v0, v2
	v_min_f32_e32 v0, v0, v2
	v_min_f32_e32 v2, v3, v5
	v_max_f32_e32 v3, v3, v5
	v_min_f32_e32 v5, v4, v6
	v_max_f32_e32 v4, v4, v6
	v_max_f32_e32 v6, v7, v9
	v_min_f32_e32 v7, v7, v9
	v_max_f32_e32 v9, v8, v10
	v_min_f32_e32 v8, v8, v10
	v_min_f32_e32 v10, v11, v16
	v_max_f32_e32 v11, v11, v16
	v_min_f32_e32 v16, v12, v25
	v_max_f32_e32 v12, v12, v25
	v_max_f32_e32 v25, v28, v49
	v_min_f32_e32 v28, v28, v49
	v_max_f32_e32 v49, v1, v0
	v_min_f32_e32 v0, v1, v0
	v_min_f32_e32 v1, v2, v5
	v_max_f32_e32 v2, v2, v5
	v_min_f32_e32 v5, v3, v4
	v_max_f32_e32 v3, v3, v4
	v_max_f32_e32 v4, v6, v9
	v_min_f32_e32 v6, v6, v9
	v_max_f32_e32 v9, v7, v8
	v_min_f32_e32 v7, v7, v8
	v_min_f32_e32 v8, v10, v16
	v_max_f32_e32 v10, v10, v16
	v_min_f32_e32 v16, v11, v12
	v_max_f32_e32 v11, v11, v12
	v_max_f32_e32 v12, v25, v1
	v_min_f32_e32 v1, v25, v1
	v_max_f32_e32 v25, v28, v2
	v_min_f32_e32 v2, v28, v2
	v_max_f32_e32 v28, v49, v5
	v_min_f32_e32 v5, v49, v5
	v_max_f32_e32 v49, v0, v3
	v_min_f32_e32 v0, v0, v3
	v_min_f32_e32 v3, v4, v8
	v_max_f32_e32 v4, v4, v8
	v_min_f32_e32 v8, v6, v10
	v_max_f32_e32 v6, v6, v10
	v_min_f32_e32 v10, v9, v16
	v_max_f32_e32 v9, v9, v16
	v_min_f32_e32 v16, v7, v11
	v_max_f32_e32 v7, v7, v11
	v_max_f32_e32 v11, v12, v28
	v_min_f32_e32 v12, v12, v28
	v_max_f32_e32 v28, v25, v49
	v_min_f32_e32 v25, v25, v49
	v_max_f32_e32 v49, v1, v5
	v_min_f32_e32 v1, v1, v5
	v_max_f32_e32 v5, v2, v0
	v_min_f32_e32 v0, v2, v0
	v_min_f32_e32 v2, v3, v10
	v_max_f32_e32 v3, v3, v10
	v_min_f32_e32 v10, v8, v16
	v_max_f32_e32 v8, v8, v16
	v_min_f32_e32 v16, v4, v9
	v_max_f32_e32 v4, v4, v9
	v_min_f32_e32 v9, v6, v7
	v_max_f32_e32 v6, v6, v7
	v_max_f32_e32 v7, v11, v28
	v_min_f32_e32 v11, v11, v28
	v_max_f32_e32 v28, v12, v25
	v_min_f32_e32 v12, v12, v25
	v_max_f32_e32 v25, v49, v5
	v_min_f32_e32 v5, v49, v5
	v_max_f32_e32 v49, v1, v0
	v_min_f32_e32 v0, v1, v0
	v_min_f32_e32 v1, v2, v10
	v_max_f32_e32 v2, v2, v10
	v_min_f32_e32 v10, v3, v8
	v_max_f32_e32 v3, v3, v8
	v_min_f32_e32 v8, v16, v9
	v_max_f32_e32 v9, v16, v9
	v_min_f32_e32 v16, v4, v6
	v_max_f32_e32 v4, v4, v6
	v_max_f32_e32 v6, v7, v1
	v_min_f32_e32 v1, v7, v1
	v_max_f32_e32 v7, v11, v2
	v_min_f32_e32 v2, v11, v2
	v_max_f32_e32 v11, v28, v10
	v_min_f32_e32 v10, v28, v10
	v_max_f32_e32 v28, v12, v3
	v_min_f32_e32 v3, v12, v3
	v_max_f32_e32 v12, v25, v8
	v_min_f32_e32 v8, v25, v8
	v_max_f32_e32 v25, v5, v9
	v_min_f32_e32 v5, v5, v9
	v_max_f32_e32 v9, v49, v16
	v_min_f32_e32 v16, v49, v16
	v_max_f32_e32 v49, v0, v4
	v_min_f32_e32 v0, v0, v4
	v_max_f32_e32 v4, v6, v12
	v_min_f32_e32 v6, v6, v12
	v_max_f32_e32 v12, v7, v25
	v_min_f32_e32 v7, v7, v25
	v_max_f32_e32 v25, v11, v9
	v_min_f32_e32 v9, v11, v9
	v_max_f32_e32 v11, v28, v49
	v_min_f32_e32 v28, v28, v49
	v_max_f32_e32 v49, v1, v8
	v_min_f32_e32 v1, v1, v8
	v_max_f32_e32 v8, v2, v5
	v_min_f32_e32 v2, v2, v5
	v_max_f32_e32 v5, v10, v16
	v_min_f32_e32 v10, v10, v16
	v_max_f32_e32 v16, v3, v0
	v_min_f32_e32 v0, v3, v0
	v_max_f32_e32 v3, v4, v25
	v_min_f32_e32 v4, v4, v25
	v_max_f32_e32 v25, v12, v11
	v_min_f32_e32 v11, v12, v11
	v_max_f32_e32 v12, v6, v9
	v_min_f32_e32 v6, v6, v9
	v_max_f32_e32 v9, v7, v28
	v_min_f32_e32 v7, v7, v28
	v_max_f32_e32 v28, v49, v5
	v_min_f32_e32 v5, v49, v5
	v_max_f32_e32 v49, v8, v16
	v_min_f32_e32 v8, v8, v16
	v_max_f32_e32 v16, v1, v10
	v_min_f32_e32 v1, v1, v10
	v_max_f32_e32 v10, v2, v0
	v_min_f32_e32 v0, v2, v0
	v_max_f32_e32 v2, v3, v25
	v_min_f32_e32 v3, v3, v25
	v_max_f32_e32 v25, v4, v11
	v_min_f32_e32 v4, v4, v11
	v_max_f32_e32 v11, v12, v9
	v_min_f32_e32 v9, v12, v9
	v_max_f32_e32 v12, v6, v7
	v_min_f32_e32 v6, v6, v7
	v_max_f32_e32 v7, v28, v49
	v_min_f32_e32 v28, v28, v49
	v_max_f32_e32 v49, v5, v8
	v_min_f32_e32 v5, v5, v8
	v_max_f32_e32 v8, v16, v10
	v_min_f32_e32 v10, v16, v10
	v_max_f32_e32 v16, v1, v0
	v_min_f32_e32 v0, v1, v0
	v_max_f32_e32 v1, v31, v43
	v_max_f32_e32 v29, v29, v47
	v_max_f32_e32 v30, v30, v46
	v_max_f32_e32 v26, v26, v45
	v_max_f32_e32 v27, v27, v41
	v_max_f32_e32 v23, v23, v44
	v_max_f32_e32 v24, v24, v42
	v_max_f32_e32 v21, v21, v40
	v_max_f32_e32 v22, v22, v39
	v_max_f32_e32 v19, v19, v38
	v_max_f32_e32 v20, v20, v37
	v_max_f32_e32 v17, v17, v36
	v_max_f32_e32 v18, v18, v35
	v_max_f32_e32 v14, v14, v34
	v_max_f32_e32 v15, v15, v33
	v_max_f32_e32 v13, v13, v32
	v_max_f32_e32 v31, v1, v22
	v_min_f32_e32 v1, v1, v22
	v_max_f32_e32 v22, v29, v19
	v_min_f32_e32 v19, v29, v19
	v_max_f32_e32 v29, v30, v20
	v_min_f32_e32 v20, v30, v20
	v_max_f32_e32 v30, v26, v17
	v_min_f32_e32 v17, v26, v17
	v_max_f32_e32 v26, v27, v18
	v_min_f32_e32 v18, v27, v18
	v_max_f32_e32 v27, v23, v14
	v_min_f32_e32 v14, v23, v14
	v_max_f32_e32 v23, v24, v15
	v_min_f32_e32 v15, v24, v15
	v_max_f32_e32 v24, v21, v13
	v_min_f32_e32 v13, v21, v13
	v_max_f32_e32 v21, v31, v26
	v_min_f32_e32 v26, v31, v26
	v_max_f32_e32 v31, v22, v27
	v_min_f32_e32 v22, v22, v27
	v_max_f32_e32 v27, v29, v23
	v_min_f32_e32 v23, v29, v23
	v_max_f32_e32 v29, v30, v24
	v_min_f32_e32 v24, v30, v24
	v_max_f32_e32 v30, v1, v18
	v_min_f32_e32 v1, v1, v18
	v_max_f32_e32 v18, v19, v14
	v_min_f32_e32 v14, v19, v14
	v_max_f32_e32 v19, v20, v15
	v_min_f32_e32 v15, v20, v15
	v_max_f32_e32 v20, v17, v13
	v_min_f32_e32 v13, v17, v13
	v_max_f32_e32 v17, v21, v27
	v_min_f32_e32 v21, v21, v27
	v_max_f32_e32 v27, v31, v29
	v_min_f32_e32 v29, v31, v29
	v_max_f32_e32 v31, v26, v23
	v_min_f32_e32 v23, v26, v23
	v_max_f32_e32 v26, v22, v24
	v_min_f32_e32 v22, v22, v24
	v_max_f32_e32 v24, v30, v19
	v_min_f32_e32 v19, v30, v19
	v_max_f32_e32 v30, v18, v20
	v_min_f32_e32 v18, v18, v20
	v_max_f32_e32 v20, v1, v15
	v_min_f32_e32 v1, v1, v15
	v_max_f32_e32 v15, v14, v13
	v_min_f32_e32 v13, v14, v13
	v_max_f32_e32 v14, v17, v27
	v_min_f32_e32 v17, v17, v27
	v_max_f32_e32 v27, v21, v29
	v_min_f32_e32 v21, v21, v29
	v_max_f32_e32 v29, v31, v26
	v_min_f32_e32 v26, v31, v26
	v_max_f32_e32 v31, v23, v22
	v_min_f32_e32 v22, v23, v22
	v_max_f32_e32 v23, v24, v30
	v_min_f32_e32 v24, v24, v30
	v_max_f32_e32 v30, v19, v18
	v_min_f32_e32 v18, v19, v18
	v_max_f32_e32 v19, v20, v15
	v_min_f32_e32 v15, v20, v15
	v_max_f32_e32 v20, v1, v13
	v_min_f32_e32 v1, v1, v13
	v_max_f32_e32 v0, v50, v0
	v_max_f32_e32 v13, v51, v16
	v_max_f32_e32 v10, v63, v10
	v_max_f32_e32 v8, v53, v8
	v_max_f32_e32 v5, v55, v5
	v_max_f32_e32 v16, v58, v49
	v_max_f32_e32 v28, v60, v28
	v_max_f32_e32 v7, v52, v7
	v_max_f32_e32 v6, v56, v6
	v_max_f32_e32 v12, v61, v12
	v_max_f32_e32 v9, v173, v9
	v_max_f32_e32 v11, v54, v11
	v_max_f32_e32 v4, v57, v4
	v_max_f32_e32 v25, v59, v25
	v_max_f32_e32 v3, v62, v3
	v_max_f32_e32 v2, v48, v2
	v_max_f32_e32 v32, v0, v6
	v_min_f32_e32 v0, v0, v6
	v_max_f32_e32 v6, v13, v12
	v_min_f32_e32 v12, v13, v12
	v_max_f32_e32 v13, v10, v9
	v_min_f32_e32 v9, v10, v9
	v_max_f32_e32 v10, v8, v11
	v_min_f32_e32 v8, v8, v11
	v_max_f32_e32 v11, v5, v4
	v_min_f32_e32 v4, v5, v4
	v_max_f32_e32 v5, v16, v25
	v_min_f32_e32 v16, v16, v25
	v_max_f32_e32 v25, v28, v3
	v_min_f32_e32 v3, v28, v3
	v_max_f32_e32 v28, v7, v2
	v_min_f32_e32 v2, v7, v2
	v_max_f32_e32 v7, v32, v11
	v_min_f32_e32 v11, v32, v11
	v_max_f32_e32 v32, v6, v5
	v_min_f32_e32 v5, v6, v5
	v_max_f32_e32 v6, v13, v25
	v_min_f32_e32 v13, v13, v25
	v_max_f32_e32 v25, v10, v28
	v_min_f32_e32 v10, v10, v28
	v_max_f32_e32 v28, v0, v4
	v_min_f32_e32 v0, v0, v4
	v_max_f32_e32 v4, v12, v16
	v_min_f32_e32 v12, v12, v16
	v_max_f32_e32 v16, v9, v3
	v_min_f32_e32 v3, v9, v3
	v_max_f32_e32 v9, v8, v2
	v_min_f32_e32 v2, v8, v2
	v_max_f32_e32 v8, v7, v6
	v_min_f32_e32 v6, v7, v6
	v_max_f32_e32 v7, v32, v25
	v_min_f32_e32 v25, v32, v25
	v_max_f32_e32 v32, v11, v13
	v_min_f32_e32 v11, v11, v13
	v_max_f32_e32 v13, v5, v10
	v_min_f32_e32 v5, v5, v10
	v_max_f32_e32 v10, v28, v16
	v_min_f32_e32 v16, v28, v16
	v_max_f32_e32 v28, v4, v9
	v_min_f32_e32 v4, v4, v9
	v_max_f32_e32 v9, v0, v3
	v_min_f32_e32 v0, v0, v3
	v_max_f32_e32 v3, v12, v2
	v_min_f32_e32 v2, v12, v2
	v_max_f32_e32 v12, v8, v7
	v_min_f32_e32 v7, v8, v7
	v_max_f32_e32 v8, v6, v25
	v_min_f32_e32 v6, v6, v25
	v_max_f32_e32 v25, v32, v13
	v_min_f32_e32 v13, v32, v13
	v_max_f32_e32 v32, v11, v5
	v_min_f32_e32 v5, v11, v5
	v_max_f32_e32 v11, v10, v28
	v_min_f32_e32 v10, v10, v28
	v_max_f32_e32 v28, v16, v4
	v_min_f32_e32 v4, v16, v4
	v_max_f32_e32 v16, v9, v3
	v_min_f32_e32 v3, v9, v3
	v_max_f32_e32 v9, v0, v2
	v_min_f32_e32 v0, v0, v2
	v_max_f32_e32 v0, v14, v0
	v_max_f32_e32 v2, v17, v9
	v_max_f32_e32 v3, v27, v3
	v_max_f32_e32 v9, v21, v16
	v_max_f32_e32 v4, v29, v4
	v_max_f32_e32 v14, v26, v28
	v_max_f32_e32 v10, v31, v10
	v_max_f32_e32 v11, v22, v11
	v_max_f32_e32 v5, v23, v5
	v_max_f32_e32 v16, v24, v32
	v_max_f32_e32 v13, v30, v13
	v_max_f32_e32 v17, v18, v25
	v_max_f32_e32 v6, v19, v6
	v_max_f32_e32 v8, v15, v8
	v_max_f32_e32 v7, v20, v7
	v_max_f32_e32 v1, v1, v12
	v_max_f32_e32 v12, v0, v5
	v_min_f32_e32 v0, v0, v5
	v_max_f32_e32 v5, v2, v16
	v_min_f32_e32 v2, v2, v16
	v_max_f32_e32 v15, v3, v13
	v_min_f32_e32 v3, v3, v13
	v_max_f32_e32 v13, v9, v17
	v_min_f32_e32 v9, v9, v17
	v_max_f32_e32 v16, v4, v6
	v_min_f32_e32 v4, v4, v6
	v_max_f32_e32 v6, v14, v8
	v_min_f32_e32 v8, v14, v8
	v_max_f32_e32 v14, v10, v7
	v_min_f32_e32 v7, v10, v7
	v_max_f32_e32 v10, v11, v1
	v_min_f32_e32 v1, v11, v1
	v_max_f32_e32 v11, v12, v16
	v_min_f32_e32 v12, v12, v16
	v_max_f32_e32 v16, v5, v6
	v_min_f32_e32 v5, v5, v6
	v_max_f32_e32 v6, v15, v14
	v_min_f32_e32 v14, v15, v14
	v_max_f32_e32 v15, v13, v10
	v_min_f32_e32 v10, v13, v10
	v_max_f32_e32 v13, v0, v4
	v_min_f32_e32 v0, v0, v4
	v_max_f32_e32 v4, v2, v8
	v_min_f32_e32 v2, v2, v8
	v_max_f32_e32 v8, v3, v7
	v_min_f32_e32 v3, v3, v7
	v_max_f32_e32 v7, v9, v1
	v_min_f32_e32 v1, v9, v1
	v_max_f32_e32 v9, v11, v6
	v_min_f32_e32 v6, v11, v6
	v_max_f32_e32 v11, v16, v15
	v_min_f32_e32 v15, v16, v15
	v_max_f32_e32 v16, v12, v14
	v_min_f32_e32 v12, v12, v14
	v_max_f32_e32 v14, v5, v10
	v_min_f32_e32 v5, v5, v10
	v_max_f32_e32 v10, v13, v8
	v_min_f32_e32 v8, v13, v8
	v_max_f32_e32 v13, v4, v7
	v_min_f32_e32 v4, v4, v7
	v_max_f32_e32 v7, v0, v3
	v_min_f32_e32 v0, v0, v3
	v_max_f32_e32 v3, v2, v1
	v_min_f32_e32 v1, v2, v1
	v_max_f32_e32 v2, v9, v11
	v_min_f32_e32 v9, v9, v11
	v_max_f32_e32 v11, v6, v15
	v_min_f32_e32 v6, v6, v15
	v_max_f32_e32 v15, v16, v14
	v_min_f32_e32 v14, v16, v14
	v_max_f32_e32 v16, v12, v5
	v_min_f32_e32 v5, v12, v5
	v_max_f32_e32 v12, v10, v13
	v_min_f32_e32 v10, v10, v13
	v_max_f32_e32 v13, v8, v4
	v_min_f32_e32 v4, v8, v4
	v_max_f32_e32 v8, v7, v3
	v_min_f32_e32 v3, v7, v3
	v_max_f32_e32 v7, v0, v1
	v_min_f32_e32 v0, v0, v1
	v_mov_b32_e32 v27, v0
	s_nop 1
	v_permlane32_swap_b32 v27, v27
	v_mov_b32_e32 v29, v7
	s_nop 1
	v_permlane32_swap_b32 v29, v29
	v_mov_b32_e32 v31, v3
	s_nop 1
	v_permlane32_swap_b32 v31, v31
	v_mov_b32_e32 v30, v8
	s_nop 1
	v_permlane32_swap_b32 v30, v30
	v_mov_b32_e32 v28, v4
	s_nop 1
	v_permlane32_swap_b32 v28, v28
	v_mov_b32_e32 v26, v13
	s_nop 1
	v_permlane32_swap_b32 v26, v26
	s_waitcnt lgkmcnt(5)
	v_mov_b32_e32 v1, v2
	s_nop 1
	v_permlane32_swap_b32 v1, v1
	v_mov_b32_e32 v25, v10
	s_nop 1
	v_permlane32_swap_b32 v25, v25
	v_max_f32_e32 v2, v2, v27
	s_waitcnt lgkmcnt(6)
	v_mov_b32_e32 v17, v9
	s_nop 1
	v_permlane32_swap_b32 v17, v17
	v_mov_b32_e32 v24, v12
	s_nop 1
	v_permlane32_swap_b32 v24, v24
	v_max_f32_e32 v9, v9, v29
	s_waitcnt lgkmcnt(7)
	v_mov_b32_e32 v18, v11
	s_nop 1
	v_permlane32_swap_b32 v18, v18
	v_mov_b32_e32 v23, v5
	s_nop 1
	v_permlane32_swap_b32 v23, v23
	v_max_f32_e32 v11, v11, v31
	s_waitcnt lgkmcnt(8)
	v_mov_b32_e32 v19, v6
	s_nop 1
	v_permlane32_swap_b32 v19, v19
	v_mov_b32_e32 v22, v16
	s_nop 1
	v_permlane32_swap_b32 v22, v22
	v_max_f32_e32 v6, v6, v30
	s_waitcnt lgkmcnt(9)
	v_mov_b32_e32 v20, v15
	s_nop 1
	v_permlane32_swap_b32 v20, v20
	v_mov_b32_e32 v21, v14
	s_nop 1
	v_permlane32_swap_b32 v21, v21
	v_max_f32_e32 v15, v15, v28
	s_waitcnt lgkmcnt(10)
	v_max_f32_e32 v14, v14, v26
	s_waitcnt lgkmcnt(8)
	v_max_f32_e32 v16, v16, v25
	s_waitcnt lgkmcnt(6)
	v_max_f32_e32 v5, v5, v24
	s_waitcnt lgkmcnt(4)
	v_max_f32_e32 v12, v12, v23
	s_waitcnt lgkmcnt(2)
	v_max_f32_e32 v10, v10, v22
	s_waitcnt lgkmcnt(0)
	v_max_f32_e32 v13, v13, v21
	v_max_f32_e32 v4, v4, v20
	v_max_f32_e32 v8, v8, v19
	v_max_f32_e32 v3, v3, v18
	v_max_f32_e32 v7, v7, v17
	v_max_f32_e32 v0, v0, v1
	v_max_f32_e32 v1, v2, v12
	v_min_f32_e32 v2, v2, v12
	v_max_f32_e32 v12, v9, v10
	v_min_f32_e32 v9, v9, v10
	v_max_f32_e32 v10, v11, v13
	v_min_f32_e32 v11, v11, v13
	v_max_f32_e32 v13, v6, v4
	v_min_f32_e32 v4, v6, v4
	v_max_f32_e32 v6, v15, v8
	v_min_f32_e32 v8, v15, v8
	v_max_f32_e32 v15, v14, v3
	v_min_f32_e32 v3, v14, v3
	v_max_f32_e32 v14, v16, v7
	v_min_f32_e32 v7, v16, v7
	v_max_f32_e32 v16, v5, v0
	v_min_f32_e32 v0, v5, v0
	v_max_f32_e32 v5, v1, v6
	v_min_f32_e32 v1, v1, v6
	v_max_f32_e32 v6, v12, v15
	v_min_f32_e32 v12, v12, v15
	v_max_f32_e32 v15, v10, v14
	v_min_f32_e32 v10, v10, v14
	v_max_f32_e32 v14, v13, v16
	v_min_f32_e32 v13, v13, v16
	v_max_f32_e32 v16, v2, v8
	v_min_f32_e32 v2, v2, v8
	v_max_f32_e32 v8, v9, v3
	v_min_f32_e32 v3, v9, v3
	v_max_f32_e32 v9, v11, v7
	v_min_f32_e32 v7, v11, v7
	v_max_f32_e32 v11, v4, v0
	v_min_f32_e32 v0, v4, v0
	v_max_f32_e32 v4, v5, v15
	v_min_f32_e32 v5, v5, v15
	v_max_f32_e32 v15, v6, v14
	v_min_f32_e32 v6, v6, v14
	v_max_f32_e32 v14, v1, v10
	v_min_f32_e32 v1, v1, v10
	v_max_f32_e32 v10, v12, v13
	v_min_f32_e32 v12, v12, v13
	v_max_f32_e32 v13, v16, v9
	v_min_f32_e32 v9, v16, v9
	v_max_f32_e32 v16, v8, v11
	v_min_f32_e32 v8, v8, v11
	v_max_f32_e32 v11, v2, v7
	v_min_f32_e32 v2, v2, v7
	v_max_f32_e32 v7, v3, v0
	v_min_f32_e32 v0, v3, v0
	v_max_f32_e32 v3, v4, v15
	v_min_f32_e32 v4, v4, v15
	v_max_f32_e32 v15, v5, v6
	v_min_f32_e32 v5, v5, v6
	v_max_f32_e32 v6, v14, v10
	v_min_f32_e32 v10, v14, v10
	v_max_f32_e32 v14, v1, v12
	v_min_f32_e32 v1, v1, v12
	v_max_f32_e32 v12, v13, v16
	v_min_f32_e32 v13, v13, v16
	v_max_f32_e32 v16, v9, v8
	v_min_f32_e32 v8, v9, v8
	v_max_f32_e32 v9, v11, v7
	v_min_f32_e32 v7, v11, v7
	v_max_f32_e32 v11, v2, v0
	v_min_f32_e32 v0, v2, v0
	v_lshl_add_u32 v2, s8, 12, v207
	ds_write2st64_b32 v2, v3, v4 offset1:1
	ds_write2st64_b32 v2, v15, v5 offset0:2 offset1:3
	ds_write2st64_b32 v2, v6, v10 offset0:4 offset1:5
	ds_write2st64_b32 v2, v14, v1 offset0:6 offset1:7
	ds_write2st64_b32 v2, v12, v13 offset0:8 offset1:9
	ds_write2st64_b32 v2, v16, v8 offset0:10 offset1:11
	ds_write2st64_b32 v2, v9, v7 offset0:12 offset1:13
	ds_write2st64_b32 v2, v11, v0 offset0:14 offset1:15
	s_mov_b64 s[6:7], 0
	s_mov_b32 s8, 1
	s_cbranch_vccz .LBB0_704
	ds_read2st64_b32 v[0:1], v207 offset1:1
	ds_read2st64_b32 v[2:3], v207 offset0:2 offset1:3
	ds_read2st64_b32 v[4:5], v207 offset0:4 offset1:5
	ds_read2st64_b32 v[6:7], v207 offset0:6 offset1:7
	ds_read2st64_b32 v[16:17], v207 offset0:16 offset1:17
	ds_read2st64_b32 v[18:19], v207 offset0:18 offset1:19
	ds_read2st64_b32 v[20:21], v207 offset0:20 offset1:21
	ds_read2st64_b32 v[22:23], v207 offset0:22 offset1:23
	ds_read2st64_b32 v[8:9], v207 offset0:8 offset1:9
	ds_read2st64_b32 v[10:11], v207 offset0:10 offset1:11
	ds_read2st64_b32 v[12:13], v207 offset0:12 offset1:13
	ds_read2st64_b32 v[14:15], v207 offset0:14 offset1:15
	ds_read2st64_b32 v[24:25], v207 offset0:24 offset1:25
	ds_read2st64_b32 v[26:27], v207 offset0:26 offset1:27
	ds_read2st64_b32 v[28:29], v207 offset0:28 offset1:29
	ds_read2st64_b32 v[30:31], v207 offset0:30 offset1:31
	s_and_saveexec_b64 s[8:9], s[38:39]
	s_cbranch_execz .LBB0_696
	s_waitcnt lgkmcnt(0)
	v_and_b32_e32 v49, 0xffffff80, v30
	v_and_b32_e32 v48, 0xffffff80, v0
	v_and_b32_e32 v39, 0xffffff80, v19
	v_and_b32_e32 v38, 0xffffff80, v20
	v_pk_add_f32 v[52:53], v[38:39], v[48:49] op_sel:[1,0] op_sel_hi:[0,1]
	v_cmp_gt_i32_e32 vcc, 0, v52
	v_bfrev_b32_e32 v43, 0.5
	s_movk_i32 s12, 0xff00
	v_cndmask_b32_e64 v43, v43, 3, vcc
	v_and_b32_e32 v42, 0xffffff80, v23
	v_and_or_b32 v56, v52, s12, v43
	v_mov_b32_e32 v43, v38
	v_pk_add_f32 v[52:53], v[48:49], v[42:43] op_sel_hi:[0,1]
	v_cmp_gt_i32_e32 vcc, 0, v53
	v_mov_b32_e32 v54, 0xfb
	v_and_b32_e32 v41, 0xffffff80, v22
	v_cndmask_b32_e64 v54, v54, 4, vcc
	v_and_b32_e32 v40, 0xffffff80, v21
	v_and_or_b32 v53, v53, s12, v54
	v_cmp_gt_i32_e32 vcc, 0, v52
	v_mov_b32_e32 v54, 0xf8
	v_mov_b32_e32 v58, 0xf9
	v_cndmask_b32_e64 v57, v54, 7, vcc
	v_pk_add_f32 v[54:55], v[48:49], v[40:41] op_sel_hi:[0,1]
	v_cmp_gt_i32_e32 vcc, 0, v55
	v_mov_b32_e32 v59, 0xfa
	v_and_b32_e32 v55, 0xffffff00, v55
	v_cndmask_b32_e64 v58, v58, 6, vcc
	v_cmp_gt_i32_e32 vcc, 0, v54
	v_and_b32_e32 v54, 0xffffff00, v54
	v_and_b32_e32 v52, 0xffffff00, v52
	v_cndmask_b32_e64 v59, v59, 5, vcc
	v_or_b32_e32 v55, v58, v55
	v_or_b32_e32 v54, v59, v54
	v_or_b32_e32 v52, v57, v52
	v_writelane_b32 v255, s8, 44
	v_min_f32_e32 v57, v55, v52
	v_max_f32_e32 v58, v53, v54
	v_min_f32_e32 v53, v53, v54
	v_max_f32_e32 v52, v55, v52
	v_writelane_b32 v255, s9, 45
	v_and_b32_e32 v45, 0xffffff80, v24
	v_and_b32_e32 v44, 0xffffff80, v27
	v_min_f32_e32 v59, v58, v57
	v_min_f32_e32 v54, v53, v52
	v_max_f32_e32 v57, v58, v57
	v_max_f32_e32 v52, v53, v52
	v_pk_add_f32 v[44:45], v[48:49], v[44:45] op_sel_hi:[0,1]
	v_and_b32_e32 v47, 0xffffff80, v26
	v_min_f32_e32 v58, v57, v52
	v_max_f32_e32 v57, v57, v52
	v_cmp_gt_i32_e32 vcc, 0, v45
	v_mov_b32_e32 v52, 0xf7
	v_and_b32_e32 v46, 0xffffff80, v25
	v_cndmask_b32_e64 v52, v52, 8, vcc
	v_and_or_b32 v45, v45, s12, v52
	v_cmp_gt_i32_e32 vcc, 0, v44
	v_mov_b32_e32 v52, 0xf4
	v_pk_add_f32 v[46:47], v[48:49], v[46:47] op_sel_hi:[0,1]
	v_cndmask_b32_e64 v52, v52, 11, vcc
	v_cmp_gt_i32_e32 vcc, 0, v47
	v_mov_b32_e32 v53, 0xf5
	v_min_f32_e32 v55, v59, v54
	v_max_f32_e32 v59, v59, v54
	v_cndmask_b32_e64 v53, v53, 10, vcc
	v_cmp_gt_i32_e32 vcc, 0, v46
	v_mov_b32_e32 v54, 0xf6
	v_and_b32_e32 v47, 0xffffff00, v47
	v_cndmask_b32_e64 v54, v54, 9, vcc
	v_and_b32_e32 v46, 0xffffff00, v46
	v_and_b32_e32 v44, 0xffffff00, v44
	v_or_b32_e32 v47, v53, v47
	v_or_b32_e32 v46, v54, v46
	v_or_b32_e32 v44, v52, v44
	v_and_b32_e32 v51, 0xffffff80, v29
	v_and_b32_e32 v50, 0xffffff80, v28
	v_writelane_b32 v255, s11, 46
	v_min_f32_e32 v52, v47, v44
	v_max_f32_e32 v53, v45, v46
	v_min_f32_e32 v46, v45, v46
	v_max_f32_e32 v47, v47, v44
	v_pk_add_f32 v[44:45], v[48:49], v[50:51] op_sel_hi:[0,1]
	v_cmp_gt_i32_e64 s[10:11], 0, v45
	v_mov_b32_e32 v50, 0xf2
	v_mov_b32_e32 v51, 0xf3
	v_cndmask_b32_e64 v50, v50, 13, s[10:11]
	v_cmp_gt_i32_e64 s[10:11], 0, v44
	v_and_b32_e32 v45, 0xffffff00, v45
	v_and_b32_e32 v44, 0xffffff00, v44
	v_cndmask_b32_e64 v51, v51, 12, s[10:11]
	v_or_b32_e32 v50, v50, v45
	v_or_b32_e32 v51, v51, v44
	v_and_b32_e32 v45, 0xffffff80, v31
	v_mov_b32_e32 v44, v49
	v_pk_add_f32 v[44:45], v[48:49], v[44:45] op_sel_hi:[0,1]
	v_cmp_gt_i32_e64 s[42:43], 0, v45
	v_mov_b32_e32 v249, 0xf0
	v_mov_b32_e32 v173, 0xf1
	v_cndmask_b32_e64 v63, v249, 15, s[42:43]
	v_cmp_gt_i32_e64 s[42:43], 0, v44
	v_and_b32_e32 v45, 0xffffff00, v45
	v_and_b32_e32 v44, 0xffffff00, v44
	v_cndmask_b32_e64 v173, v173, 14, s[42:43]
	v_or_b32_e32 v45, v63, v45
	v_or_b32_e32 v44, v173, v44
	v_max_f32_e32 v62, v51, v50
	v_min_f32_e32 v63, v44, v45
	v_min_f32_e32 v50, v51, v50
	v_max_f32_e32 v44, v44, v45
	v_max_f32_e32 v54, v53, v52
	v_max_f32_e32 v60, v46, v47
	v_min_f32_e32 v173, v62, v63
	v_min_f32_e32 v45, v50, v44
	v_min_f32_e32 v51, v53, v52
	v_min_f32_e32 v46, v46, v47
	v_max_f32_e32 v52, v62, v63
	v_max_f32_e32 v44, v50, v44
	v_max_f32_e32 v61, v54, v60
	v_min_f32_e32 v178, v173, v45
	v_max_f32_e32 v47, v51, v46
	v_min_f32_e32 v50, v52, v44
	v_min_f32_e32 v54, v54, v60
	v_max_f32_e32 v45, v173, v45
	v_min_f32_e32 v46, v51, v46
	v_max_f32_e32 v44, v52, v44
	v_min_f32_e32 v179, v61, v178
	v_min_f32_e32 v53, v47, v50
	v_min_f32_e32 v60, v54, v45
	v_min_f32_e32 v52, v46, v44
	v_max_f32_e32 v61, v61, v178
	v_max_f32_e32 v47, v47, v50
	v_max_f32_e32 v45, v54, v45
	v_max_f32_e32 v44, v46, v44
	v_min_f32_e32 v62, v179, v53
	v_min_f32_e32 v63, v60, v52
	v_min_f32_e32 v50, v61, v47
	v_min_f32_e32 v46, v45, v44
	v_max_f32_e32 v53, v179, v53
	v_max_f32_e32 v52, v60, v52
	v_max_f32_e32 v47, v61, v47
	v_max_f32_e32 v44, v45, v44
	v_min_f32_e32 v60, v53, v52
	v_min_f32_e32 v61, v47, v44
	v_max_f32_e32 v52, v53, v52
	v_max_f32_e32 v53, v47, v44
	v_and_b32_e32 v44, 0xffffff80, v1
	v_add_f32_e32 v45, v39, v44
	v_min_f32_e32 v51, v62, v63
	v_min_f32_e32 v173, v50, v46
	v_max_f32_e32 v62, v62, v63
	v_max_f32_e32 v63, v50, v46
	v_cmp_gt_i32_e32 vcc, 0, v45
	v_mov_b32_e32 v46, 0xec
	v_mov_b32_e32 v47, 0xe9
	v_cndmask_b32_e64 v46, v46, 19, vcc
	v_and_or_b32 v45, v45, s12, v46
	v_pk_add_f32 v[42:43], v[44:45], v[42:43] op_sel_hi:[0,1]
	v_cmp_gt_i32_e32 vcc, 0, v43
	v_mov_b32_e32 v46, 0xeb
	v_pk_add_f32 v[40:41], v[44:45], v[40:41] op_sel_hi:[0,1]
	v_cndmask_b32_e64 v46, v46, 20, vcc
	v_and_or_b32 v43, v43, s12, v46
	v_cmp_gt_i32_e32 vcc, 0, v42
	v_mov_b32_e32 v46, 0xe8
	v_mov_b32_e32 v50, 0xea
	v_cndmask_b32_e64 v46, v46, 23, vcc
	v_cmp_gt_i32_e32 vcc, 0, v41
	v_and_b32_e32 v41, 0xffffff00, v41
	v_and_b32_e32 v42, 0xffffff00, v42
	v_cndmask_b32_e64 v47, v47, 22, vcc
	v_cmp_gt_i32_e32 vcc, 0, v40
	v_and_b32_e32 v40, 0xffffff00, v40
	v_or_b32_e32 v41, v47, v41
	v_cndmask_b32_e64 v50, v50, 21, vcc
	v_or_b32_e32 v40, v50, v40
	v_or_b32_e32 v42, v46, v42
	v_and_b32_e32 v182, 0xffffff80, v3
	v_min_f32_e32 v46, v41, v42
	v_max_f32_e32 v47, v43, v40
	v_min_f32_e32 v40, v43, v40
	v_max_f32_e32 v41, v41, v42
	v_and_b32_e32 v37, 0xffffff80, v4
	v_max_f32_e32 v43, v47, v46
	v_min_f32_e32 v42, v40, v41
	v_max_f32_e32 v40, v40, v41
	v_min_f32_e32 v50, v47, v46
	v_and_b32_e32 v46, 0xffffff80, v2
	v_and_b32_e32 v36, 0xffffff80, v18
	v_min_f32_e32 v179, v43, v40
	v_max_f32_e32 v180, v43, v40
	v_pk_add_f32 v[40:41], v[46:47], v[38:39] op_sel_hi:[0,1]
	v_cmp_gt_i32_e32 vcc, 0, v41
	v_mov_b32_e32 v38, 0xdc
	v_and_b32_e32 v35, 0xffffff80, v7
	v_cndmask_b32_e64 v38, v38, 35, vcc
	v_and_or_b32 v41, v41, s12, v38
	v_cmp_gt_i32_e32 vcc, 0, v40
	v_mov_b32_e32 v38, 0xdb
	v_and_b32_e32 v34, 0xffffff80, v17
	v_cndmask_b32_e64 v38, v38, 36, vcc
	v_and_or_b32 v181, v40, s12, v38
	v_add_f32_e32 v38, v39, v182
	v_cmp_gt_i32_e32 vcc, 0, v38
	v_mov_b32_e32 v39, 0xcc
	s_nop 0
	v_cndmask_b32_e64 v39, v39, 51, vcc
	v_and_or_b32 v54, v38, s12, v39
	v_pk_add_f32 v[38:39], v[48:49], v[36:37]
	v_min_f32_e32 v178, v50, v42
	v_cmp_gt_i32_e32 vcc, 0, v38
	v_bfrev_b32_e32 v39, -0.5
	v_max_f32_e32 v50, v50, v42
	v_cndmask_b32_e64 v39, v39, 2, vcc
	v_and_or_b32 v38, v38, s12, v39
	v_mov_b32_e32 v39, 0xed
	v_and_b32_e32 v43, 0xffffff80, v6
	v_min_f32_e32 v183, v38, v56
	v_max_f32_e32 v56, v38, v56
	v_add_f32_e32 v38, v36, v44
	v_cmp_gt_i32_e32 vcc, 0, v38
	v_and_b32_e32 v42, 0xffffff80, v5
	v_and_b32_e32 v33, 0xffffff80, v14
	v_cndmask_b32_e64 v39, v39, 18, vcc
	v_and_or_b32 v38, v38, s12, v39
	v_mov_b32_e32 v39, 0xdd
	v_and_b32_e32 v32, 0xffffff80, v16
	v_min_f32_e32 v190, v38, v45
	v_max_f32_e32 v195, v38, v45
	v_add_f32_e32 v38, v36, v46
	v_cmp_gt_i32_e32 vcc, 0, v38
	v_mov_b32_e32 v45, 0x61
	v_mov_b32_e32 v234, 0xef
	v_cndmask_b32_e64 v39, v39, 34, vcc
	v_and_or_b32 v38, v38, s12, v39
	v_mov_b32_e32 v39, 0xcd
	v_mov_b32_e32 v241, 0xdf
	v_min_f32_e32 v209, v38, v41
	v_max_f32_e32 v210, v38, v41
	v_add_f32_e32 v38, v36, v182
	v_cmp_gt_i32_e32 vcc, 0, v38
	v_mov_b32_e32 v41, 0x42
	v_mov_b32_e32 v244, 0xcf
	v_cndmask_b32_e64 v39, v39, 50, vcc
	v_and_or_b32 v40, v38, s12, v39
	v_pk_add_f32 v[38:39], v[36:37], v[36:37] op_sel:[1,0] op_sel_hi:[0,1]
	v_cmp_gt_i32_e32 vcc, 0, v38
	v_mov_b32_e32 v39, 0xbd
	v_and_b32_e32 v47, 0xffffff80, v8
	v_cndmask_b32_e32 v39, v39, v41, vcc
	v_and_or_b32 v41, v38, s12, v39
	v_pk_add_f32 v[38:39], v[48:49], v[34:35]
	v_pk_add_f32 v[48:49], v[48:49], v[32:33]
	v_cmp_gt_i32_e32 vcc, 0, v38
	v_mov_b32_e32 v39, 0xfe
	s_mov_b32 s28, 0xff61b1e6
	v_cndmask_b32_e64 v39, v39, 1, vcc
	v_and_or_b32 v211, v38, s12, v39
	v_add_f32_e32 v38, v34, v44
	v_cmp_gt_i32_e32 vcc, 0, v38
	v_mov_b32_e32 v39, 0xee
	v_add_f32_e32 v44, v32, v44
	v_cndmask_b32_e64 v39, v39, 17, vcc
	v_and_or_b32 v212, v38, s12, v39
	v_add_f32_e32 v38, v34, v46
	v_cmp_gt_i32_e32 vcc, 0, v38
	v_mov_b32_e32 v39, 0xde
	v_add_f32_e32 v46, v32, v46
	v_cndmask_b32_e64 v39, v39, 33, vcc
	v_and_or_b32 v213, v38, s12, v39
	v_add_f32_e32 v38, v34, v182
	v_cmp_gt_i32_e32 vcc, 0, v38
	v_mov_b32_e32 v39, 0xce
	v_add_f32_e32 v182, v32, v182
	v_cndmask_b32_e64 v39, v39, 49, vcc
	v_and_or_b32 v38, v38, s12, v39
	v_cmp_gt_i32_e64 s[74:75], 0, v46
	v_cmp_gt_i32_e64 s[84:85], 0, v182
	v_min_f32_e32 v219, v38, v40
	v_max_f32_e32 v220, v38, v40
	v_pk_add_f32 v[38:39], v[36:37], v[34:35] op_sel:[1,0] op_sel_hi:[0,1]
	v_cmp_gt_i32_e32 vcc, 0, v38
	v_mov_b32_e32 v39, 0xbe
	v_mov_b32_e32 v40, 0x41
	v_cndmask_b32_e32 v39, v39, v40, vcc
	v_and_or_b32 v38, v38, s12, v39
	v_mov_b32_e32 v40, v35
	v_cndmask_b32_e64 v241, v241, 32, s[74:75]
	v_min_f32_e32 v215, v38, v41
	v_max_f32_e32 v216, v38, v41
	v_pk_add_f32 v[38:39], v[34:35], v[42:43]
	v_mov_b32_e32 v41, v43
	v_pk_add_f32 v[40:41], v[34:35], v[40:41] op_sel_hi:[0,1]
	v_cmp_gt_i32_e32 vcc, 0, v38
	v_mov_b32_e32 v34, 0xae
	v_mov_b32_e32 v39, 0x51
	v_cndmask_b32_e32 v34, v34, v39, vcc
	v_cmp_gt_i32_e32 vcc, 0, v41
	v_mov_b32_e32 v39, 0x9e
	v_and_b32_e32 v38, 0xffffff00, v38
	v_cndmask_b32_e32 v39, v39, v45, vcc
	v_or_b32_e32 v218, v34, v38
	v_cmp_gt_i32_e32 vcc, 0, v40
	v_mov_b32_e32 v34, 0x8e
	v_mov_b32_e32 v38, 0x71
	v_cndmask_b32_e32 v34, v34, v38, vcc
	v_and_or_b32 v214, v40, s12, v34
	v_cmp_gt_i32_e32 vcc, 0, v48
	v_mov_b32_e32 v34, 0xff
	v_cndmask_b32_e64 v244, v244, 48, s[84:85]
	v_cndmask_b32_e64 v34, v34, 0, vcc
	v_and_or_b32 v34, v48, s12, v34
	v_and_or_b32 v46, v46, s12, v241
	v_and_or_b32 v182, v182, s12, v244
	v_max_f32_e32 v48, v34, v211
	v_min_f32_e32 v34, v34, v211
	v_max_f32_e32 v49, v48, v183
	v_max_f32_e32 v211, v34, v56
	v_min_f32_e32 v48, v48, v183
	v_min_f32_e32 v34, v34, v56
	v_max_f32_e32 v221, v49, v211
	v_max_f32_e32 v56, v48, v34
	v_min_f32_e32 v49, v49, v211
	v_min_f32_e32 v34, v48, v34
	v_max_f32_e32 v222, v221, v55
	v_max_f32_e32 v183, v56, v58
	v_max_f32_e32 v211, v49, v59
	v_max_f32_e32 v48, v34, v57
	v_min_f32_e32 v55, v221, v55
	v_min_f32_e32 v56, v56, v58
	v_min_f32_e32 v49, v49, v59
	v_min_f32_e32 v34, v34, v57
	v_max_f32_e32 v241, v46, v213
	v_max_f32_e32 v58, v55, v56
	v_max_f32_e32 v57, v49, v34
	v_min_f32_e32 v55, v55, v56
	v_min_f32_e32 v34, v49, v34
	v_min_f32_e32 v46, v46, v213
	v_max_f32_e32 v244, v181, v182
	v_max_f32_e32 v49, v55, v34
	v_min_f32_e32 v34, v55, v34
	v_cmp_gt_i32_e64 s[6:7], 0, v44
	v_min_f32_e32 v181, v181, v182
	s_nop 0
	v_cndmask_b32_e64 v234, v234, 16, s[6:7]
	v_and_or_b32 v44, v44, s12, v234
	v_max_f32_e32 v234, v44, v212
	v_min_f32_e32 v44, v44, v212
	v_max_f32_e32 v235, v234, v190
	v_max_f32_e32 v212, v44, v195
	v_min_f32_e32 v190, v234, v190
	v_min_f32_e32 v44, v44, v195
	v_max_f32_e32 v242, v241, v209
	v_max_f32_e32 v213, v46, v210
	v_min_f32_e32 v245, v244, v219
	v_min_f32_e32 v182, v181, v220
	v_min_f32_e32 v209, v241, v209
	v_min_f32_e32 v46, v46, v210
	v_max_f32_e32 v219, v244, v219
	v_max_f32_e32 v181, v181, v220
	v_max_f32_e32 v59, v58, v57
	v_min_f32_e32 v57, v58, v57
	v_max_f32_e32 v236, v235, v212
	v_max_f32_e32 v195, v190, v44
	v_min_f32_e32 v212, v235, v212
	v_min_f32_e32 v44, v190, v44
	v_max_f32_e32 v243, v242, v213
	v_min_f32_e32 v246, v245, v182
	v_max_f32_e32 v210, v209, v46
	v_min_f32_e32 v220, v219, v181
	v_min_f32_e32 v213, v242, v213
	v_max_f32_e32 v182, v245, v182
	v_min_f32_e32 v46, v209, v46
	v_max_f32_e32 v181, v219, v181
	v_max_f32_e32 v237, v236, v178
	v_max_f32_e32 v234, v195, v179
	v_max_f32_e32 v235, v212, v50
	v_max_f32_e32 v190, v44, v180
	v_min_f32_e32 v247, v243, v246
	v_min_f32_e32 v241, v210, v220
	v_min_f32_e32 v242, v213, v182
	v_min_f32_e32 v209, v46, v181
	v_min_f32_e32 v178, v236, v178
	v_min_f32_e32 v179, v195, v179
	v_min_f32_e32 v50, v212, v50
	v_min_f32_e32 v44, v44, v180
	v_max_f32_e32 v236, v243, v246
	v_max_f32_e32 v210, v210, v220
	v_max_f32_e32 v182, v213, v182
	v_max_f32_e32 v46, v46, v181
	v_max_f32_e32 v223, v222, v183
	v_max_f32_e32 v224, v211, v48
	v_min_f32_e32 v183, v222, v183
	v_min_f32_e32 v48, v211, v48
	v_max_f32_e32 v238, v237, v234
	v_max_f32_e32 v239, v235, v190
	v_min_f32_e32 v244, v247, v241
	v_min_f32_e32 v219, v242, v209
	v_max_f32_e32 v195, v178, v179
	v_max_f32_e32 v180, v50, v44
	v_min_f32_e32 v220, v236, v210
	v_min_f32_e32 v181, v182, v46
	v_min_f32_e32 v234, v237, v234
	v_min_f32_e32 v190, v235, v190
	v_max_f32_e32 v237, v247, v241
	v_max_f32_e32 v209, v242, v209
	v_min_f32_e32 v178, v178, v179
	v_min_f32_e32 v44, v50, v44
	v_max_f32_e32 v50, v236, v210
	v_max_f32_e32 v46, v182, v46
	v_max_f32_e32 v225, v223, v224
	v_max_f32_e32 v211, v183, v48
	v_min_f32_e32 v223, v223, v224
	v_min_f32_e32 v48, v183, v48
	v_max_f32_e32 v240, v238, v239
	v_min_f32_e32 v245, v244, v219
	v_max_f32_e32 v212, v195, v180
	v_min_f32_e32 v213, v220, v181
	v_max_f32_e32 v235, v234, v190
	v_min_f32_e32 v241, v237, v209
	v_max_f32_e32 v179, v178, v44
	v_min_f32_e32 v182, v50, v46
	v_min_f32_e32 v238, v238, v239
	v_max_f32_e32 v219, v244, v219
	v_min_f32_e32 v180, v195, v180
	v_max_f32_e32 v181, v220, v181
	v_min_f32_e32 v190, v234, v190
	v_max_f32_e32 v209, v237, v209
	v_min_f32_e32 v44, v178, v44
	v_max_f32_e32 v46, v50, v46
	v_max_f32_e32 v226, v225, v51
	v_max_f32_e32 v221, v59, v173
	v_max_f32_e32 v222, v211, v60
	v_max_f32_e32 v56, v49, v61
	v_max_f32_e32 v224, v223, v62
	v_max_f32_e32 v58, v57, v63
	v_max_f32_e32 v183, v48, v52
	v_max_f32_e32 v55, v34, v53
	v_min_f32_e32 v248, v240, v245
	v_min_f32_e32 v243, v212, v213
	v_min_f32_e32 v242, v235, v241
	v_min_f32_e32 v210, v179, v182
	v_min_f32_e32 v239, v238, v219
	v_min_f32_e32 v195, v180, v181
	v_min_f32_e32 v234, v190, v209
	v_min_f32_e32 v178, v44, v46
	v_max_f32_e32 v227, v226, v221
	v_max_f32_e32 v228, v222, v56
	v_max_f32_e32 v230, v224, v58
	v_max_f32_e32 v231, v183, v55
	v_min_f32_e32 v246, v248, v243
	v_min_f32_e32 v236, v242, v210
	v_min_f32_e32 v220, v239, v195
	v_min_f32_e32 v237, v234, v178
	v_max_f32_e32 v229, v227, v228
	v_max_f32_e32 v232, v230, v231
	v_min_f32_e32 v247, v246, v236
	v_min_f32_e32 v244, v220, v237
	v_min_f32_e32 v51, v225, v51
	v_min_f32_e32 v59, v59, v173
	v_min_f32_e32 v60, v211, v60
	v_min_f32_e32 v61, v49, v61
	v_min_f32_e32 v62, v223, v62
	v_min_f32_e32 v57, v57, v63
	v_min_f32_e32 v48, v48, v52
	v_min_f32_e32 v34, v34, v53
	v_max_f32_e32 v63, v240, v245
	v_max_f32_e32 v212, v212, v213
	v_max_f32_e32 v235, v235, v241
	v_max_f32_e32 v179, v179, v182
	v_max_f32_e32 v219, v238, v219
	v_max_f32_e32 v180, v180, v181
	v_max_f32_e32 v190, v190, v209
	v_max_f32_e32 v44, v44, v46
	v_max_f32_e32 v233, v229, v232
	v_min_f32_e32 v50, v247, v244
	v_max_f32_e32 v173, v51, v59
	v_max_f32_e32 v211, v60, v61
	v_max_f32_e32 v223, v62, v57
	v_max_f32_e32 v53, v48, v34
	v_min_f32_e32 v213, v63, v212
	v_min_f32_e32 v182, v235, v179
	v_min_f32_e32 v181, v219, v180
	v_min_f32_e32 v46, v190, v44
	v_min_f32_e32 v227, v227, v228
	v_min_f32_e32 v228, v230, v231
	v_max_f32_e32 v230, v246, v236
	v_max_f32_e32 v220, v220, v237
	v_max_f32_e32 v50, v233, v50
	v_max_f32_e32 v44, v190, v44
	v_max_f32_e32 v225, v173, v211
	v_max_f32_e32 v233, v223, v53
	v_min_f32_e32 v240, v213, v182
	v_min_f32_e32 v209, v181, v46
	v_min_f32_e32 v221, v226, v221
	v_min_f32_e32 v222, v222, v56
	v_min_f32_e32 v224, v224, v58
	v_min_f32_e32 v183, v183, v55
	v_max_f32_e32 v241, v248, v243
	v_max_f32_e32 v210, v242, v210
	v_max_f32_e32 v195, v239, v195
	v_max_f32_e32 v234, v234, v178
	v_min_f32_e32 v51, v51, v59
	v_min_f32_e32 v59, v60, v61
	v_min_f32_e32 v57, v62, v57
	v_min_f32_e32 v34, v48, v34
	v_max_f32_e32 v60, v63, v212
	v_max_f32_e32 v62, v235, v179
	v_max_f32_e32 v58, v227, v228
	v_min_f32_e32 v63, v230, v220
	v_min_f32_e32 v211, v173, v211
	v_min_f32_e32 v223, v223, v53
	v_max_f32_e32 v213, v213, v182
	v_max_f32_e32 v46, v181, v46
	v_max_f32_e32 v226, v221, v222
	v_max_f32_e32 v238, v224, v183
	v_max_f32_e32 v243, v51, v59
	v_max_f32_e32 v245, v57, v34
	v_min_f32_e32 v179, v60, v62
	v_max_f32_e32 v63, v58, v63
	v_max_f32_e32 v53, v211, v223
	v_min_f32_e32 v58, v213, v46
	v_min_f32_e32 v181, v221, v222
	v_min_f32_e32 v221, v224, v183
	v_max_f32_e32 v222, v241, v210
	v_max_f32_e32 v224, v195, v234
	v_min_f32_e32 v51, v51, v59
	v_min_f32_e32 v59, v57, v34
	v_max_f32_e32 v231, v60, v62
	v_min_f32_e32 v57, v229, v232
	v_max_f32_e32 v62, v247, v244
	v_min_f32_e32 v239, v195, v234
	v_min_f32_e32 v242, v241, v210
	v_max_f32_e32 v212, v219, v180
	v_max_f32_e32 v178, v53, v58
	v_max_f32_e32 v53, v181, v221
	v_min_f32_e32 v173, v222, v224
	v_max_f32_e32 v183, v57, v62
	v_min_f32_e32 v57, v225, v233
	v_max_f32_e32 v62, v240, v209
	v_min_f32_e32 v219, v212, v44
	v_max_f32_e32 v180, v53, v173
	v_max_f32_e32 v190, v57, v62
	v_min_f32_e32 v57, v226, v238
	v_max_f32_e32 v173, v242, v239
	v_max_f32_e32 v55, v226, v238
	v_min_f32_e32 v56, v242, v239
	v_max_f32_e32 v210, v230, v220
	v_max_f32_e32 v195, v57, v173
	v_min_f32_e32 v57, v243, v245
	v_max_f32_e32 v173, v179, v219
	v_max_f32_e32 v55, v55, v56
	v_min_f32_e32 v56, v179, v219
	v_min_f32_e32 v179, v227, v228
	v_min_f32_e32 v52, v240, v209
	v_max_f32_e32 v209, v57, v173
	v_max_f32_e32 v46, v213, v46
	v_max_f32_e32 v44, v212, v44
	v_max_f32_e32 v210, v179, v210
	v_min_f32_e32 v179, v211, v223
	v_max_f32_e32 v211, v179, v46
	v_min_f32_e32 v46, v181, v221
	v_max_f32_e32 v181, v222, v224
	v_min_f32_e32 v53, v231, v44
	v_max_f32_e32 v44, v231, v44
	v_max_f32_e32 v212, v46, v181
	v_min_f32_e32 v46, v51, v59
	v_max_f32_e32 v34, v51, v59
	v_pk_add_f32 v[36:37], v[36:37], v[32:33] op_sel:[1,0] op_sel_hi:[0,1]
	v_mov_b32_e32 v37, 0xbf
	v_max_f32_e32 v213, v46, v44
	v_cmp_gt_i32_e32 vcc, 0, v36
	v_mov_b32_e32 v221, 0x50
	v_and_b32_e32 v41, 0xffffff00, v41
	v_cndmask_b32_e64 v37, v37, 64, vcc
	v_and_or_b32 v36, v36, s12, v37
	v_or_b32_e32 v217, v39, v41
	v_max_f32_e32 v49, v225, v233
	v_max_f32_e32 v44, v54, v36
	v_min_f32_e32 v54, v54, v36
	v_pk_add_f32 v[36:37], v[32:33], v[42:43] op_sel_hi:[0,1]
	v_cmp_gt_i32_e64 s[68:69], 0, v37
	v_mov_b32_e32 v42, 0x9f
	v_mov_b32_e32 v43, 0x60
	v_cndmask_b32_e64 v42, v42, v43, s[68:69]
	v_cmp_gt_i32_e64 s[68:69], 0, v36
	v_mov_b32_e32 v43, 0xaf
	v_and_b32_e32 v37, 0xffffff00, v37
	v_cndmask_b32_e64 v43, v43, v221, s[68:69]
	v_and_b32_e32 v36, 0xffffff00, v36
	v_or_b32_e32 v37, v42, v37
	v_or_b32_e32 v36, v43, v36
	v_min_f32_e32 v42, v37, v217
	v_max_f32_e32 v43, v36, v218
	v_max_f32_e32 v37, v37, v217
	v_min_f32_e32 v36, v36, v218
	v_max_f32_e32 v46, v44, v215
	v_max_f32_e32 v219, v54, v216
	v_min_f32_e32 v221, v43, v42
	v_min_f32_e32 v217, v36, v37
	v_max_f32_e32 v42, v43, v42
	v_max_f32_e32 v36, v36, v37
	v_max_f32_e32 v220, v46, v219
	v_min_f32_e32 v44, v44, v215
	v_min_f32_e32 v54, v54, v216
	v_min_f32_e32 v219, v46, v219
	v_mov_b32_e32 v46, v35
	v_min_f32_e32 v216, v42, v36
	v_max_f32_e32 v225, v42, v36
	v_pk_add_f32 v[36:37], v[32:33], v[46:47] op_sel_hi:[0,1]
	v_and_b32_e32 v45, 0xffffff80, v9
	v_max_f32_e32 v215, v44, v54
	v_min_f32_e32 v54, v44, v54
	v_mov_b32_e32 v44, v35
	v_cmp_gt_i32_e32 vcc, 0, v37
	v_mov_b32_e32 v35, 0x7f
	v_pk_add_f32 v[42:43], v[32:33], v[44:45] op_sel_hi:[0,1]
	v_cndmask_b32_e32 v35, v35, v196, vcc
	v_cmp_gt_i32_e32 vcc, 0, v36
	v_mov_b32_e32 v47, 0x8f
	v_mov_b32_e32 v45, 0x6f
	v_cndmask_b32_e32 v44, v47, v198, vcc
	v_cmp_gt_i32_e32 vcc, 0, v43
	v_mov_b32_e32 v46, 0x90
	v_and_b32_e32 v37, 0xffffff00, v37
	v_and_b32_e32 v36, 0xffffff00, v36
	v_cndmask_b32_e32 v45, v45, v46, vcc
	v_and_b32_e32 v43, 0xffffff00, v43
	v_cmp_gt_i32_e32 vcc, 0, v42
	v_or_b32_e32 v35, v35, v37
	v_or_b32_e32 v36, v44, v36
	v_or_b32_e32 v37, v45, v43
	v_and_b32_e32 v41, 0xffffff80, v10
	v_and_b32_e32 v40, 0xffffff80, v13
	v_cndmask_b32_e32 v46, v47, v198, vcc
	v_cmp_lt_f32_e32 vcc, v37, v35
	v_cmp_lt_f32_e64 s[8:9], v214, v36
	v_and_b32_e32 v39, 0xffffff80, v12
	v_cndmask_b32_e32 v43, v35, v37, vcc
	v_cndmask_b32_e64 v45, v36, v214, s[8:9]
	v_cndmask_b32_e32 v35, v37, v35, vcc
	v_pk_add_f32 v[36:37], v[32:33], v[40:41] op_sel_hi:[0,1]
	v_cmp_gt_i32_e64 s[80:81], 0, v37
	v_mov_b32_e32 v40, 0x5f
	v_mov_b32_e32 v41, 0xa0
	v_and_b32_e32 v38, 0xffffff80, v11
	v_cndmask_b32_e64 v40, v40, v41, s[80:81]
	v_and_b32_e32 v42, 0xffffff00, v42
	v_and_or_b32 v37, v37, s12, v40
	v_cmp_gt_i32_e64 s[80:81], 0, v36
	v_mov_b32_e32 v40, 0xd0
	v_pk_add_f32 v[38:39], v[32:33], v[38:39] op_sel_hi:[0,1]
	v_or_b32_e32 v42, v46, v42
	v_cndmask_b32_e64 v40, 47, v40, s[80:81]
	v_cmp_gt_i32_e64 s[80:81], 0, v39
	v_mov_b32_e32 v41, 0xc0
	v_cndmask_b32_e64 v42, v214, v42, s[8:9]
	v_cndmask_b32_e64 v41, 63, v41, s[80:81]
	v_cmp_gt_i32_e64 s[80:81], 0, v38
	v_mov_b32_e32 v214, 0x4f
	v_mov_b32_e32 v229, 0xb0
	v_cndmask_b32_e64 v214, v214, v229, s[80:81]
	v_and_b32_e32 v39, 0xffffff00, v39
	v_and_b32_e32 v38, 0xffffff00, v38
	v_and_b32_e32 v36, 0xffffff00, v36
	v_or_b32_e32 v39, v41, v39
	v_or_b32_e32 v38, v214, v38
	v_or_b32_e32 v36, v40, v36
	v_min_f32_e32 v40, v39, v36
	v_max_f32_e32 v41, v37, v38
	v_min_f32_e32 v37, v37, v38
	v_max_f32_e32 v36, v39, v36
	v_max_f32_e32 v44, v42, v43
	v_max_f32_e32 v46, v45, v35
	v_min_f32_e32 v214, v41, v40
	v_min_f32_e32 v38, v37, v36
	v_min_f32_e32 v42, v42, v43
	v_min_f32_e32 v35, v45, v35
	v_max_f32_e32 v40, v41, v40
	v_max_f32_e32 v36, v37, v36
	v_max_f32_e32 v47, v44, v46
	v_min_f32_e32 v39, v214, v38
	v_max_f32_e32 v43, v42, v35
	v_min_f32_e32 v37, v40, v36
	v_min_f32_e32 v44, v44, v46
	v_max_f32_e32 v38, v214, v38
	v_min_f32_e32 v35, v42, v35
	v_max_f32_e32 v36, v40, v36
	v_min_f32_e32 v218, v221, v217
	v_max_f32_e32 v217, v221, v217
	v_min_f32_e32 v229, v47, v39
	v_min_f32_e32 v41, v43, v37
	v_min_f32_e32 v46, v44, v38
	v_min_f32_e32 v40, v35, v36
	v_max_f32_e32 v39, v47, v39
	v_max_f32_e32 v37, v43, v37
	v_max_f32_e32 v38, v44, v38
	v_max_f32_e32 v35, v35, v36
	v_max_f32_e32 v222, v220, v218
	v_max_f32_e32 v223, v215, v216
	v_max_f32_e32 v221, v219, v217
	v_max_f32_e32 v226, v54, v225
	v_min_f32_e32 v218, v220, v218
	v_min_f32_e32 v215, v215, v216
	v_min_f32_e32 v217, v219, v217
	v_min_f32_e32 v54, v54, v225
	v_min_f32_e32 v43, v39, v37
	v_min_f32_e32 v36, v38, v35
	v_max_f32_e32 v37, v39, v37
	v_max_f32_e32 v35, v38, v35
	v_max_f32_e32 v216, v218, v215
	v_max_f32_e32 v219, v217, v54
	v_min_f32_e32 v44, v43, v36
	v_min_f32_e32 v215, v218, v215
	v_min_f32_e32 v54, v217, v54
	v_min_f32_e32 v38, v37, v35
	v_max_f32_e32 v43, v43, v36
	v_max_f32_e32 v35, v37, v35
	v_and_b32_e32 v37, 0xffffff80, v15
	v_mov_b32_e32 v36, v33
	v_pk_add_f32 v[32:33], v[32:33], v[36:37] op_sel_hi:[0,1]
	v_mov_b32_e32 v37, 0xe0
	v_max_f32_e32 v217, v215, v54
	v_min_f32_e32 v54, v215, v54
	v_cmp_gt_i32_e64 s[76:77], 0, v33
	v_and_b32_e32 v33, 0xffffff00, v33
	s_nop 0
	v_cndmask_b32_e64 v36, 15, v249, s[76:77]
	v_cmp_gt_i32_e64 s[76:77], 0, v32
	v_and_b32_e32 v32, 0xffffff00, v32
	v_or_b32_e32 v33, v36, v33
	v_cndmask_b32_e64 v37, 31, v37, s[76:77]
	v_or_b32_e32 v32, v37, v32
	v_max_f32_e32 v36, v32, v33
	v_min_f32_e32 v32, v32, v33
	v_max_f32_e32 v37, v36, v36
	v_max_f32_e32 v33, v32, v32
	v_max_f32_e32 v37, 0xff61b1e6, v37
	v_max_f32_e32 v33, 0xff61b1e6, v33
	v_max_f32_e32 v224, v222, v223
	v_max_f32_e32 v233, v37, v33
	v_min_f32_e32 v33, v37, v33
	v_max_f32_e32 v234, 0xff61b1e6, v233
	v_max_f32_e32 v37, 0xff61b1e6, v33
	v_cmp_nlt_f32_e32 vcc, s28, v33
	v_max_f32_e32 v227, v221, v226
	v_max_f32_e32 v235, v234, v37
	v_cmp_nlt_f32_e64 s[88:89], s28, v235
	v_cndmask_b32_e32 v33, v199, v33, vcc
	v_min_f32_e32 v45, v229, v41
	v_cndmask_b32_e64 v236, v199, v235, s[88:89]
	v_cmp_nlt_f32_e64 s[88:89], s28, v233
	v_min_f32_e32 v42, v46, v40
	v_min_f32_e32 v222, v222, v223
	v_cndmask_b32_e64 v233, v199, v233, s[88:89]
	v_cmp_nlt_f32_e64 s[88:89], s28, v36
	v_min_f32_e32 v221, v221, v226
	v_max_f32_e32 v41, v229, v41
	v_cndmask_b32_e64 v36, v199, v36, s[88:89]
	v_cmp_nlt_f32_e64 s[88:89], s28, v32
	v_max_f32_e32 v40, v46, v40
	s_nop 0
	v_cndmask_b32_e64 v32, v199, v32, s[88:89]
	v_max_f32_e32 v237, v36, v32
	v_min_f32_e32 v32, v36, v32
	v_max_f32_e32 v238, v233, v237
	v_max_f32_e32 v36, v33, v32
	v_max_f32_e32 v228, v224, v227
	v_min_f32_e32 v214, v45, v42
	v_max_f32_e32 v220, v216, v219
	v_max_f32_e32 v223, v222, v221
	v_min_f32_e32 v46, v41, v40
	v_min_f32_e32 v224, v224, v227
	v_max_f32_e32 v42, v45, v42
	v_min_f32_e32 v216, v216, v219
	v_min_f32_e32 v221, v222, v221
	v_max_f32_e32 v40, v41, v40
	v_max_f32_e32 v239, v238, v36
	v_min_f32_e32 v233, v233, v237
	v_min_f32_e32 v32, v33, v32
	v_min_f32_e32 v37, v234, v37
	v_min_f32_e32 v36, v238, v36
	v_max_f32_e32 v52, v49, v52
	s_mov_b64 s[6:7], s[96:97]
	v_cmp_nlt_f32_e64 s[88:89], s28, v239
	v_cmp_nlt_f32_e64 s[76:77], s28, v37
	v_cmp_nlt_f32_e64 s[14:15], s28, v36
	v_max_f32_e32 v230, v228, v214
	v_max_f32_e32 v47, v220, v44
	v_max_f32_e32 v226, v223, v46
	v_max_f32_e32 v39, v217, v38
	v_max_f32_e32 v45, v224, v42
	v_max_f32_e32 v219, v216, v43
	v_max_f32_e32 v41, v221, v40
	v_max_f32_e32 v215, v54, v35
	v_cndmask_b32_e64 v240, v199, v239, s[88:89]
	v_max_f32_e32 v33, v233, v32
	v_cndmask_b32_e64 v234, v199, v37, s[76:77]
	v_cndmask_b32_e64 v238, v199, v36, s[14:15]
	v_min_f32_e32 v32, v233, v32
	v_cmp_nlt_f32_e64 s[88:89], s28, v33
	v_cmp_nlt_f32_e32 vcc, s28, v32
	v_max_f32_e32 v48, v243, v245
	v_max_f32_e32 v225, v230, v47
	v_max_f32_e32 v218, v226, v39
	v_max_f32_e32 v227, v45, v219
	v_max_f32_e32 v222, v41, v215
	v_min_f32_e32 v241, v236, v240
	v_cndmask_b32_e64 v237, v199, v33, s[88:89]
	v_min_f32_e32 v243, v234, v238
	v_cndmask_b32_e32 v233, v199, v32, vcc
	v_max_f32_e32 v229, v225, v218
	v_max_f32_e32 v231, v227, v222
	v_min_f32_e32 v242, v241, v237
	v_min_f32_e32 v244, v243, v233
	v_min_f32_e32 v214, v228, v214
	v_max_f32_e32 v232, v229, v231
	v_min_f32_e32 v245, v242, v244
	v_max_f32_e32 v228, 0xff61b1e6, v235
	v_max_f32_e32 v235, v239, v239
	v_max_f32_e32 v36, v36, v36
	v_min_f32_e32 v44, v220, v44
	v_min_f32_e32 v46, v223, v46
	v_min_f32_e32 v38, v217, v38
	v_min_f32_e32 v42, v224, v42
	v_min_f32_e32 v43, v216, v43
	v_min_f32_e32 v40, v221, v40
	v_min_f32_e32 v35, v54, v35
	v_max_f32_e32 v235, 0xff61b1e6, v235
	v_max_f32_e32 v33, v33, v33
	v_max_f32_e32 v37, 0xff61b1e6, v37
	v_max_f32_e32 v36, 0xff61b1e6, v36
	v_max_f32_e32 v32, v32, v32
	v_max_f32_e32 v232, v232, v245
	s_mov_b32 s36, s18
	v_max_f32_e32 v33, 0xff61b1e6, v33
	v_max_f32_e32 v32, 0xff61b1e6, v32
	v_max_f32_e32 v220, v214, v44
	v_max_f32_e32 v217, v46, v38
	v_max_f32_e32 v216, v42, v43
	v_max_f32_e32 v54, v40, v35
	v_min_f32_e32 v239, v228, v235
	v_min_f32_e32 v245, 0xff61b1e6, v33
	v_min_f32_e32 v247, v37, v36
	v_min_f32_e32 v248, 0xff61b1e6, v32
	v_max_f32_e32 v223, v220, v217
	v_max_f32_e32 v221, v216, v54
	v_min_f32_e32 v246, v239, v245
	v_min_f32_e32 v249, v247, v248
	v_min_f32_e32 v47, v230, v47
	v_max_f32_e32 v230, v236, v240
	v_cmp_ngt_f32_e64 s[16:17], s28, v237
	v_max_f32_e32 v234, v234, v238
	v_cmp_ngt_f32_e64 s[14:15], s28, v233
	v_min_f32_e32 v44, v214, v44
	v_min_f32_e32 v38, v46, v38
	v_min_f32_e32 v42, v42, v43
	v_min_f32_e32 v35, v40, v35
	v_max_f32_e32 v214, v228, v235
	v_max_f32_e32 v36, v37, v36
	v_max_f32_e32 v224, v223, v221
	v_min_f32_e32 v250, v246, v249
	v_min_f32_e32 v39, v226, v39
	v_min_f32_e32 v45, v45, v219
	v_min_f32_e32 v41, v41, v215
	v_cndmask_b32_e64 v236, v199, v237, s[16:17]
	v_cndmask_b32_e64 v238, v199, v233, s[14:15]
	v_max_f32_e32 v46, v44, v38
	v_max_f32_e32 v40, v42, v35
	v_min_f32_e32 v228, v214, v33
	v_min_f32_e32 v37, v36, v32
	v_max_f32_e32 v224, v224, v250
	v_max_f32_e32 v226, v47, v39
	v_max_f32_e32 v215, v45, v41
	v_min_f32_e32 v240, v230, v236
	v_min_f32_e32 v250, v234, v238
	v_min_f32_e32 v218, v225, v218
	v_min_f32_e32 v222, v227, v222
	v_max_f32_e32 v237, v241, v237
	v_max_f32_e32 v233, v243, v233
	v_min_f32_e32 v39, v47, v39
	v_min_f32_e32 v41, v45, v41
	v_max_f32_e32 v47, v230, v236
	v_max_f32_e32 v230, v234, v238
	v_max_f32_e32 v43, v46, v40
	v_min_f32_e32 v235, v228, v37
	v_min_f32_e32 v217, v220, v217
	v_min_f32_e32 v54, v216, v54
	v_max_f32_e32 v239, v239, v245
	v_max_f32_e32 v243, v247, v248
	v_min_f32_e32 v38, v44, v38
	v_min_f32_e32 v35, v42, v35
	v_max_f32_e32 v33, v214, v33
	v_max_f32_e32 v32, v36, v32
	v_max_f32_e32 v219, v226, v215
	v_max_f32_e32 v227, v218, v222
	v_min_f32_e32 v241, v237, v233
	v_max_f32_e32 v45, v39, v41
	v_min_f32_e32 v234, v47, v230
	v_min_f32_e32 v229, v229, v231
	v_max_f32_e32 v231, v242, v244
	v_min_f32_e32 v215, v226, v215
	v_max_f32_e32 v226, v240, v250
	v_min_f32_e32 v251, v240, v250
	v_max_f32_e32 v43, v43, v235
	v_max_f32_e32 v216, v217, v54
	v_min_f32_e32 v245, v239, v243
	v_max_f32_e32 v42, v38, v35
	v_min_f32_e32 v36, v33, v32
	v_min_f32_e32 v221, v223, v221
	v_max_f32_e32 v223, v246, v249
	v_min_f32_e32 v40, v46, v40
	v_max_f32_e32 v37, v228, v37
	v_min_f32_e32 v218, v218, v222
	v_max_f32_e32 v222, v237, v233
	v_min_f32_e32 v54, v217, v54
	v_max_f32_e32 v217, v239, v243
	v_min_f32_e32 v39, v39, v41
	v_max_f32_e32 v41, v47, v230
	v_min_f32_e32 v35, v38, v35
	v_max_f32_e32 v32, v33, v32
	v_max_f32_e32 v227, v227, v241
	v_max_f32_e32 v45, v45, v234
	v_max_f32_e32 v229, v229, v231
	v_max_f32_e32 v215, v215, v226
	v_max_f32_e32 v61, v48, v56
	v_max_f32_e32 v182, v34, v53
	v_max_f32_e32 v219, v219, v251
	v_max_f32_e32 v216, v216, v245
	v_max_f32_e32 v36, v42, v36
	v_max_f32_e32 v221, v221, v223
	v_max_f32_e32 v37, v40, v37
	v_max_f32_e32 v218, v218, v222
	v_max_f32_e32 v217, v54, v217
	v_max_f32_e32 v39, v39, v41
	v_max_f32_e32 v32, v35, v32
	v_max_f32_e32 v49, v50, v52
	v_max_f32_e32 v56, v55, v61
	v_max_f32_e32 v58, v63, v178
	v_max_f32_e32 v60, v180, v182
	v_max_f32_e32 v62, v183, v190
	v_max_f32_e32 v173, v195, v209
	v_max_f32_e32 v179, v210, v211
	v_max_f32_e32 v181, v212, v213
	v_min_f32_e32 v225, v232, v224
	v_min_f32_e32 v241, v219, v43
	v_min_f32_e32 v245, v227, v216
	v_min_f32_e32 v42, v45, v36
	v_min_f32_e32 v223, v229, v221
	v_min_f32_e32 v40, v215, v37
	v_min_f32_e32 v222, v218, v217
	v_min_f32_e32 v33, v39, v32
	v_max_f32_e32 v48, v49, v56
	v_max_f32_e32 v53, v58, v60
	v_max_f32_e32 v57, v62, v173
	v_max_f32_e32 v59, v179, v181
	v_min_f32_e32 v220, v225, v241
	v_min_f32_e32 v44, v245, v42
	v_min_f32_e32 v46, v223, v40
	v_min_f32_e32 v35, v222, v33
	v_max_f32_e32 v34, v48, v53
	v_max_f32_e32 v51, v57, v59
	v_min_f32_e32 v214, v220, v44
	v_min_f32_e32 v38, v46, v35
	v_min_f32_e32 v47, v55, v61
	v_max_f32_e32 v235, v34, v51
	v_min_f32_e32 v41, v214, v38
	v_min_f32_e32 v61, v63, v178
	v_min_f32_e32 v63, v180, v182
	v_max_f32_e32 v54, v235, v41
	v_min_f32_e32 v41, v50, v52
	v_min_f32_e32 v182, v183, v190
	v_min_f32_e32 v183, v195, v209
	v_min_f32_e32 v190, v210, v211
	v_min_f32_e32 v209, v212, v213
	v_max_f32_e32 v212, v232, v224
	v_max_f32_e32 v43, v219, v43
	v_max_f32_e32 v216, v227, v216
	v_max_f32_e32 v36, v45, v36
	v_max_f32_e32 v221, v229, v221
	v_max_f32_e32 v37, v215, v37
	v_max_f32_e32 v217, v218, v217
	v_max_f32_e32 v32, v39, v32
	v_min_f32_e32 v49, v49, v56
	v_min_f32_e32 v224, v58, v60
	v_min_f32_e32 v62, v62, v173
	v_min_f32_e32 v173, v179, v181
	v_max_f32_e32 v181, v225, v241
	v_max_f32_e32 v42, v245, v42
	v_max_f32_e32 v40, v223, v40
	v_max_f32_e32 v33, v222, v33
	v_max_f32_e32 v50, v41, v47
	v_max_f32_e32 v178, v61, v63
	v_max_f32_e32 v195, v182, v183
	v_min_f32_e32 v213, v212, v43
	v_min_f32_e32 v45, v216, v36
	v_min_f32_e32 v215, v221, v37
	v_min_f32_e32 v39, v217, v32
	v_max_f32_e32 v226, v49, v224
	v_max_f32_e32 v179, v62, v173
	v_min_f32_e32 v225, v181, v42
	v_min_f32_e32 v222, v40, v33
	v_min_f32_e32 v41, v41, v47
	v_min_f32_e32 v47, v61, v63
	v_min_f32_e32 v63, v182, v183
	v_min_f32_e32 v182, v190, v209
	v_max_f32_e32 v43, v212, v43
	v_max_f32_e32 v36, v216, v36
	v_max_f32_e32 v37, v221, v37
	v_max_f32_e32 v32, v217, v32
	v_cmp_gt_f32_e64 s[24:25], v63, v182
	v_max_f32_e32 v210, v190, v209
	v_max_f32_e32 v56, v226, v179
	v_min_f32_e32 v58, v225, v222
	v_max_f32_e32 v223, v41, v47
	v_cndmask_b32_e64 v183, v182, v63, s[24:25]
	v_min_f32_e32 v209, v43, v36
	v_min_f32_e32 v212, v37, v32
	v_max_f32_e32 v56, v56, v58
	v_max_f32_e32 v58, v223, v183
	v_min_f32_e32 v60, v209, v212
	v_min_f32_e32 v48, v48, v53
	v_min_f32_e32 v217, v57, v59
	v_max_f32_e32 v44, v220, v44
	v_max_f32_e32 v35, v46, v35
	v_max_f32_e32 v58, v58, v60
	v_max_f32_e32 v53, v48, v217
	v_min_f32_e32 v46, v44, v35
	v_max_f32_e32 v180, v50, v178
	v_min_f32_e32 v219, v213, v45
	v_min_f32_e32 v218, v215, v39
	v_max_f32_e32 v59, v53, v46
	v_min_f32_e32 v46, v50, v178
	v_min_f32_e32 v50, v195, v210
	v_max_f32_e32 v45, v213, v45
	v_max_f32_e32 v39, v215, v39
	v_min_f32_e32 v49, v49, v224
	v_max_f32_e32 v53, v46, v50
	v_min_f32_e32 v57, v45, v39
	v_min_f32_e32 v213, v62, v173
	v_max_f32_e32 v42, v181, v42
	v_max_f32_e32 v33, v40, v33
	v_max_f32_e32 v60, v53, v57
	v_cmp_gt_f32_e64 s[20:21], v49, v213
	v_max_f32_e32 v211, v195, v210
	s_nop 0
	v_cndmask_b32_e64 v57, v213, v49, s[20:21]
	v_min_f32_e32 v40, v42, v33
	v_max_f32_e32 v36, v43, v36
	v_max_f32_e32 v32, v37, v32
	v_max_f32_e32 v61, v57, v40
	v_min_f32_e32 v40, v41, v47
	v_cndmask_b32_e64 v41, v63, v182, s[24:25]
	v_cmp_gt_f32_e64 s[14:15], v40, v41
	v_min_f32_e32 v34, v34, v51
	s_nop 0
	v_cndmask_b32_e64 v47, v41, v40, s[14:15]
	v_min_f32_e32 v37, v36, v32
	s_mov_b64 s[96:97], s[6:7]
	v_max_f32_e32 v62, v47, v37
	v_max_f32_e32 v37, v214, v38
	v_max_f32_e32 v35, v44, v35
	v_min_f32_e32 v55, v219, v218
	v_max_f32_e32 v63, v34, v37
	v_min_f32_e32 v34, v180, v211
	v_max_f32_e32 v37, v219, v218
	v_max_f32_e32 v52, v180, v211
	v_max_f32_e32 v33, v42, v33
	v_max_f32_e32 v173, v34, v37
	v_min_f32_e32 v34, v226, v179
	v_max_f32_e32 v37, v225, v222
	v_max_f32_e32 v32, v36, v32
	v_max_f32_e32 v178, v34, v37
	v_min_f32_e32 v34, v223, v183
	v_max_f32_e32 v37, v209, v212
	v_max_f32_e32 v55, v52, v55
	v_max_f32_e32 v179, v34, v37
	v_min_f32_e32 v34, v48, v217
	v_max_f32_e32 v180, v34, v35
	v_min_f32_e32 v34, v46, v50
	v_max_f32_e32 v35, v45, v39
	v_max_f32_e32 v181, v34, v35
	v_cndmask_b32_e64 v34, v49, v213, s[20:21]
	v_max_f32_e32 v182, v34, v33
	v_cndmask_b32_e64 v33, v40, v41, s[14:15]
	v_min_f32_e32 v52, v54, v55
	v_min_f32_e32 v190, v56, v58
	v_max_f32_e32 v183, v33, v32
	v_min_f32_e32 v53, v59, v60
	v_min_f32_e32 v57, v61, v62
	v_min_f32_e32 v195, v63, v173
	v_min_f32_e32 v209, v178, v179
	v_min_f32_e32 v210, v180, v181
	v_min_f32_e32 v211, v182, v183
	v_min_f32_e32 v216, v52, v190
	v_min_f32_e32 v215, v53, v57
	v_min_f32_e32 v51, v195, v209
	v_min_f32_e32 v50, v210, v211
	s_movk_i32 s10, 0xff
	v_min_f32_e32 v220, v216, v215
	v_min_f32_e32 v212, v51, v50
	s_movk_i32 s8, 0x7f
	v_bitop3_b32 v35, v31, s8, v31 bitop3:0xc
	v_min_f32_e32 v32, v220, v212
	v_and_b32_e32 v33, 0xff, v32
	v_bitop3_b32 v34, v32, s10, v32 bitop3:0xc
	v_cmp_gt_i32_e64 s[6:7], 0, v32
	v_readlane_b32 s94, v255, 39
	v_readlane_b32 s95, v255, 40
	v_cndmask_b32_e64 v213, v34, v33, s[6:7]
	v_and_b32_e32 v33, 0x7f, v31
	v_cmp_gt_i32_e64 s[6:7], 0, v31
	v_and_b32_e32 v34, 15, v213
	v_lshrrev_b32_e32 v214, 4, v213
	v_cndmask_b32_e64 v31, v35, v33, s[6:7]
	v_and_b32_e32 v33, 0x7f, v30
	v_bitop3_b32 v35, v30, s8, v30 bitop3:0xc
	v_cmp_gt_i32_e64 s[6:7], 0, v30
	v_readlane_b32 s86, v255, 31
	v_readlane_b32 s82, v255, 33
	v_cndmask_b32_e64 v30, v35, v33, s[6:7]
	v_and_b32_e32 v33, 0x7f, v29
	v_bitop3_b32 v35, v29, s8, v29 bitop3:0xc
	v_cmp_gt_i32_e64 s[6:7], 0, v29
	v_readlane_b32 s84, v255, 25
	v_readlane_b32 s87, v255, 32
	v_cndmask_b32_e64 v29, v35, v33, s[6:7]
	v_and_b32_e32 v33, 0x7f, v28
	v_bitop3_b32 v35, v28, s8, v28 bitop3:0xc
	v_cmp_gt_i32_e64 s[6:7], 0, v28
	v_readlane_b32 s92, v255, 35
	v_readlane_b32 s88, v255, 29
	v_cndmask_b32_e64 v28, v35, v33, s[6:7]
	v_and_b32_e32 v33, 0x7f, v27
	v_bitop3_b32 v35, v27, s8, v27 bitop3:0xc
	v_cmp_gt_i32_e64 s[6:7], 0, v27
	v_readlane_b32 s90, v255, 27
	v_readlane_b32 s78, v255, 13
	v_cndmask_b32_e64 v27, v35, v33, s[6:7]
	v_and_b32_e32 v33, 0x7f, v26
	v_bitop3_b32 v35, v26, s8, v26 bitop3:0xc
	v_cmp_gt_i32_e64 s[6:7], 0, v26
	v_readlane_b32 s83, v255, 34
	v_readlane_b32 s74, v255, 9
	v_cndmask_b32_e64 v26, v35, v33, s[6:7]
	v_and_b32_e32 v33, 0x7f, v25
	v_bitop3_b32 v35, v25, s8, v25 bitop3:0xc
	v_cmp_gt_i32_e64 s[6:7], 0, v25
	v_readlane_b32 s85, v255, 26
	v_readlane_b32 s76, v255, 11
	v_cndmask_b32_e64 v25, v35, v33, s[6:7]
	v_and_b32_e32 v33, 0x7f, v24
	v_bitop3_b32 v35, v24, s8, v24 bitop3:0xc
	v_cmp_gt_i32_e64 s[6:7], 0, v24
	v_readlane_b32 s22, v255, 23
	v_readlane_b32 s34, v255, 17
	v_cndmask_b32_e64 v24, v35, v33, s[6:7]
	v_and_b32_e32 v33, 0x7f, v23
	v_bitop3_b32 v35, v23, s8, v23 bitop3:0xc
	v_cmp_gt_i32_e64 s[6:7], 0, v23
	v_readlane_b32 s30, v255, 15
	v_readlane_b32 s81, v255, 41
	v_cndmask_b32_e64 v23, v35, v33, s[6:7]
	v_and_b32_e32 v33, 0x7f, v22
	v_bitop3_b32 v35, v22, s8, v22 bitop3:0xc
	v_cmp_gt_i32_e64 s[6:7], 0, v22
	s_movk_i32 s87, 0x4000
	v_readlane_b32 s93, v255, 36
	v_cndmask_b32_e64 v22, v35, v33, s[6:7]
	v_and_b32_e32 v33, 0x7f, v21
	v_bitop3_b32 v35, v21, s8, v21 bitop3:0xc
	v_cmp_gt_i32_e64 s[6:7], 0, v21
	v_readlane_b32 s89, v255, 30
	v_readlane_b32 s91, v255, 28
	v_cndmask_b32_e64 v21, v35, v33, s[6:7]
	v_and_b32_e32 v33, 0x7f, v20
	v_bitop3_b32 v35, v20, s8, v20 bitop3:0xc
	v_cmp_gt_i32_e64 s[6:7], 0, v20
	v_readlane_b32 s79, v255, 14
	v_readlane_b32 s83, v255, 37
	v_cndmask_b32_e64 v20, v35, v33, s[6:7]
	v_and_b32_e32 v33, 0x7f, v19
	v_bitop3_b32 v35, v19, s8, v19 bitop3:0xc
	v_cmp_gt_i32_e64 s[6:7], 0, v19
	v_readlane_b32 s75, v255, 10
	v_readlane_b32 s85, v255, 38
	v_cndmask_b32_e64 v19, v35, v33, s[6:7]
	v_and_b32_e32 v33, 0x7f, v18
	v_bitop3_b32 v35, v18, s8, v18 bitop3:0xc
	v_cmp_gt_i32_e64 s[6:7], 0, v18
	v_readlane_b32 s77, v255, 12
	v_readlane_b32 s23, v255, 24
	v_cndmask_b32_e64 v18, v35, v33, s[6:7]
	v_and_b32_e32 v33, 0x7f, v17
	v_bitop3_b32 v35, v17, s8, v17 bitop3:0xc
	v_cmp_gt_i32_e64 s[6:7], 0, v17
	s_mov_b32 s18, s36
	s_movk_i32 s27, 0x1200
	v_cndmask_b32_e64 v17, v35, v33, s[6:7]
	v_and_b32_e32 v33, 0x7f, v16
	v_bitop3_b32 v35, v16, s8, v16 bitop3:0xc
	v_cmp_gt_i32_e64 s[6:7], 0, v16
	v_readlane_b32 s35, v255, 18
	v_readlane_b32 s31, v255, 16
	v_cndmask_b32_e64 v33, v35, v33, s[6:7]
	v_cmp_eq_u32_e64 s[6:7], 0, v34
	v_bitop3_b32 v35, v15, s8, v15 bitop3:0xc
	s_nop 0
	v_cndmask_b32_e64 v16, 0, v33, s[6:7]
	v_cmp_eq_u32_e64 s[6:7], 1, v34
	s_nop 1
	v_cndmask_b32_e64 v16, v16, v17, s[6:7]
	v_cmp_eq_u32_e64 s[6:7], 2, v34
	s_nop 1
	v_cndmask_b32_e64 v16, v16, v18, s[6:7]
	v_cmp_eq_u32_e64 s[6:7], 3, v34
	s_nop 1
	v_cndmask_b32_e64 v16, v16, v19, s[6:7]
	v_cmp_eq_u32_e64 s[6:7], 4, v34
	s_nop 1
	v_cndmask_b32_e64 v16, v16, v20, s[6:7]
	v_cmp_eq_u32_e64 s[6:7], 5, v34
	s_nop 1
	v_cndmask_b32_e64 v16, v16, v21, s[6:7]
	v_cmp_eq_u32_e64 s[6:7], 6, v34
	s_nop 1
	v_cndmask_b32_e64 v16, v16, v22, s[6:7]
	v_cmp_eq_u32_e64 s[6:7], 7, v34
	s_nop 1
	v_cndmask_b32_e64 v16, v16, v23, s[6:7]
	v_cmp_eq_u32_e64 s[6:7], 8, v34
	s_nop 1
	v_cndmask_b32_e64 v16, v16, v24, s[6:7]
	v_cmp_eq_u32_e64 s[6:7], 9, v34
	s_nop 1
	v_cndmask_b32_e64 v16, v16, v25, s[6:7]
	v_cmp_eq_u32_e64 s[6:7], 10, v34
	s_nop 1
	v_cndmask_b32_e64 v16, v16, v26, s[6:7]
	v_cmp_eq_u32_e64 s[6:7], 11, v34
	s_nop 1
	v_cndmask_b32_e64 v16, v16, v27, s[6:7]
	v_cmp_eq_u32_e64 s[6:7], 12, v34
	s_nop 1
	v_cndmask_b32_e64 v16, v16, v28, s[6:7]
	v_cmp_eq_u32_e64 s[6:7], 13, v34
	s_nop 1
	v_cndmask_b32_e64 v16, v16, v29, s[6:7]
	v_cmp_eq_u32_e64 s[6:7], 14, v34
	s_nop 1
	v_cndmask_b32_e64 v16, v16, v30, s[6:7]
	v_cmp_eq_u32_e64 s[6:7], 15, v34
	v_and_b32_e32 v34, 0x7f, v15
	s_nop 0
	v_cndmask_b32_e64 v16, v16, v31, s[6:7]
	v_cmp_gt_i32_e64 s[6:7], 0, v15
	v_and_b32_e32 v15, 0x7f, v14
	s_nop 0
	v_cndmask_b32_e64 v34, v35, v34, s[6:7]
	v_bitop3_b32 v35, v14, s8, v14 bitop3:0xc
	v_cmp_gt_i32_e64 s[6:7], 0, v14
	v_and_b32_e32 v14, 0x7f, v13
	s_nop 0
	v_cndmask_b32_e64 v35, v35, v15, s[6:7]
	v_bitop3_b32 v15, v13, s8, v13 bitop3:0xc
	v_cmp_gt_i32_e64 s[6:7], 0, v13
	v_and_b32_e32 v13, 0x7f, v12
	s_nop 0
	v_cndmask_b32_e64 v36, v15, v14, s[6:7]
	v_bitop3_b32 v14, v12, s8, v12 bitop3:0xc
	v_cmp_gt_i32_e64 s[6:7], 0, v12
	v_and_b32_e32 v12, 0x7f, v11
	v_max_f32_e32 v15, v59, v60
	v_cndmask_b32_e64 v37, v14, v13, s[6:7]
	v_bitop3_b32 v13, v11, s8, v11 bitop3:0xc
	v_cmp_gt_i32_e64 s[6:7], 0, v11
	v_and_b32_e32 v11, 0x7f, v10
	v_max_f32_e32 v14, v56, v58
	v_cndmask_b32_e64 v38, v13, v12, s[6:7]
	v_bitop3_b32 v12, v10, s8, v10 bitop3:0xc
	v_cmp_gt_i32_e64 s[6:7], 0, v10
	v_and_b32_e32 v10, 0x7f, v9
	v_max_f32_e32 v59, v61, v62
	v_cndmask_b32_e64 v39, v12, v11, s[6:7]
	v_bitop3_b32 v11, v9, s8, v9 bitop3:0xc
	v_cmp_gt_i32_e64 s[6:7], 0, v9
	v_and_b32_e32 v9, 0x7f, v8
	v_max_f32_e32 v60, v63, v173
	v_cndmask_b32_e64 v40, v11, v10, s[6:7]
	v_bitop3_b32 v10, v8, s8, v8 bitop3:0xc
	v_cmp_gt_i32_e64 s[6:7], 0, v8
	v_and_b32_e32 v8, 0x7f, v7
	v_max_f32_e32 v61, v178, v179
	v_cndmask_b32_e64 v41, v10, v9, s[6:7]
	v_bitop3_b32 v9, v7, s8, v7 bitop3:0xc
	v_cmp_gt_i32_e64 s[6:7], 0, v7
	v_and_b32_e32 v7, 0x7f, v6
	v_max_f32_e32 v62, v180, v181
	v_cndmask_b32_e64 v42, v9, v8, s[6:7]
	v_bitop3_b32 v8, v6, s8, v6 bitop3:0xc
	v_cmp_gt_i32_e64 s[6:7], 0, v6
	v_and_b32_e32 v6, 0x7f, v5
	v_max_f32_e32 v9, v210, v211
	v_cndmask_b32_e64 v43, v8, v7, s[6:7]
	v_bitop3_b32 v7, v5, s8, v5 bitop3:0xc
	v_cmp_gt_i32_e64 s[6:7], 0, v5
	v_and_b32_e32 v5, 0x7f, v4
	v_max_f32_e32 v8, v195, v209
	v_cndmask_b32_e64 v44, v7, v6, s[6:7]
	v_bitop3_b32 v6, v4, s8, v4 bitop3:0xc
	v_cmp_gt_i32_e64 s[6:7], 0, v4
	v_and_b32_e32 v4, 0x7f, v3
	v_max_f32_e32 v63, v182, v183
	v_cndmask_b32_e64 v45, v6, v5, s[6:7]
	v_bitop3_b32 v5, v3, s8, v3 bitop3:0xc
	v_cmp_gt_i32_e64 s[6:7], 0, v3
	v_and_b32_e32 v3, 0x7f, v2
	s_nop 0
	v_cndmask_b32_e64 v46, v5, v4, s[6:7]
	v_bitop3_b32 v4, v2, s8, v2 bitop3:0xc
	v_cmp_gt_i32_e64 s[6:7], 0, v2
	v_and_b32_e32 v2, 0x7f, v1
	s_nop 0
	v_cndmask_b32_e64 v47, v4, v3, s[6:7]
	v_bitop3_b32 v3, v1, s8, v1 bitop3:0xc
	v_cmp_gt_i32_e64 s[6:7], 0, v1
	v_and_b32_e32 v1, 0x7f, v0
	v_max_f32_e32 v4, v51, v50
	v_cndmask_b32_e64 v48, v3, v2, s[6:7]
	v_bitop3_b32 v2, v0, s8, v0 bitop3:0xc
	v_cmp_gt_i32_e64 s[6:7], 0, v0
	v_min_f32_e32 v56, v60, v61
	s_nop 0
	v_cndmask_b32_e64 v49, v2, v1, s[6:7]
	v_cmp_gt_u32_e64 s[6:7], 16, v213
	v_min_f32_e32 v58, v62, v63
	s_nop 0
	v_cndmask_b32_e64 v0, 0, v49, s[6:7]
	v_cmp_eq_u32_e64 s[6:7], 1, v214
	v_max_f32_e32 v60, v60, v61
	v_max_f32_e32 v61, v62, v63
	v_cndmask_b32_e64 v0, v0, v48, s[6:7]
	v_cmp_eq_u32_e64 s[6:7], 2, v214
	v_readlane_b32 s46, v255, 21
	v_readlane_b32 s44, v255, 19
	v_cndmask_b32_e64 v0, v0, v47, s[6:7]
	v_cmp_eq_u32_e64 s[6:7], 3, v214
	v_readlane_b32 s47, v255, 22
	v_readlane_b32 s45, v255, 20
	v_cndmask_b32_e64 v0, v0, v46, s[6:7]
	v_cmp_eq_u32_e64 s[6:7], 4, v214
	s_nop 1
	v_cndmask_b32_e64 v0, v0, v45, s[6:7]
	v_cmp_eq_u32_e64 s[6:7], 5, v214
	s_nop 1
	v_cndmask_b32_e64 v0, v0, v44, s[6:7]
	v_cmp_eq_u32_e64 s[6:7], 6, v214
	s_nop 1
	v_cndmask_b32_e64 v0, v0, v43, s[6:7]
	v_cmp_eq_u32_e64 s[6:7], 7, v214
	s_nop 1
	v_cndmask_b32_e64 v0, v0, v42, s[6:7]
	v_cmp_eq_u32_e64 s[6:7], 8, v214
	s_nop 1
	v_cndmask_b32_e64 v0, v0, v41, s[6:7]
	v_cmp_eq_u32_e64 s[6:7], 9, v214
	s_nop 1
	v_cndmask_b32_e64 v0, v0, v40, s[6:7]
	v_cmp_eq_u32_e64 s[6:7], 10, v214
	s_nop 1
	v_cndmask_b32_e64 v0, v0, v39, s[6:7]
	v_cmp_eq_u32_e64 s[6:7], 11, v214
	s_nop 1
	v_cndmask_b32_e64 v0, v0, v38, s[6:7]
	v_cmp_eq_u32_e64 s[6:7], 12, v214
	s_nop 1
	v_cndmask_b32_e64 v0, v0, v37, s[6:7]
	v_cmp_eq_u32_e64 s[6:7], 13, v214
	s_nop 1
	v_cndmask_b32_e64 v0, v0, v36, s[6:7]
	v_cmp_eq_u32_e64 s[6:7], 14, v214
	s_nop 1
	v_cndmask_b32_e64 v0, v0, v35, s[6:7]
	v_cmp_eq_u32_e64 s[6:7], 15, v214
	s_nop 1
	v_cndmask_b32_e64 v3, v0, v34, s[6:7]
	v_max_f32_e32 v0, v220, v212
	v_and_b32_e32 v1, 0xff, v0
	v_bitop3_b32 v2, v0, s10, v0 bitop3:0xc
	v_cmp_gt_i32_e64 s[6:7], 0, v0
	v_and_b32_e32 v12, 0xffffff00, v0
	v_lshl_add_u32 v3, v3, 7, v16
	v_cndmask_b32_e64 v0, v2, v1, s[6:7]
	v_lshrrev_b32_e32 v1, 4, v0
	v_cmp_gt_u32_e64 s[6:7], 16, v0
	v_and_b32_e32 v0, 15, v0
	s_nop 0
	v_cndmask_b32_e64 v2, 0, v49, s[6:7]
	v_cmp_eq_u32_e64 s[6:7], 1, v1
	s_nop 1
	v_cndmask_b32_e64 v2, v2, v48, s[6:7]
	v_cmp_eq_u32_e64 s[6:7], 2, v1
	s_nop 1
	v_cndmask_b32_e64 v2, v2, v47, s[6:7]
	v_cmp_eq_u32_e64 s[6:7], 3, v1
	s_nop 1
	v_cndmask_b32_e64 v2, v2, v46, s[6:7]
	v_cmp_eq_u32_e64 s[6:7], 4, v1
	s_nop 1
	v_cndmask_b32_e64 v2, v2, v45, s[6:7]
	v_cmp_eq_u32_e64 s[6:7], 5, v1
	s_nop 1
	v_cndmask_b32_e64 v2, v2, v44, s[6:7]
	v_cmp_eq_u32_e64 s[6:7], 6, v1
	s_nop 1
	v_cndmask_b32_e64 v2, v2, v43, s[6:7]
	v_cmp_eq_u32_e64 s[6:7], 7, v1
	s_nop 1
	v_cndmask_b32_e64 v2, v2, v42, s[6:7]
	v_cmp_eq_u32_e64 s[6:7], 8, v1
	s_nop 1
	v_cndmask_b32_e64 v2, v2, v41, s[6:7]
	v_cmp_eq_u32_e64 s[6:7], 9, v1
	s_nop 1
	v_cndmask_b32_e64 v2, v2, v40, s[6:7]
	v_cmp_eq_u32_e64 s[6:7], 10, v1
	s_nop 1
	v_cndmask_b32_e64 v2, v2, v39, s[6:7]
	v_cmp_eq_u32_e64 s[6:7], 11, v1
	s_nop 1
	v_cndmask_b32_e64 v2, v2, v38, s[6:7]
	v_cmp_eq_u32_e64 s[6:7], 12, v1
	s_nop 1
	v_cndmask_b32_e64 v2, v2, v37, s[6:7]
	v_cmp_eq_u32_e64 s[6:7], 13, v1
	s_nop 1
	v_cndmask_b32_e64 v2, v2, v36, s[6:7]
	v_cmp_eq_u32_e64 s[6:7], 14, v1
	s_nop 1
	v_cndmask_b32_e64 v2, v2, v35, s[6:7]
	v_cmp_eq_u32_e64 s[6:7], 15, v1
	s_nop 1
	v_cndmask_b32_e64 v1, v2, v34, s[6:7]
	v_cmp_eq_u32_e64 s[6:7], 0, v0
	s_nop 1
	v_cndmask_b32_e64 v2, 0, v33, s[6:7]
	v_cmp_eq_u32_e64 s[6:7], 1, v0
	s_nop 1
	v_cndmask_b32_e64 v2, v2, v17, s[6:7]
	v_cmp_eq_u32_e64 s[6:7], 2, v0
	s_nop 1
	v_cndmask_b32_e64 v2, v2, v18, s[6:7]
	v_cmp_eq_u32_e64 s[6:7], 3, v0
	s_nop 1
	v_cndmask_b32_e64 v2, v2, v19, s[6:7]
	v_cmp_eq_u32_e64 s[6:7], 4, v0
	s_nop 1
	v_cndmask_b32_e64 v2, v2, v20, s[6:7]
	v_cmp_eq_u32_e64 s[6:7], 5, v0
	s_nop 1
	v_cndmask_b32_e64 v2, v2, v21, s[6:7]
	v_cmp_eq_u32_e64 s[6:7], 6, v0
	s_nop 1
	v_cndmask_b32_e64 v2, v2, v22, s[6:7]
	v_cmp_eq_u32_e64 s[6:7], 7, v0
	s_nop 1
	v_cndmask_b32_e64 v2, v2, v23, s[6:7]
	v_cmp_eq_u32_e64 s[6:7], 8, v0
	s_nop 1
	v_cndmask_b32_e64 v2, v2, v24, s[6:7]
	v_cmp_eq_u32_e64 s[6:7], 9, v0
	s_nop 1
	v_cndmask_b32_e64 v2, v2, v25, s[6:7]
	v_cmp_eq_u32_e64 s[6:7], 10, v0
	s_nop 1
	v_cndmask_b32_e64 v2, v2, v26, s[6:7]
	v_cmp_eq_u32_e64 s[6:7], 11, v0
	s_nop 1
	v_cndmask_b32_e64 v2, v2, v27, s[6:7]
	v_cmp_eq_u32_e64 s[6:7], 12, v0
	s_nop 1
	v_cndmask_b32_e64 v2, v2, v28, s[6:7]
	v_cmp_eq_u32_e64 s[6:7], 13, v0
	s_nop 1
	v_cndmask_b32_e64 v2, v2, v29, s[6:7]
	v_cmp_eq_u32_e64 s[6:7], 14, v0
	s_nop 1
	v_cndmask_b32_e64 v2, v2, v30, s[6:7]
	v_cmp_eq_u32_e64 s[6:7], 15, v0
	s_nop 1
	v_cndmask_b32_e64 v0, v2, v31, s[6:7]
	v_lshl_add_u32 v2, v1, 7, v0
	v_max_f32_e32 v0, v216, v215
	v_min_f32_e32 v1, v0, v4
	v_and_b32_e32 v5, 0xff, v1
	v_bitop3_b32 v6, v1, s10, v1 bitop3:0xc
	v_cmp_gt_i32_e64 s[8:9], 0, v1
	v_and_b32_e32 v50, 0xffffff00, v1
	v_max_f32_e32 v0, v0, v4
	v_cndmask_b32_e64 v1, v6, v5, s[8:9]
	v_lshrrev_b32_e32 v5, 4, v1
	v_cmp_gt_u32_e64 s[8:9], 16, v1
	v_and_b32_e32 v1, 15, v1
	v_and_b32_e32 v4, 0xff, v0
	v_cndmask_b32_e64 v6, 0, v49, s[8:9]
	v_cmp_eq_u32_e64 s[8:9], 1, v5
	v_cmp_gt_i32_e64 s[6:7], 0, v0
	v_and_b32_e32 v51, 0xffffff00, v0
	v_cndmask_b32_e64 v6, v6, v48, s[8:9]
	v_cmp_eq_u32_e64 s[8:9], 2, v5
	s_nop 1
	v_cndmask_b32_e64 v6, v6, v47, s[8:9]
	v_cmp_eq_u32_e64 s[8:9], 3, v5
	s_nop 1
	v_cndmask_b32_e64 v6, v6, v46, s[8:9]
	v_cmp_eq_u32_e64 s[8:9], 4, v5
	s_nop 1
	v_cndmask_b32_e64 v6, v6, v45, s[8:9]
	v_cmp_eq_u32_e64 s[8:9], 5, v5
	s_nop 1
	v_cndmask_b32_e64 v6, v6, v44, s[8:9]
	v_cmp_eq_u32_e64 s[8:9], 6, v5
	s_nop 1
	v_cndmask_b32_e64 v6, v6, v43, s[8:9]
	v_cmp_eq_u32_e64 s[8:9], 7, v5
	s_nop 1
	v_cndmask_b32_e64 v6, v6, v42, s[8:9]
	v_cmp_eq_u32_e64 s[8:9], 8, v5
	s_nop 1
	v_cndmask_b32_e64 v6, v6, v41, s[8:9]
	v_cmp_eq_u32_e64 s[8:9], 9, v5
	s_nop 1
	v_cndmask_b32_e64 v6, v6, v40, s[8:9]
	v_cmp_eq_u32_e64 s[8:9], 10, v5
	s_nop 1
	v_cndmask_b32_e64 v6, v6, v39, s[8:9]
	v_cmp_eq_u32_e64 s[8:9], 11, v5
	s_nop 1
	v_cndmask_b32_e64 v6, v6, v38, s[8:9]
	v_cmp_eq_u32_e64 s[8:9], 12, v5
	s_nop 1
	v_cndmask_b32_e64 v6, v6, v37, s[8:9]
	v_cmp_eq_u32_e64 s[8:9], 13, v5
	s_nop 1
	v_cndmask_b32_e64 v6, v6, v36, s[8:9]
	v_cmp_eq_u32_e64 s[8:9], 14, v5
	s_nop 1
	v_cndmask_b32_e64 v6, v6, v35, s[8:9]
	v_cmp_eq_u32_e64 s[8:9], 15, v5
	s_nop 1
	v_cndmask_b32_e64 v5, v6, v34, s[8:9]
	v_cmp_eq_u32_e64 s[8:9], 0, v1
	s_nop 1
	v_cndmask_b32_e64 v6, 0, v33, s[8:9]
	v_cmp_eq_u32_e64 s[8:9], 1, v1
	s_nop 1
	v_cndmask_b32_e64 v6, v6, v17, s[8:9]
	v_cmp_eq_u32_e64 s[8:9], 2, v1
	s_nop 1
	v_cndmask_b32_e64 v6, v6, v18, s[8:9]
	v_cmp_eq_u32_e64 s[8:9], 3, v1
	s_nop 1
	v_cndmask_b32_e64 v6, v6, v19, s[8:9]
	v_cmp_eq_u32_e64 s[8:9], 4, v1
	s_nop 1
	v_cndmask_b32_e64 v6, v6, v20, s[8:9]
	v_cmp_eq_u32_e64 s[8:9], 5, v1
	s_nop 1
	v_cndmask_b32_e64 v6, v6, v21, s[8:9]
	v_cmp_eq_u32_e64 s[8:9], 6, v1
	s_nop 1
	v_cndmask_b32_e64 v6, v6, v22, s[8:9]
	v_cmp_eq_u32_e64 s[8:9], 7, v1
	s_nop 1
	v_cndmask_b32_e64 v6, v6, v23, s[8:9]
	v_cmp_eq_u32_e64 s[8:9], 8, v1
	s_nop 1
	v_cndmask_b32_e64 v6, v6, v24, s[8:9]
	v_cmp_eq_u32_e64 s[8:9], 9, v1
	s_nop 1
	v_cndmask_b32_e64 v6, v6, v25, s[8:9]
	v_cmp_eq_u32_e64 s[8:9], 10, v1
	s_nop 1
	v_cndmask_b32_e64 v6, v6, v26, s[8:9]
	v_cmp_eq_u32_e64 s[8:9], 11, v1
	s_nop 1
	v_cndmask_b32_e64 v6, v6, v27, s[8:9]
	v_cmp_eq_u32_e64 s[8:9], 12, v1
	s_nop 1
	v_cndmask_b32_e64 v6, v6, v28, s[8:9]
	v_cmp_eq_u32_e64 s[8:9], 13, v1
	s_nop 1
	v_cndmask_b32_e64 v6, v6, v29, s[8:9]
	v_cmp_eq_u32_e64 s[8:9], 14, v1
	s_nop 1
	v_cndmask_b32_e64 v6, v6, v30, s[8:9]
	v_cmp_eq_u32_e64 s[8:9], 15, v1
	s_nop 1
	v_cndmask_b32_e64 v1, v6, v31, s[8:9]
	v_lshl_add_u32 v1, v5, 7, v1
	v_bitop3_b32 v5, v0, s10, v0 bitop3:0xc
	v_cndmask_b32_e64 v0, v5, v4, s[6:7]
	v_lshrrev_b32_e32 v4, 4, v0
	v_cmp_gt_u32_e64 s[6:7], 16, v0
	v_and_b32_e32 v0, 15, v0
	s_nop 0
	v_cndmask_b32_e64 v5, 0, v49, s[6:7]
	v_cmp_eq_u32_e64 s[6:7], 1, v4
	s_nop 1
	v_cndmask_b32_e64 v5, v5, v48, s[6:7]
	v_cmp_eq_u32_e64 s[6:7], 2, v4
	s_nop 1
	v_cndmask_b32_e64 v5, v5, v47, s[6:7]
	v_cmp_eq_u32_e64 s[6:7], 3, v4
	s_nop 1
	v_cndmask_b32_e64 v5, v5, v46, s[6:7]
	v_cmp_eq_u32_e64 s[6:7], 4, v4
	s_nop 1
	v_cndmask_b32_e64 v5, v5, v45, s[6:7]
	v_cmp_eq_u32_e64 s[6:7], 5, v4
	s_nop 1
	v_cndmask_b32_e64 v5, v5, v44, s[6:7]
	v_cmp_eq_u32_e64 s[6:7], 6, v4
	s_nop 1
	v_cndmask_b32_e64 v5, v5, v43, s[6:7]
	v_cmp_eq_u32_e64 s[6:7], 7, v4
	s_nop 1
	v_cndmask_b32_e64 v5, v5, v42, s[6:7]
	v_cmp_eq_u32_e64 s[6:7], 8, v4
	s_nop 1
	v_cndmask_b32_e64 v5, v5, v41, s[6:7]
	v_cmp_eq_u32_e64 s[6:7], 9, v4
	s_nop 1
	v_cndmask_b32_e64 v5, v5, v40, s[6:7]
	v_cmp_eq_u32_e64 s[6:7], 10, v4
	s_nop 1
	v_cndmask_b32_e64 v5, v5, v39, s[6:7]
	v_cmp_eq_u32_e64 s[6:7], 11, v4
	s_nop 1
	v_cndmask_b32_e64 v5, v5, v38, s[6:7]
	v_cmp_eq_u32_e64 s[6:7], 12, v4
	s_nop 1
	v_cndmask_b32_e64 v5, v5, v37, s[6:7]
	v_cmp_eq_u32_e64 s[6:7], 13, v4
	s_nop 1
	v_cndmask_b32_e64 v5, v5, v36, s[6:7]
	v_cmp_eq_u32_e64 s[6:7], 14, v4
	s_nop 1
	v_cndmask_b32_e64 v5, v5, v35, s[6:7]
	v_cmp_eq_u32_e64 s[6:7], 15, v4
	s_nop 1
	v_cndmask_b32_e64 v4, v5, v34, s[6:7]
	v_cmp_eq_u32_e64 s[6:7], 0, v0
	s_nop 1
	v_cndmask_b32_e64 v5, 0, v33, s[6:7]
	v_cmp_eq_u32_e64 s[6:7], 1, v0
	s_nop 1
	v_cndmask_b32_e64 v5, v5, v17, s[6:7]
	v_cmp_eq_u32_e64 s[6:7], 2, v0
	s_nop 1
	v_cndmask_b32_e64 v5, v5, v18, s[6:7]
	v_cmp_eq_u32_e64 s[6:7], 3, v0
	s_nop 1
	v_cndmask_b32_e64 v5, v5, v19, s[6:7]
	v_cmp_eq_u32_e64 s[6:7], 4, v0
	s_nop 1
	v_cndmask_b32_e64 v5, v5, v20, s[6:7]
	v_cmp_eq_u32_e64 s[6:7], 5, v0
	s_nop 1
	v_cndmask_b32_e64 v5, v5, v21, s[6:7]
	v_cmp_eq_u32_e64 s[6:7], 6, v0
	s_nop 1
	v_cndmask_b32_e64 v5, v5, v22, s[6:7]
	v_cmp_eq_u32_e64 s[6:7], 7, v0
	s_nop 1
	v_cndmask_b32_e64 v5, v5, v23, s[6:7]
	v_cmp_eq_u32_e64 s[6:7], 8, v0
	s_nop 1
	v_cndmask_b32_e64 v5, v5, v24, s[6:7]
	v_cmp_eq_u32_e64 s[6:7], 9, v0
	s_nop 1
	v_cndmask_b32_e64 v5, v5, v25, s[6:7]
	v_cmp_eq_u32_e64 s[6:7], 10, v0
	s_nop 1
	v_cndmask_b32_e64 v5, v5, v26, s[6:7]
	v_cmp_eq_u32_e64 s[6:7], 11, v0
	s_nop 1
	v_cndmask_b32_e64 v5, v5, v27, s[6:7]
	v_cmp_eq_u32_e64 s[6:7], 12, v0
	s_nop 1
	v_cndmask_b32_e64 v5, v5, v28, s[6:7]
	v_cmp_eq_u32_e64 s[6:7], 13, v0
	s_nop 1
	v_cndmask_b32_e64 v5, v5, v29, s[6:7]
	v_cmp_eq_u32_e64 s[6:7], 14, v0
	s_nop 1
	v_cndmask_b32_e64 v5, v5, v30, s[6:7]
	v_cmp_eq_u32_e64 s[6:7], 15, v0
	s_nop 1
	v_cndmask_b32_e64 v0, v5, v31, s[6:7]
	v_lshl_add_u32 v0, v4, 7, v0
	v_max_f32_e32 v4, v52, v190
	v_max_f32_e32 v5, v53, v57
	v_min_f32_e32 v6, v4, v5
	v_min_f32_e32 v10, v8, v9
	v_max_f32_e32 v4, v4, v5
	v_max_f32_e32 v8, v8, v9
	v_min_f32_e32 v7, v6, v10
	v_and_b32_e32 v11, 0xff, v7
	v_bitop3_b32 v13, v7, s10, v7 bitop3:0xc
	v_cmp_gt_i32_e64 s[8:9], 0, v7
	v_and_b32_e32 v52, 0xffffff00, v7
	v_max_f32_e32 v6, v6, v10
	v_cndmask_b32_e64 v7, v13, v11, s[8:9]
	v_lshrrev_b32_e32 v11, 4, v7
	v_cmp_gt_u32_e64 s[8:9], 16, v7
	v_and_b32_e32 v7, 15, v7
	v_and_b32_e32 v10, 0xff, v6
	v_cndmask_b32_e64 v13, 0, v49, s[8:9]
	v_cmp_eq_u32_e64 s[8:9], 1, v11
	v_cmp_gt_i32_e64 s[6:7], 0, v6
	v_and_b32_e32 v53, 0xffffff00, v6
	v_cndmask_b32_e64 v13, v13, v48, s[8:9]
	v_cmp_eq_u32_e64 s[8:9], 2, v11
	s_nop 1
	v_cndmask_b32_e64 v13, v13, v47, s[8:9]
	v_cmp_eq_u32_e64 s[8:9], 3, v11
	s_nop 1
	v_cndmask_b32_e64 v13, v13, v46, s[8:9]
	v_cmp_eq_u32_e64 s[8:9], 4, v11
	s_nop 1
	v_cndmask_b32_e64 v13, v13, v45, s[8:9]
	v_cmp_eq_u32_e64 s[8:9], 5, v11
	s_nop 1
	v_cndmask_b32_e64 v13, v13, v44, s[8:9]
	v_cmp_eq_u32_e64 s[8:9], 6, v11
	s_nop 1
	v_cndmask_b32_e64 v13, v13, v43, s[8:9]
	v_cmp_eq_u32_e64 s[8:9], 7, v11
	s_nop 1
	v_cndmask_b32_e64 v13, v13, v42, s[8:9]
	v_cmp_eq_u32_e64 s[8:9], 8, v11
	s_nop 1
	v_cndmask_b32_e64 v13, v13, v41, s[8:9]
	v_cmp_eq_u32_e64 s[8:9], 9, v11
	s_nop 1
	v_cndmask_b32_e64 v13, v13, v40, s[8:9]
	v_cmp_eq_u32_e64 s[8:9], 10, v11
	s_nop 1
	v_cndmask_b32_e64 v13, v13, v39, s[8:9]
	v_cmp_eq_u32_e64 s[8:9], 11, v11
	s_nop 1
	v_cndmask_b32_e64 v13, v13, v38, s[8:9]
	v_cmp_eq_u32_e64 s[8:9], 12, v11
	s_nop 1
	v_cndmask_b32_e64 v13, v13, v37, s[8:9]
	v_cmp_eq_u32_e64 s[8:9], 13, v11
	s_nop 1
	v_cndmask_b32_e64 v13, v13, v36, s[8:9]
	v_cmp_eq_u32_e64 s[8:9], 14, v11
	s_nop 1
	v_cndmask_b32_e64 v13, v13, v35, s[8:9]
	v_cmp_eq_u32_e64 s[8:9], 15, v11
	s_nop 1
	v_cndmask_b32_e64 v11, v13, v34, s[8:9]
	v_cmp_eq_u32_e64 s[8:9], 0, v7
	s_nop 1
	v_cndmask_b32_e64 v13, 0, v33, s[8:9]
	v_cmp_eq_u32_e64 s[8:9], 1, v7
	s_nop 1
	v_cndmask_b32_e64 v13, v13, v17, s[8:9]
	v_cmp_eq_u32_e64 s[8:9], 2, v7
	s_nop 1
	v_cndmask_b32_e64 v13, v13, v18, s[8:9]
	v_cmp_eq_u32_e64 s[8:9], 3, v7
	s_nop 1
	v_cndmask_b32_e64 v13, v13, v19, s[8:9]
	v_cmp_eq_u32_e64 s[8:9], 4, v7
	s_nop 1
	v_cndmask_b32_e64 v13, v13, v20, s[8:9]
	v_cmp_eq_u32_e64 s[8:9], 5, v7
	s_nop 1
	v_cndmask_b32_e64 v13, v13, v21, s[8:9]
	v_cmp_eq_u32_e64 s[8:9], 6, v7
	s_nop 1
	v_cndmask_b32_e64 v13, v13, v22, s[8:9]
	v_cmp_eq_u32_e64 s[8:9], 7, v7
	s_nop 1
	v_cndmask_b32_e64 v13, v13, v23, s[8:9]
	v_cmp_eq_u32_e64 s[8:9], 8, v7
	s_nop 1
	v_cndmask_b32_e64 v13, v13, v24, s[8:9]
	v_cmp_eq_u32_e64 s[8:9], 9, v7
	s_nop 1
	v_cndmask_b32_e64 v13, v13, v25, s[8:9]
	v_cmp_eq_u32_e64 s[8:9], 10, v7
	s_nop 1
	v_cndmask_b32_e64 v13, v13, v26, s[8:9]
	v_cmp_eq_u32_e64 s[8:9], 11, v7
	s_nop 1
	v_cndmask_b32_e64 v13, v13, v27, s[8:9]
	v_cmp_eq_u32_e64 s[8:9], 12, v7
	s_nop 1
	v_cndmask_b32_e64 v13, v13, v28, s[8:9]
	v_cmp_eq_u32_e64 s[8:9], 13, v7
	s_nop 1
	v_cndmask_b32_e64 v13, v13, v29, s[8:9]
	v_cmp_eq_u32_e64 s[8:9], 14, v7
	s_nop 1
	v_cndmask_b32_e64 v13, v13, v30, s[8:9]
	v_cmp_eq_u32_e64 s[8:9], 15, v7
	s_nop 1
	v_cndmask_b32_e64 v7, v13, v31, s[8:9]
	v_lshl_add_u32 v7, v11, 7, v7
	v_bitop3_b32 v11, v6, s10, v6 bitop3:0xc
	v_cndmask_b32_e64 v6, v11, v10, s[6:7]
	v_lshrrev_b32_e32 v10, 4, v6
	v_cmp_gt_u32_e64 s[6:7], 16, v6
	v_and_b32_e32 v6, 15, v6
	v_max_f32_e32 v13, v54, v55
	v_cndmask_b32_e64 v11, 0, v49, s[6:7]
	v_cmp_eq_u32_e64 s[6:7], 1, v10
	v_min_f32_e32 v55, v56, v58
	s_nop 0
	v_cndmask_b32_e64 v11, v11, v48, s[6:7]
	v_cmp_eq_u32_e64 s[6:7], 2, v10
	v_max_f32_e32 v58, v56, v58
	s_nop 0
	v_cndmask_b32_e64 v11, v11, v47, s[6:7]
	v_cmp_eq_u32_e64 s[6:7], 3, v10
	s_nop 1
	v_cndmask_b32_e64 v11, v11, v46, s[6:7]
	v_cmp_eq_u32_e64 s[6:7], 4, v10
	s_nop 1
	v_cndmask_b32_e64 v11, v11, v45, s[6:7]
	v_cmp_eq_u32_e64 s[6:7], 5, v10
	s_nop 1
	v_cndmask_b32_e64 v11, v11, v44, s[6:7]
	v_cmp_eq_u32_e64 s[6:7], 6, v10
	s_nop 1
	v_cndmask_b32_e64 v11, v11, v43, s[6:7]
	v_cmp_eq_u32_e64 s[6:7], 7, v10
	s_nop 1
	v_cndmask_b32_e64 v11, v11, v42, s[6:7]
	v_cmp_eq_u32_e64 s[6:7], 8, v10
	s_nop 1
	v_cndmask_b32_e64 v11, v11, v41, s[6:7]
	v_cmp_eq_u32_e64 s[6:7], 9, v10
	s_nop 1
	v_cndmask_b32_e64 v11, v11, v40, s[6:7]
	v_cmp_eq_u32_e64 s[6:7], 10, v10
	s_nop 1
	v_cndmask_b32_e64 v11, v11, v39, s[6:7]
	v_cmp_eq_u32_e64 s[6:7], 11, v10
	s_nop 1
	v_cndmask_b32_e64 v11, v11, v38, s[6:7]
	v_cmp_eq_u32_e64 s[6:7], 12, v10
	s_nop 1
	v_cndmask_b32_e64 v11, v11, v37, s[6:7]
	v_cmp_eq_u32_e64 s[6:7], 13, v10
	s_nop 1
	v_cndmask_b32_e64 v11, v11, v36, s[6:7]
	v_cmp_eq_u32_e64 s[6:7], 14, v10
	s_nop 1
	v_cndmask_b32_e64 v11, v11, v35, s[6:7]
	v_cmp_eq_u32_e64 s[6:7], 15, v10
	s_nop 1
	v_cndmask_b32_e64 v10, v11, v34, s[6:7]
	v_cmp_eq_u32_e64 s[6:7], 0, v6
	s_nop 1
	v_cndmask_b32_e64 v11, 0, v33, s[6:7]
	v_cmp_eq_u32_e64 s[6:7], 1, v6
	s_nop 1
	v_cndmask_b32_e64 v11, v11, v17, s[6:7]
	v_cmp_eq_u32_e64 s[6:7], 2, v6
	s_nop 1
	v_cndmask_b32_e64 v11, v11, v18, s[6:7]
	v_cmp_eq_u32_e64 s[6:7], 3, v6
	s_nop 1
	v_cndmask_b32_e64 v11, v11, v19, s[6:7]
	v_cmp_eq_u32_e64 s[6:7], 4, v6
	s_nop 1
	v_cndmask_b32_e64 v11, v11, v20, s[6:7]
	v_cmp_eq_u32_e64 s[6:7], 5, v6
	s_nop 1
	v_cndmask_b32_e64 v11, v11, v21, s[6:7]
	v_cmp_eq_u32_e64 s[6:7], 6, v6
	s_nop 1
	v_cndmask_b32_e64 v11, v11, v22, s[6:7]
	v_cmp_eq_u32_e64 s[6:7], 7, v6
	s_nop 1
	v_cndmask_b32_e64 v11, v11, v23, s[6:7]
	v_cmp_eq_u32_e64 s[6:7], 8, v6
	s_nop 1
	v_cndmask_b32_e64 v11, v11, v24, s[6:7]
	v_cmp_eq_u32_e64 s[6:7], 9, v6
	s_nop 1
	v_cndmask_b32_e64 v11, v11, v25, s[6:7]
	v_cmp_eq_u32_e64 s[6:7], 10, v6
	s_nop 1
	v_cndmask_b32_e64 v11, v11, v26, s[6:7]
	v_cmp_eq_u32_e64 s[6:7], 11, v6
	s_nop 1
	v_cndmask_b32_e64 v11, v11, v27, s[6:7]
	v_cmp_eq_u32_e64 s[6:7], 12, v6
	s_nop 1
	v_cndmask_b32_e64 v11, v11, v28, s[6:7]
	v_cmp_eq_u32_e64 s[6:7], 13, v6
	s_nop 1
	v_cndmask_b32_e64 v11, v11, v29, s[6:7]
	v_cmp_eq_u32_e64 s[6:7], 14, v6
	s_nop 1
	v_cndmask_b32_e64 v11, v11, v30, s[6:7]
	v_cmp_eq_u32_e64 s[6:7], 15, v6
	s_nop 1
	v_cndmask_b32_e64 v6, v11, v31, s[6:7]
	v_lshl_add_u32 v6, v10, 7, v6
	v_min_f32_e32 v5, v4, v8
	v_and_b32_e32 v9, 0xff, v5
	v_bitop3_b32 v10, v5, s10, v5 bitop3:0xc
	v_cmp_gt_i32_e64 s[8:9], 0, v5
	v_and_b32_e32 v57, 0xffffff00, v5
	v_max_f32_e32 v4, v4, v8
	v_cndmask_b32_e64 v5, v10, v9, s[8:9]
	v_lshrrev_b32_e32 v9, 4, v5
	v_cmp_gt_u32_e64 s[8:9], 16, v5
	v_and_b32_e32 v5, 15, v5
	v_and_b32_e32 v8, 0xff, v4
	v_cndmask_b32_e64 v10, 0, v49, s[8:9]
	v_cmp_eq_u32_e64 s[8:9], 1, v9
	v_cmp_gt_i32_e64 s[6:7], 0, v4
	v_and_b32_e32 v209, 0xffffff00, v4
	v_cndmask_b32_e64 v10, v10, v48, s[8:9]
	v_cmp_eq_u32_e64 s[8:9], 2, v9
	s_nop 1
	v_cndmask_b32_e64 v10, v10, v47, s[8:9]
	v_cmp_eq_u32_e64 s[8:9], 3, v9
	s_nop 1
	v_cndmask_b32_e64 v10, v10, v46, s[8:9]
	v_cmp_eq_u32_e64 s[8:9], 4, v9
	s_nop 1
	v_cndmask_b32_e64 v10, v10, v45, s[8:9]
	v_cmp_eq_u32_e64 s[8:9], 5, v9
	s_nop 1
	v_cndmask_b32_e64 v10, v10, v44, s[8:9]
	v_cmp_eq_u32_e64 s[8:9], 6, v9
	s_nop 1
	v_cndmask_b32_e64 v10, v10, v43, s[8:9]
	v_cmp_eq_u32_e64 s[8:9], 7, v9
	s_nop 1
	v_cndmask_b32_e64 v10, v10, v42, s[8:9]
	v_cmp_eq_u32_e64 s[8:9], 8, v9
	s_nop 1
	v_cndmask_b32_e64 v10, v10, v41, s[8:9]
	v_cmp_eq_u32_e64 s[8:9], 9, v9
	s_nop 1
	v_cndmask_b32_e64 v10, v10, v40, s[8:9]
	v_cmp_eq_u32_e64 s[8:9], 10, v9
	s_nop 1
	v_cndmask_b32_e64 v10, v10, v39, s[8:9]
	v_cmp_eq_u32_e64 s[8:9], 11, v9
	s_nop 1
	v_cndmask_b32_e64 v10, v10, v38, s[8:9]
	v_cmp_eq_u32_e64 s[8:9], 12, v9
	s_nop 1
	v_cndmask_b32_e64 v10, v10, v37, s[8:9]
	v_cmp_eq_u32_e64 s[8:9], 13, v9
	s_nop 1
	v_cndmask_b32_e64 v10, v10, v36, s[8:9]
	v_cmp_eq_u32_e64 s[8:9], 14, v9
	s_nop 1
	v_cndmask_b32_e64 v10, v10, v35, s[8:9]
	v_cmp_eq_u32_e64 s[8:9], 15, v9
	s_nop 1
	v_cndmask_b32_e64 v9, v10, v34, s[8:9]
	v_cmp_eq_u32_e64 s[8:9], 0, v5
	s_nop 1
	v_cndmask_b32_e64 v10, 0, v33, s[8:9]
	v_cmp_eq_u32_e64 s[8:9], 1, v5
	s_nop 1
	v_cndmask_b32_e64 v10, v10, v17, s[8:9]
	v_cmp_eq_u32_e64 s[8:9], 2, v5
	s_nop 1
	v_cndmask_b32_e64 v10, v10, v18, s[8:9]
	v_cmp_eq_u32_e64 s[8:9], 3, v5
	s_nop 1
	v_cndmask_b32_e64 v10, v10, v19, s[8:9]
	v_cmp_eq_u32_e64 s[8:9], 4, v5
	s_nop 1
	v_cndmask_b32_e64 v10, v10, v20, s[8:9]
	v_cmp_eq_u32_e64 s[8:9], 5, v5
	s_nop 1
	v_cndmask_b32_e64 v10, v10, v21, s[8:9]
	v_cmp_eq_u32_e64 s[8:9], 6, v5
	s_nop 1
	v_cndmask_b32_e64 v10, v10, v22, s[8:9]
	v_cmp_eq_u32_e64 s[8:9], 7, v5
	s_nop 1
	v_cndmask_b32_e64 v10, v10, v23, s[8:9]
	v_cmp_eq_u32_e64 s[8:9], 8, v5
	s_nop 1
	v_cndmask_b32_e64 v10, v10, v24, s[8:9]
	v_cmp_eq_u32_e64 s[8:9], 9, v5
	s_nop 1
	v_cndmask_b32_e64 v10, v10, v25, s[8:9]
	v_cmp_eq_u32_e64 s[8:9], 10, v5
	s_nop 1
	v_cndmask_b32_e64 v10, v10, v26, s[8:9]
	v_cmp_eq_u32_e64 s[8:9], 11, v5
	s_nop 1
	v_cndmask_b32_e64 v10, v10, v27, s[8:9]
	v_cmp_eq_u32_e64 s[8:9], 12, v5
	s_nop 1
	v_cndmask_b32_e64 v10, v10, v28, s[8:9]
	v_cmp_eq_u32_e64 s[8:9], 13, v5
	s_nop 1
	v_cndmask_b32_e64 v10, v10, v29, s[8:9]
	v_cmp_eq_u32_e64 s[8:9], 14, v5
	s_nop 1
	v_cndmask_b32_e64 v10, v10, v30, s[8:9]
	v_cmp_eq_u32_e64 s[8:9], 15, v5
	s_nop 1
	v_cndmask_b32_e64 v5, v10, v31, s[8:9]
	v_lshl_add_u32 v5, v9, 7, v5
	v_bitop3_b32 v9, v4, s10, v4 bitop3:0xc
	v_cndmask_b32_e64 v4, v9, v8, s[6:7]
	v_lshrrev_b32_e32 v8, 4, v4
	v_cmp_gt_u32_e64 s[6:7], 16, v4
	v_and_b32_e32 v4, 15, v4
	s_nop 0
	v_cndmask_b32_e64 v9, 0, v49, s[6:7]
	v_cmp_eq_u32_e64 s[6:7], 1, v8
	s_nop 1
	v_cndmask_b32_e64 v9, v9, v48, s[6:7]
	v_cmp_eq_u32_e64 s[6:7], 2, v8
	s_nop 1
	v_cndmask_b32_e64 v9, v9, v47, s[6:7]
	v_cmp_eq_u32_e64 s[6:7], 3, v8
	s_nop 1
	v_cndmask_b32_e64 v9, v9, v46, s[6:7]
	v_cmp_eq_u32_e64 s[6:7], 4, v8
	s_nop 1
	v_cndmask_b32_e64 v9, v9, v45, s[6:7]
	v_cmp_eq_u32_e64 s[6:7], 5, v8
	s_nop 1
	v_cndmask_b32_e64 v9, v9, v44, s[6:7]
	v_cmp_eq_u32_e64 s[6:7], 6, v8
	s_nop 1
	v_cndmask_b32_e64 v9, v9, v43, s[6:7]
	v_cmp_eq_u32_e64 s[6:7], 7, v8
	s_nop 1
	v_cndmask_b32_e64 v9, v9, v42, s[6:7]
	v_cmp_eq_u32_e64 s[6:7], 8, v8
	s_nop 1
	v_cndmask_b32_e64 v9, v9, v41, s[6:7]
	v_cmp_eq_u32_e64 s[6:7], 9, v8
	s_nop 1
	v_cndmask_b32_e64 v9, v9, v40, s[6:7]
	v_cmp_eq_u32_e64 s[6:7], 10, v8
	s_nop 1
	v_cndmask_b32_e64 v9, v9, v39, s[6:7]
	v_cmp_eq_u32_e64 s[6:7], 11, v8
	s_nop 1
	v_cndmask_b32_e64 v9, v9, v38, s[6:7]
	v_cmp_eq_u32_e64 s[6:7], 12, v8
	s_nop 1
	v_cndmask_b32_e64 v9, v9, v37, s[6:7]
	v_cmp_eq_u32_e64 s[6:7], 13, v8
	s_nop 1
	v_cndmask_b32_e64 v9, v9, v36, s[6:7]
	v_cmp_eq_u32_e64 s[6:7], 14, v8
	s_nop 1
	v_cndmask_b32_e64 v9, v9, v35, s[6:7]
	v_cmp_eq_u32_e64 s[6:7], 15, v8
	s_nop 1
	v_cndmask_b32_e64 v8, v9, v34, s[6:7]
	v_cmp_eq_u32_e64 s[6:7], 0, v4
	s_nop 1
	v_cndmask_b32_e64 v9, 0, v33, s[6:7]
	v_cmp_eq_u32_e64 s[6:7], 1, v4
	s_nop 1
	v_cndmask_b32_e64 v9, v9, v17, s[6:7]
	v_cmp_eq_u32_e64 s[6:7], 2, v4
	s_nop 1
	v_cndmask_b32_e64 v9, v9, v18, s[6:7]
	v_cmp_eq_u32_e64 s[6:7], 3, v4
	s_nop 1
	v_cndmask_b32_e64 v9, v9, v19, s[6:7]
	v_cmp_eq_u32_e64 s[6:7], 4, v4
	s_nop 1
	v_cndmask_b32_e64 v9, v9, v20, s[6:7]
	v_cmp_eq_u32_e64 s[6:7], 5, v4
	s_nop 1
	v_cndmask_b32_e64 v9, v9, v21, s[6:7]
	v_cmp_eq_u32_e64 s[6:7], 6, v4
	s_nop 1
	v_cndmask_b32_e64 v9, v9, v22, s[6:7]
	v_cmp_eq_u32_e64 s[6:7], 7, v4
	s_nop 1
	v_cndmask_b32_e64 v9, v9, v23, s[6:7]
	v_cmp_eq_u32_e64 s[6:7], 8, v4
	s_nop 1
	v_cndmask_b32_e64 v9, v9, v24, s[6:7]
	v_cmp_eq_u32_e64 s[6:7], 9, v4
	s_nop 1
	v_cndmask_b32_e64 v9, v9, v25, s[6:7]
	v_cmp_eq_u32_e64 s[6:7], 10, v4
	s_nop 1
	v_cndmask_b32_e64 v9, v9, v26, s[6:7]
	v_cmp_eq_u32_e64 s[6:7], 11, v4
	s_nop 1
	v_cndmask_b32_e64 v9, v9, v27, s[6:7]
	v_cmp_eq_u32_e64 s[6:7], 12, v4
	s_nop 1
	v_cndmask_b32_e64 v9, v9, v28, s[6:7]
	v_cmp_eq_u32_e64 s[6:7], 13, v4
	s_nop 1
	v_cndmask_b32_e64 v9, v9, v29, s[6:7]
	v_cmp_eq_u32_e64 s[6:7], 14, v4
	s_nop 1
	v_cndmask_b32_e64 v9, v9, v30, s[6:7]
	v_cmp_eq_u32_e64 s[6:7], 15, v4
	s_nop 1
	v_cndmask_b32_e64 v4, v9, v31, s[6:7]
	v_lshl_add_u32 v4, v8, 7, v4
	v_min_f32_e32 v8, v13, v14
	v_min_f32_e32 v9, v15, v59
	v_max_f32_e32 v13, v13, v14
	v_max_f32_e32 v59, v15, v59
	v_min_f32_e32 v10, v8, v9
	v_max_f32_e32 v8, v8, v9
	v_min_f32_e32 v11, v10, v55
	v_and_b32_e32 v173, 0xff, v11
	v_bitop3_b32 v178, v11, s10, v11 bitop3:0xc
	v_cmp_gt_i32_e64 s[8:9], 0, v11
	v_and_b32_e32 v54, 0xffffff00, v11
	v_max_f32_e32 v10, v10, v55
	v_cndmask_b32_e64 v11, v178, v173, s[8:9]
	v_lshrrev_b32_e32 v173, 4, v11
	v_cmp_gt_u32_e64 s[8:9], 16, v11
	v_and_b32_e32 v11, 15, v11
	v_cmp_gt_i32_e64 s[6:7], 0, v10
	v_cndmask_b32_e64 v178, 0, v49, s[8:9]
	v_cmp_eq_u32_e64 s[8:9], 1, v173
	v_and_b32_e32 v55, 0xffffff00, v10
	s_nop 0
	v_cndmask_b32_e64 v178, v178, v48, s[8:9]
	v_cmp_eq_u32_e64 s[8:9], 2, v173
	v_min_f32_e32 v14, v13, v59
	v_min_f32_e32 v62, v60, v61
	v_cndmask_b32_e64 v178, v178, v47, s[8:9]
	v_cmp_eq_u32_e64 s[8:9], 3, v173
	v_max_f32_e32 v59, v13, v59
	v_max_f32_e32 v60, v60, v61
	v_cndmask_b32_e64 v178, v178, v46, s[8:9]
	v_cmp_eq_u32_e64 s[8:9], 4, v173
	s_nop 0
	s_nop 0
	v_cndmask_b32_e64 v178, v178, v45, s[8:9]
	v_cmp_eq_u32_e64 s[8:9], 5, v173
	v_min_f32_e32 v13, v59, v60
	v_and_b32_e32 v61, 0xffffff00, v13
	v_cndmask_b32_e64 v178, v178, v44, s[8:9]
	v_cmp_eq_u32_e64 s[8:9], 6, v173
	v_max_f32_e32 v59, v59, v60
	v_cmp_gt_i32_e32 vcc, 0, v59
	v_cndmask_b32_e64 v178, v178, v43, s[8:9]
	v_cmp_eq_u32_e64 s[8:9], 7, v173
	v_and_b32_e32 v60, 0xffffff00, v59
	v_sub_f32_e32 v12, v12, v60
	v_cndmask_b32_e64 v178, v178, v42, s[8:9]
	v_cmp_eq_u32_e64 s[8:9], 8, v173
	v_mul_f32_e32 v12, 0x3fb8aa3b, v12
	s_nop 0
	v_cndmask_b32_e64 v178, v178, v41, s[8:9]
	v_cmp_eq_u32_e64 s[8:9], 9, v173
	s_nop 1
	v_cndmask_b32_e64 v178, v178, v40, s[8:9]
	v_cmp_eq_u32_e64 s[8:9], 10, v173
	s_nop 1
	v_cndmask_b32_e64 v178, v178, v39, s[8:9]
	v_cmp_eq_u32_e64 s[8:9], 11, v173
	s_nop 1
	v_cndmask_b32_e64 v178, v178, v38, s[8:9]
	v_cmp_eq_u32_e64 s[8:9], 12, v173
	s_nop 1
	v_cndmask_b32_e64 v178, v178, v37, s[8:9]
	v_cmp_eq_u32_e64 s[8:9], 13, v173
	s_nop 1
	v_cndmask_b32_e64 v178, v178, v36, s[8:9]
	v_cmp_eq_u32_e64 s[8:9], 14, v173
	s_nop 1
	v_cndmask_b32_e64 v178, v178, v35, s[8:9]
	v_cmp_eq_u32_e64 s[8:9], 15, v173
	s_nop 1
	v_cndmask_b32_e64 v173, v178, v34, s[8:9]
	v_cmp_eq_u32_e64 s[8:9], 0, v11
	s_nop 1
	v_cndmask_b32_e64 v178, 0, v33, s[8:9]
	v_cmp_eq_u32_e64 s[8:9], 1, v11
	s_nop 1
	v_cndmask_b32_e64 v178, v178, v17, s[8:9]
	v_cmp_eq_u32_e64 s[8:9], 2, v11
	s_nop 1
	v_cndmask_b32_e64 v178, v178, v18, s[8:9]
	v_cmp_eq_u32_e64 s[8:9], 3, v11
	s_nop 1
	v_cndmask_b32_e64 v178, v178, v19, s[8:9]
	v_cmp_eq_u32_e64 s[8:9], 4, v11
	s_nop 1
	v_cndmask_b32_e64 v178, v178, v20, s[8:9]
	v_cmp_eq_u32_e64 s[8:9], 5, v11
	s_nop 1
	v_cndmask_b32_e64 v178, v178, v21, s[8:9]
	v_cmp_eq_u32_e64 s[8:9], 6, v11
	s_nop 1
	v_cndmask_b32_e64 v178, v178, v22, s[8:9]
	v_cmp_eq_u32_e64 s[8:9], 7, v11
	s_nop 1
	v_cndmask_b32_e64 v178, v178, v23, s[8:9]
	v_cmp_eq_u32_e64 s[8:9], 8, v11
	s_nop 1
	v_cndmask_b32_e64 v178, v178, v24, s[8:9]
	v_cmp_eq_u32_e64 s[8:9], 9, v11
	s_nop 1
	v_cndmask_b32_e64 v178, v178, v25, s[8:9]
	v_cmp_eq_u32_e64 s[8:9], 10, v11
	s_nop 1
	v_cndmask_b32_e64 v178, v178, v26, s[8:9]
	v_cmp_eq_u32_e64 s[8:9], 11, v11
	s_nop 1
	v_cndmask_b32_e64 v178, v178, v27, s[8:9]
	v_cmp_eq_u32_e64 s[8:9], 12, v11
	s_nop 1
	v_cndmask_b32_e64 v178, v178, v28, s[8:9]
	v_cmp_eq_u32_e64 s[8:9], 13, v11
	s_nop 1
	v_cndmask_b32_e64 v178, v178, v29, s[8:9]
	v_cmp_eq_u32_e64 s[8:9], 14, v11
	s_nop 1
	v_cndmask_b32_e64 v178, v178, v30, s[8:9]
	v_cmp_eq_u32_e64 s[8:9], 15, v11
	s_nop 1
	v_cndmask_b32_e64 v11, v178, v31, s[8:9]
	v_lshl_add_u32 v11, v173, 7, v11
	v_and_b32_e32 v173, 0xff, v10
	v_bitop3_b32 v178, v10, s10, v10 bitop3:0xc
	v_cndmask_b32_e64 v10, v178, v173, s[6:7]
	v_lshrrev_b32_e32 v173, 4, v10
	v_cmp_gt_u32_e64 s[6:7], 16, v10
	v_and_b32_e32 v10, 15, v10
	s_nop 0
	v_cndmask_b32_e64 v178, 0, v49, s[6:7]
	v_cmp_eq_u32_e64 s[6:7], 1, v173
	s_nop 1
	v_cndmask_b32_e64 v178, v178, v48, s[6:7]
	v_cmp_eq_u32_e64 s[6:7], 2, v173
	s_nop 1
	v_cndmask_b32_e64 v178, v178, v47, s[6:7]
	v_cmp_eq_u32_e64 s[6:7], 3, v173
	s_nop 1
	v_cndmask_b32_e64 v178, v178, v46, s[6:7]
	v_cmp_eq_u32_e64 s[6:7], 4, v173
	s_nop 1
	v_cndmask_b32_e64 v178, v178, v45, s[6:7]
	v_cmp_eq_u32_e64 s[6:7], 5, v173
	s_nop 1
	v_cndmask_b32_e64 v178, v178, v44, s[6:7]
	v_cmp_eq_u32_e64 s[6:7], 6, v173
	s_nop 1
	v_cndmask_b32_e64 v178, v178, v43, s[6:7]
	v_cmp_eq_u32_e64 s[6:7], 7, v173
	s_nop 1
	v_cndmask_b32_e64 v178, v178, v42, s[6:7]
	v_cmp_eq_u32_e64 s[6:7], 8, v173
	s_nop 1
	v_cndmask_b32_e64 v178, v178, v41, s[6:7]
	v_cmp_eq_u32_e64 s[6:7], 9, v173
	s_nop 1
	v_cndmask_b32_e64 v178, v178, v40, s[6:7]
	v_cmp_eq_u32_e64 s[6:7], 10, v173
	s_nop 1
	v_cndmask_b32_e64 v178, v178, v39, s[6:7]
	v_cmp_eq_u32_e64 s[6:7], 11, v173
	s_nop 1
	v_cndmask_b32_e64 v178, v178, v38, s[6:7]
	v_cmp_eq_u32_e64 s[6:7], 12, v173
	s_nop 1
	v_cndmask_b32_e64 v178, v178, v37, s[6:7]
	v_cmp_eq_u32_e64 s[6:7], 13, v173
	s_nop 1
	v_cndmask_b32_e64 v178, v178, v36, s[6:7]
	v_cmp_eq_u32_e64 s[6:7], 14, v173
	s_nop 1
	v_cndmask_b32_e64 v178, v178, v35, s[6:7]
	v_cmp_eq_u32_e64 s[6:7], 15, v173
	s_nop 1
	v_cndmask_b32_e64 v173, v178, v34, s[6:7]
	v_cmp_eq_u32_e64 s[6:7], 0, v10
	s_nop 1
	v_cndmask_b32_e64 v178, 0, v33, s[6:7]
	v_cmp_eq_u32_e64 s[6:7], 1, v10
	s_nop 1
	v_cndmask_b32_e64 v178, v178, v17, s[6:7]
	v_cmp_eq_u32_e64 s[6:7], 2, v10
	s_nop 1
	v_cndmask_b32_e64 v178, v178, v18, s[6:7]
	v_cmp_eq_u32_e64 s[6:7], 3, v10
	s_nop 1
	v_cndmask_b32_e64 v178, v178, v19, s[6:7]
	v_cmp_eq_u32_e64 s[6:7], 4, v10
	s_nop 1
	v_cndmask_b32_e64 v178, v178, v20, s[6:7]
	v_cmp_eq_u32_e64 s[6:7], 5, v10
	s_nop 1
	v_cndmask_b32_e64 v178, v178, v21, s[6:7]
	v_cmp_eq_u32_e64 s[6:7], 6, v10
	s_nop 1
	v_cndmask_b32_e64 v178, v178, v22, s[6:7]
	v_cmp_eq_u32_e64 s[6:7], 7, v10
	s_nop 1
	v_cndmask_b32_e64 v178, v178, v23, s[6:7]
	v_cmp_eq_u32_e64 s[6:7], 8, v10
	s_nop 1
	v_cndmask_b32_e64 v178, v178, v24, s[6:7]
	v_cmp_eq_u32_e64 s[6:7], 9, v10
	s_nop 1
	v_cndmask_b32_e64 v178, v178, v25, s[6:7]
	v_cmp_eq_u32_e64 s[6:7], 10, v10
	s_nop 1
	v_cndmask_b32_e64 v178, v178, v26, s[6:7]
	v_cmp_eq_u32_e64 s[6:7], 11, v10
	s_nop 1
	v_cndmask_b32_e64 v178, v178, v27, s[6:7]
	v_cmp_eq_u32_e64 s[6:7], 12, v10
	s_nop 1
	v_cndmask_b32_e64 v178, v178, v28, s[6:7]
	v_cmp_eq_u32_e64 s[6:7], 13, v10
	s_nop 1
	v_cndmask_b32_e64 v178, v178, v29, s[6:7]
	v_cmp_eq_u32_e64 s[6:7], 14, v10
	s_nop 1
	v_cndmask_b32_e64 v178, v178, v30, s[6:7]
	v_cmp_eq_u32_e64 s[6:7], 15, v10
	s_nop 1
	v_cndmask_b32_e64 v10, v178, v31, s[6:7]
	v_lshl_add_u32 v10, v173, 7, v10
	v_min_f32_e32 v9, v8, v58
	v_and_b32_e32 v173, 0xff, v9
	v_bitop3_b32 v178, v9, s10, v9 bitop3:0xc
	v_cmp_gt_i32_e64 s[8:9], 0, v9
	v_and_b32_e32 v56, 0xffffff00, v9
	v_max_f32_e32 v8, v8, v58
	v_cndmask_b32_e64 v9, v178, v173, s[8:9]
	v_lshrrev_b32_e32 v173, 4, v9
	v_cmp_gt_u32_e64 s[8:9], 16, v9
	v_and_b32_e32 v9, 15, v9
	v_cmp_gt_i32_e64 s[6:7], 0, v8
	v_cndmask_b32_e64 v178, 0, v49, s[8:9]
	v_cmp_eq_u32_e64 s[8:9], 1, v173
	v_and_b32_e32 v58, 0xffffff00, v8
	s_nop 0
	v_cndmask_b32_e64 v178, v178, v48, s[8:9]
	v_cmp_eq_u32_e64 s[8:9], 2, v173
	s_nop 1
	v_cndmask_b32_e64 v178, v178, v47, s[8:9]
	v_cmp_eq_u32_e64 s[8:9], 3, v173
	s_nop 1
	v_cndmask_b32_e64 v178, v178, v46, s[8:9]
	v_cmp_eq_u32_e64 s[8:9], 4, v173
	s_nop 1
	v_cndmask_b32_e64 v178, v178, v45, s[8:9]
	v_cmp_eq_u32_e64 s[8:9], 5, v173
	s_nop 1
	v_cndmask_b32_e64 v178, v178, v44, s[8:9]
	v_cmp_eq_u32_e64 s[8:9], 6, v173
	s_nop 1
	v_cndmask_b32_e64 v178, v178, v43, s[8:9]
	v_cmp_eq_u32_e64 s[8:9], 7, v173
	s_nop 1
	v_cndmask_b32_e64 v178, v178, v42, s[8:9]
	v_cmp_eq_u32_e64 s[8:9], 8, v173
	s_nop 1
	v_cndmask_b32_e64 v178, v178, v41, s[8:9]
	v_cmp_eq_u32_e64 s[8:9], 9, v173
	s_nop 1
	v_cndmask_b32_e64 v178, v178, v40, s[8:9]
	v_cmp_eq_u32_e64 s[8:9], 10, v173
	s_nop 1
	v_cndmask_b32_e64 v178, v178, v39, s[8:9]
	v_cmp_eq_u32_e64 s[8:9], 11, v173
	s_nop 1
	v_cndmask_b32_e64 v178, v178, v38, s[8:9]
	v_cmp_eq_u32_e64 s[8:9], 12, v173
	s_nop 1
	v_cndmask_b32_e64 v178, v178, v37, s[8:9]
	v_cmp_eq_u32_e64 s[8:9], 13, v173
	s_nop 1
	v_cndmask_b32_e64 v178, v178, v36, s[8:9]
	v_cmp_eq_u32_e64 s[8:9], 14, v173
	s_nop 1
	v_cndmask_b32_e64 v178, v178, v35, s[8:9]
	v_cmp_eq_u32_e64 s[8:9], 15, v173
	s_nop 1
	v_cndmask_b32_e64 v173, v178, v34, s[8:9]
	v_cmp_eq_u32_e64 s[8:9], 0, v9
	s_nop 1
	v_cndmask_b32_e64 v178, 0, v33, s[8:9]
	v_cmp_eq_u32_e64 s[8:9], 1, v9
	s_nop 1
	v_cndmask_b32_e64 v178, v178, v17, s[8:9]
	v_cmp_eq_u32_e64 s[8:9], 2, v9
	s_nop 1
	v_cndmask_b32_e64 v178, v178, v18, s[8:9]
	v_cmp_eq_u32_e64 s[8:9], 3, v9
	s_nop 1
	v_cndmask_b32_e64 v178, v178, v19, s[8:9]
	v_cmp_eq_u32_e64 s[8:9], 4, v9
	s_nop 1
	v_cndmask_b32_e64 v178, v178, v20, s[8:9]
	v_cmp_eq_u32_e64 s[8:9], 5, v9
	s_nop 1
	v_cndmask_b32_e64 v178, v178, v21, s[8:9]
	v_cmp_eq_u32_e64 s[8:9], 6, v9
	s_nop 1
	v_cndmask_b32_e64 v178, v178, v22, s[8:9]
	v_cmp_eq_u32_e64 s[8:9], 7, v9
	s_nop 1
	v_cndmask_b32_e64 v178, v178, v23, s[8:9]
	v_cmp_eq_u32_e64 s[8:9], 8, v9
	s_nop 1
	v_cndmask_b32_e64 v178, v178, v24, s[8:9]
	v_cmp_eq_u32_e64 s[8:9], 9, v9
	s_nop 1
	v_cndmask_b32_e64 v178, v178, v25, s[8:9]
	v_cmp_eq_u32_e64 s[8:9], 10, v9
	s_nop 1
	v_cndmask_b32_e64 v178, v178, v26, s[8:9]
	v_cmp_eq_u32_e64 s[8:9], 11, v9
	s_nop 1
	v_cndmask_b32_e64 v178, v178, v27, s[8:9]
	v_cmp_eq_u32_e64 s[8:9], 12, v9
	s_nop 1
	v_cndmask_b32_e64 v178, v178, v28, s[8:9]
	v_cmp_eq_u32_e64 s[8:9], 13, v9
	s_nop 1
	v_cndmask_b32_e64 v178, v178, v29, s[8:9]
	v_cmp_eq_u32_e64 s[8:9], 14, v9
	s_nop 1
	v_cndmask_b32_e64 v178, v178, v30, s[8:9]
	v_cmp_eq_u32_e64 s[8:9], 15, v9
	s_nop 1
	v_cndmask_b32_e64 v9, v178, v31, s[8:9]
	v_lshl_add_u32 v9, v173, 7, v9
	v_and_b32_e32 v173, 0xff, v8
	v_bitop3_b32 v178, v8, s10, v8 bitop3:0xc
	v_cndmask_b32_e64 v8, v178, v173, s[6:7]
	v_lshrrev_b32_e32 v173, 4, v8
	v_cmp_gt_u32_e64 s[6:7], 16, v8
	v_and_b32_e32 v8, 15, v8
	s_nop 0
	v_cndmask_b32_e64 v178, 0, v49, s[6:7]
	v_cmp_eq_u32_e64 s[6:7], 1, v173
	s_nop 1
	v_cndmask_b32_e64 v178, v178, v48, s[6:7]
	v_cmp_eq_u32_e64 s[6:7], 2, v173
	s_nop 1
	v_cndmask_b32_e64 v178, v178, v47, s[6:7]
	v_cmp_eq_u32_e64 s[6:7], 3, v173
	s_nop 1
	v_cndmask_b32_e64 v178, v178, v46, s[6:7]
	v_cmp_eq_u32_e64 s[6:7], 4, v173
	s_nop 1
	v_cndmask_b32_e64 v178, v178, v45, s[6:7]
	v_cmp_eq_u32_e64 s[6:7], 5, v173
	s_nop 1
	v_cndmask_b32_e64 v178, v178, v44, s[6:7]
	v_cmp_eq_u32_e64 s[6:7], 6, v173
	s_nop 1
	v_cndmask_b32_e64 v178, v178, v43, s[6:7]
	v_cmp_eq_u32_e64 s[6:7], 7, v173
	s_nop 1
	v_cndmask_b32_e64 v178, v178, v42, s[6:7]
	v_cmp_eq_u32_e64 s[6:7], 8, v173
	s_nop 1
	v_cndmask_b32_e64 v178, v178, v41, s[6:7]
	v_cmp_eq_u32_e64 s[6:7], 9, v173
	s_nop 1
	v_cndmask_b32_e64 v178, v178, v40, s[6:7]
	v_cmp_eq_u32_e64 s[6:7], 10, v173
	s_nop 1
	v_cndmask_b32_e64 v178, v178, v39, s[6:7]
	v_cmp_eq_u32_e64 s[6:7], 11, v173
	s_nop 1
	v_cndmask_b32_e64 v178, v178, v38, s[6:7]
	v_cmp_eq_u32_e64 s[6:7], 12, v173
	s_nop 1
	v_cndmask_b32_e64 v178, v178, v37, s[6:7]
	v_cmp_eq_u32_e64 s[6:7], 13, v173
	s_nop 1
	v_cndmask_b32_e64 v178, v178, v36, s[6:7]
	v_cmp_eq_u32_e64 s[6:7], 14, v173
	s_nop 1
	v_cndmask_b32_e64 v178, v178, v35, s[6:7]
	v_cmp_eq_u32_e64 s[6:7], 15, v173
	s_nop 1
	v_cndmask_b32_e64 v173, v178, v34, s[6:7]
	v_cmp_eq_u32_e64 s[6:7], 0, v8
	s_nop 1
	v_cndmask_b32_e64 v178, 0, v33, s[6:7]
	v_cmp_eq_u32_e64 s[6:7], 1, v8
	s_nop 1
	v_cndmask_b32_e64 v178, v178, v17, s[6:7]
	v_cmp_eq_u32_e64 s[6:7], 2, v8
	s_nop 1
	v_cndmask_b32_e64 v178, v178, v18, s[6:7]
	v_cmp_eq_u32_e64 s[6:7], 3, v8
	s_nop 1
	v_cndmask_b32_e64 v178, v178, v19, s[6:7]
	v_cmp_eq_u32_e64 s[6:7], 4, v8
	s_nop 1
	v_cndmask_b32_e64 v178, v178, v20, s[6:7]
	v_cmp_eq_u32_e64 s[6:7], 5, v8
	s_nop 1
	v_cndmask_b32_e64 v178, v178, v21, s[6:7]
	v_cmp_eq_u32_e64 s[6:7], 6, v8
	s_nop 1
	v_cndmask_b32_e64 v178, v178, v22, s[6:7]
	v_cmp_eq_u32_e64 s[6:7], 7, v8
	s_nop 1
	v_cndmask_b32_e64 v178, v178, v23, s[6:7]
	v_cmp_eq_u32_e64 s[6:7], 8, v8
	s_nop 1
	v_cndmask_b32_e64 v178, v178, v24, s[6:7]
	v_cmp_eq_u32_e64 s[6:7], 9, v8
	s_nop 1
	v_cndmask_b32_e64 v178, v178, v25, s[6:7]
	v_cmp_eq_u32_e64 s[6:7], 10, v8
	s_nop 1
	v_cndmask_b32_e64 v178, v178, v26, s[6:7]
	v_cmp_eq_u32_e64 s[6:7], 11, v8
	s_nop 1
	v_cndmask_b32_e64 v178, v178, v27, s[6:7]
	v_cmp_eq_u32_e64 s[6:7], 12, v8
	s_nop 1
	v_cndmask_b32_e64 v178, v178, v28, s[6:7]
	v_cmp_eq_u32_e64 s[6:7], 13, v8
	s_nop 1
	v_cndmask_b32_e64 v178, v178, v29, s[6:7]
	v_cmp_eq_u32_e64 s[6:7], 14, v8
	s_nop 1
	v_cndmask_b32_e64 v178, v178, v30, s[6:7]
	v_cmp_eq_u32_e64 s[6:7], 15, v8
	s_nop 1
	v_cndmask_b32_e64 v8, v178, v31, s[6:7]
	v_lshl_add_u32 v8, v173, 7, v8
	v_min_f32_e32 v15, v14, v62
	v_and_b32_e32 v173, 0xff, v15
	v_bitop3_b32 v178, v15, s10, v15 bitop3:0xc
	v_cmp_gt_i32_e64 s[8:9], 0, v15
	v_and_b32_e32 v63, 0xffffff00, v15
	v_max_f32_e32 v14, v14, v62
	v_cndmask_b32_e64 v15, v178, v173, s[8:9]
	v_lshrrev_b32_e32 v173, 4, v15
	v_cmp_gt_u32_e64 s[8:9], 16, v15
	v_and_b32_e32 v15, 15, v15
	v_cmp_gt_i32_e64 s[6:7], 0, v14
	v_cndmask_b32_e64 v178, 0, v49, s[8:9]
	v_cmp_eq_u32_e64 s[8:9], 1, v173
	v_and_b32_e32 v62, 0xffffff00, v14
	s_nop 0
	v_cndmask_b32_e64 v178, v178, v48, s[8:9]
	v_cmp_eq_u32_e64 s[8:9], 2, v173
	s_nop 1
	v_cndmask_b32_e64 v178, v178, v47, s[8:9]
	v_cmp_eq_u32_e64 s[8:9], 3, v173
	s_nop 1
	v_cndmask_b32_e64 v178, v178, v46, s[8:9]
	v_cmp_eq_u32_e64 s[8:9], 4, v173
	s_nop 1
	v_cndmask_b32_e64 v178, v178, v45, s[8:9]
	v_cmp_eq_u32_e64 s[8:9], 5, v173
	s_nop 1
	v_cndmask_b32_e64 v178, v178, v44, s[8:9]
	v_cmp_eq_u32_e64 s[8:9], 6, v173
	s_nop 1
	v_cndmask_b32_e64 v178, v178, v43, s[8:9]
	v_cmp_eq_u32_e64 s[8:9], 7, v173
	s_nop 1
	v_cndmask_b32_e64 v178, v178, v42, s[8:9]
	v_cmp_eq_u32_e64 s[8:9], 8, v173
	s_nop 1
	v_cndmask_b32_e64 v178, v178, v41, s[8:9]
	v_cmp_eq_u32_e64 s[8:9], 9, v173
	s_nop 1
	v_cndmask_b32_e64 v178, v178, v40, s[8:9]
	v_cmp_eq_u32_e64 s[8:9], 10, v173
	s_nop 1
	v_cndmask_b32_e64 v178, v178, v39, s[8:9]
	v_cmp_eq_u32_e64 s[8:9], 11, v173
	s_nop 1
	v_cndmask_b32_e64 v178, v178, v38, s[8:9]
	v_cmp_eq_u32_e64 s[8:9], 12, v173
	s_nop 1
	v_cndmask_b32_e64 v178, v178, v37, s[8:9]
	v_cmp_eq_u32_e64 s[8:9], 13, v173
	s_nop 1
	v_cndmask_b32_e64 v178, v178, v36, s[8:9]
	v_cmp_eq_u32_e64 s[8:9], 14, v173
	s_nop 1
	v_cndmask_b32_e64 v178, v178, v35, s[8:9]
	v_cmp_eq_u32_e64 s[8:9], 15, v173
	s_nop 1
	v_cndmask_b32_e64 v173, v178, v34, s[8:9]
	v_cmp_eq_u32_e64 s[8:9], 0, v15
	s_nop 1
	v_cndmask_b32_e64 v178, 0, v33, s[8:9]
	v_cmp_eq_u32_e64 s[8:9], 1, v15
	s_nop 1
	v_cndmask_b32_e64 v178, v178, v17, s[8:9]
	v_cmp_eq_u32_e64 s[8:9], 2, v15
	s_nop 1
	v_cndmask_b32_e64 v178, v178, v18, s[8:9]
	v_cmp_eq_u32_e64 s[8:9], 3, v15
	s_nop 1
	v_cndmask_b32_e64 v178, v178, v19, s[8:9]
	v_cmp_eq_u32_e64 s[8:9], 4, v15
	s_nop 1
	v_cndmask_b32_e64 v178, v178, v20, s[8:9]
	v_cmp_eq_u32_e64 s[8:9], 5, v15
	s_nop 1
	v_cndmask_b32_e64 v178, v178, v21, s[8:9]
	v_cmp_eq_u32_e64 s[8:9], 6, v15
	s_nop 1
	v_cndmask_b32_e64 v178, v178, v22, s[8:9]
	v_cmp_eq_u32_e64 s[8:9], 7, v15
	s_nop 1
	v_cndmask_b32_e64 v178, v178, v23, s[8:9]
	v_cmp_eq_u32_e64 s[8:9], 8, v15
	s_nop 1
	v_cndmask_b32_e64 v178, v178, v24, s[8:9]
	v_cmp_eq_u32_e64 s[8:9], 9, v15
	s_nop 1
	v_cndmask_b32_e64 v178, v178, v25, s[8:9]
	v_cmp_eq_u32_e64 s[8:9], 10, v15
	s_nop 1
	v_cndmask_b32_e64 v178, v178, v26, s[8:9]
	v_cmp_eq_u32_e64 s[8:9], 11, v15
	s_nop 1
	v_cndmask_b32_e64 v178, v178, v27, s[8:9]
	v_cmp_eq_u32_e64 s[8:9], 12, v15
	s_nop 1
	v_cndmask_b32_e64 v178, v178, v28, s[8:9]
	v_cmp_eq_u32_e64 s[8:9], 13, v15
	s_nop 1
	v_cndmask_b32_e64 v178, v178, v29, s[8:9]
	v_cmp_eq_u32_e64 s[8:9], 14, v15
	s_nop 1
	v_cndmask_b32_e64 v178, v178, v30, s[8:9]
	v_cmp_eq_u32_e64 s[8:9], 15, v15
	s_nop 1
	v_cndmask_b32_e64 v15, v178, v31, s[8:9]
	v_lshl_add_u32 v15, v173, 7, v15
	v_and_b32_e32 v173, 0xff, v14
	v_bitop3_b32 v178, v14, s10, v14 bitop3:0xc
	v_cndmask_b32_e64 v14, v178, v173, s[6:7]
	v_lshrrev_b32_e32 v173, 4, v14
	v_cmp_gt_u32_e64 s[6:7], 16, v14
	v_and_b32_e32 v14, 15, v14
	v_readlane_b32 s8, v253, 23
	v_cndmask_b32_e64 v178, 0, v49, s[6:7]
	v_cmp_eq_u32_e64 s[6:7], 1, v173
	v_readlane_b32 s9, v253, 24
	s_nop 0
	v_cndmask_b32_e64 v178, v178, v48, s[6:7]
	v_cmp_eq_u32_e64 s[6:7], 2, v173
	s_nop 1
	v_cndmask_b32_e64 v178, v178, v47, s[6:7]
	v_cmp_eq_u32_e64 s[6:7], 3, v173
	s_nop 1
	v_cndmask_b32_e64 v178, v178, v46, s[6:7]
	v_cmp_eq_u32_e64 s[6:7], 4, v173
	s_nop 1
	v_cndmask_b32_e64 v178, v178, v45, s[6:7]
	v_cmp_eq_u32_e64 s[6:7], 5, v173
	s_nop 1
	v_cndmask_b32_e64 v178, v178, v44, s[6:7]
	v_cmp_eq_u32_e64 s[6:7], 6, v173
	s_nop 1
	v_cndmask_b32_e64 v178, v178, v43, s[6:7]
	v_cmp_eq_u32_e64 s[6:7], 7, v173
	s_nop 1
	v_cndmask_b32_e64 v178, v178, v42, s[6:7]
	v_cmp_eq_u32_e64 s[6:7], 8, v173
	s_nop 1
	v_cndmask_b32_e64 v178, v178, v41, s[6:7]
	v_cmp_eq_u32_e64 s[6:7], 9, v173
	s_nop 1
	v_cndmask_b32_e64 v178, v178, v40, s[6:7]
	v_cmp_eq_u32_e64 s[6:7], 10, v173
	s_nop 1
	v_cndmask_b32_e64 v178, v178, v39, s[6:7]
	v_cmp_eq_u32_e64 s[6:7], 11, v173
	s_nop 1
	v_cndmask_b32_e64 v178, v178, v38, s[6:7]
	v_cmp_eq_u32_e64 s[6:7], 12, v173
	s_nop 1
	v_cndmask_b32_e64 v178, v178, v37, s[6:7]
	v_cmp_eq_u32_e64 s[6:7], 13, v173
	s_nop 1
	v_cndmask_b32_e64 v178, v178, v36, s[6:7]
	v_cmp_eq_u32_e64 s[6:7], 14, v173
	s_nop 1
	v_cndmask_b32_e64 v178, v178, v35, s[6:7]
	v_cmp_eq_u32_e64 s[6:7], 15, v173
	s_nop 1
	v_cndmask_b32_e64 v173, v178, v34, s[6:7]
	v_cmp_eq_u32_e64 s[6:7], 0, v14
	s_nop 1
	v_cndmask_b32_e64 v178, 0, v33, s[6:7]
	v_cmp_eq_u32_e64 s[6:7], 1, v14
	s_nop 1
	v_cndmask_b32_e64 v178, v178, v17, s[6:7]
	v_cmp_eq_u32_e64 s[6:7], 2, v14
	s_nop 1
	v_cndmask_b32_e64 v178, v178, v18, s[6:7]
	v_cmp_eq_u32_e64 s[6:7], 3, v14
	s_nop 1
	v_cndmask_b32_e64 v178, v178, v19, s[6:7]
	v_cmp_eq_u32_e64 s[6:7], 4, v14
	s_nop 1
	v_cndmask_b32_e64 v178, v178, v20, s[6:7]
	v_cmp_eq_u32_e64 s[6:7], 5, v14
	s_nop 1
	v_cndmask_b32_e64 v178, v178, v21, s[6:7]
	v_cmp_eq_u32_e64 s[6:7], 6, v14
	s_nop 1
	v_cndmask_b32_e64 v178, v178, v22, s[6:7]
	v_cmp_eq_u32_e64 s[6:7], 7, v14
	s_nop 1
	v_cndmask_b32_e64 v178, v178, v23, s[6:7]
	v_cmp_eq_u32_e64 s[6:7], 8, v14
	s_nop 1
	v_cndmask_b32_e64 v178, v178, v24, s[6:7]
	v_cmp_eq_u32_e64 s[6:7], 9, v14
	s_nop 1
	v_cndmask_b32_e64 v178, v178, v25, s[6:7]
	v_cmp_eq_u32_e64 s[6:7], 10, v14
	s_nop 1
	v_cndmask_b32_e64 v178, v178, v26, s[6:7]
	v_cmp_eq_u32_e64 s[6:7], 11, v14
	s_nop 1
	v_cndmask_b32_e64 v178, v178, v27, s[6:7]
	v_cmp_eq_u32_e64 s[6:7], 12, v14
	s_nop 1
	v_cndmask_b32_e64 v178, v178, v28, s[6:7]
	v_cmp_eq_u32_e64 s[6:7], 13, v14
	s_nop 1
	v_cndmask_b32_e64 v178, v178, v29, s[6:7]
	v_cmp_eq_u32_e64 s[6:7], 14, v14
	s_nop 1
	v_cndmask_b32_e64 v178, v178, v30, s[6:7]
	v_cmp_eq_u32_e64 s[6:7], 15, v14
	s_nop 1
	v_cndmask_b32_e64 v14, v178, v31, s[6:7]
	v_lshl_add_u32 v14, v173, 7, v14
	v_and_b32_e32 v173, 0xff, v13
	v_bitop3_b32 v178, v13, s10, v13 bitop3:0xc
	v_cmp_gt_i32_e64 s[6:7], 0, v13
	s_nop 1
	v_cndmask_b32_e64 v13, v178, v173, s[6:7]
	v_lshrrev_b32_e32 v173, 4, v13
	v_cmp_gt_u32_e64 s[6:7], 16, v13
	v_and_b32_e32 v13, 15, v13
	s_nop 0
	v_cndmask_b32_e64 v178, 0, v49, s[6:7]
	v_cmp_eq_u32_e64 s[6:7], 1, v173
	s_nop 1
	v_cndmask_b32_e64 v178, v178, v48, s[6:7]
	v_cmp_eq_u32_e64 s[6:7], 2, v173
	s_nop 1
	v_cndmask_b32_e64 v178, v178, v47, s[6:7]
	v_cmp_eq_u32_e64 s[6:7], 3, v173
	s_nop 1
	v_cndmask_b32_e64 v178, v178, v46, s[6:7]
	v_cmp_eq_u32_e64 s[6:7], 4, v173
	s_nop 1
	v_cndmask_b32_e64 v178, v178, v45, s[6:7]
	v_cmp_eq_u32_e64 s[6:7], 5, v173
	s_nop 1
	v_cndmask_b32_e64 v178, v178, v44, s[6:7]
	v_cmp_eq_u32_e64 s[6:7], 6, v173
	s_nop 1
	v_cndmask_b32_e64 v178, v178, v43, s[6:7]
	v_cmp_eq_u32_e64 s[6:7], 7, v173
	s_nop 1
	v_cndmask_b32_e64 v178, v178, v42, s[6:7]
	v_cmp_eq_u32_e64 s[6:7], 8, v173
	s_nop 1
	v_cndmask_b32_e64 v178, v178, v41, s[6:7]
	v_cmp_eq_u32_e64 s[6:7], 9, v173
	s_nop 1
	v_cndmask_b32_e64 v178, v178, v40, s[6:7]
	v_cmp_eq_u32_e64 s[6:7], 10, v173
	s_nop 1
	v_cndmask_b32_e64 v178, v178, v39, s[6:7]
	v_cmp_eq_u32_e64 s[6:7], 11, v173
	s_nop 1
	v_cndmask_b32_e64 v178, v178, v38, s[6:7]
	v_cmp_eq_u32_e64 s[6:7], 12, v173
	s_nop 1
	v_cndmask_b32_e64 v178, v178, v37, s[6:7]
	v_cmp_eq_u32_e64 s[6:7], 13, v173
	s_nop 1
	v_cndmask_b32_e64 v178, v178, v36, s[6:7]
	v_cmp_eq_u32_e64 s[6:7], 14, v173
	s_nop 1
	v_cndmask_b32_e64 v178, v178, v35, s[6:7]
	v_cmp_eq_u32_e64 s[6:7], 15, v173
	s_nop 1
	v_cndmask_b32_e64 v173, v178, v34, s[6:7]
	v_cmp_eq_u32_e64 s[6:7], 0, v13
	s_nop 1
	v_cndmask_b32_e64 v178, 0, v33, s[6:7]
	v_cmp_eq_u32_e64 s[6:7], 1, v13
	s_nop 1
	v_cndmask_b32_e64 v178, v178, v17, s[6:7]
	v_cmp_eq_u32_e64 s[6:7], 2, v13
	s_nop 1
	v_cndmask_b32_e64 v178, v178, v18, s[6:7]
	v_cmp_eq_u32_e64 s[6:7], 3, v13
	s_nop 1
	v_cndmask_b32_e64 v178, v178, v19, s[6:7]
	v_cmp_eq_u32_e64 s[6:7], 4, v13
	s_nop 1
	v_cndmask_b32_e64 v178, v178, v20, s[6:7]
	v_cmp_eq_u32_e64 s[6:7], 5, v13
	s_nop 1
	v_cndmask_b32_e64 v178, v178, v21, s[6:7]
	v_cmp_eq_u32_e64 s[6:7], 6, v13
	s_nop 1
	v_cndmask_b32_e64 v178, v178, v22, s[6:7]
	v_cmp_eq_u32_e64 s[6:7], 7, v13
	s_nop 1
	v_cndmask_b32_e64 v178, v178, v23, s[6:7]
	v_cmp_eq_u32_e64 s[6:7], 8, v13
	s_nop 1
	v_cndmask_b32_e64 v178, v178, v24, s[6:7]
	v_cmp_eq_u32_e64 s[6:7], 9, v13
	s_nop 1
	v_cndmask_b32_e64 v178, v178, v25, s[6:7]
	v_cmp_eq_u32_e64 s[6:7], 10, v13
	s_nop 1
	v_cndmask_b32_e64 v178, v178, v26, s[6:7]
	v_cmp_eq_u32_e64 s[6:7], 11, v13
	s_nop 1
	v_cndmask_b32_e64 v178, v178, v27, s[6:7]
	v_cmp_eq_u32_e64 s[6:7], 12, v13
	s_nop 1
	v_cndmask_b32_e64 v178, v178, v28, s[6:7]
	v_cmp_eq_u32_e64 s[6:7], 13, v13
	s_nop 1
	v_cndmask_b32_e64 v178, v178, v29, s[6:7]
	v_cmp_eq_u32_e64 s[6:7], 14, v13
	s_nop 1
	v_cndmask_b32_e64 v178, v178, v30, s[6:7]
	v_cmp_eq_u32_e64 s[6:7], 15, v13
	s_nop 1
	v_cndmask_b32_e64 v13, v178, v31, s[6:7]
	v_lshl_add_u32 v13, v173, 7, v13
	v_and_b32_e32 v173, 0xff, v59
	v_bitop3_b32 v178, v59, s10, v59 bitop3:0xc
	v_cndmask_b32_e32 v59, v178, v173, vcc
	v_lshrrev_b32_e32 v173, 4, v59
	v_cmp_gt_u32_e32 vcc, 16, v59
	s_nop 1
	v_cndmask_b32_e32 v49, 0, v49, vcc
	v_cmp_eq_u32_e32 vcc, 1, v173
	s_nop 1
	v_cndmask_b32_e32 v48, v49, v48, vcc
	v_cmp_eq_u32_e32 vcc, 2, v173
	s_nop 1
	v_cndmask_b32_e32 v47, v48, v47, vcc
	v_cmp_eq_u32_e32 vcc, 3, v173
	s_nop 1
	v_cndmask_b32_e32 v46, v47, v46, vcc
	v_cmp_eq_u32_e32 vcc, 4, v173
	s_nop 1
	v_cndmask_b32_e32 v45, v46, v45, vcc
	v_cmp_eq_u32_e32 vcc, 5, v173
	s_nop 1
	v_cndmask_b32_e32 v44, v45, v44, vcc
	v_cmp_eq_u32_e32 vcc, 6, v173
	s_nop 1
	v_cndmask_b32_e32 v43, v44, v43, vcc
	v_cmp_eq_u32_e32 vcc, 7, v173
	s_nop 1
	v_cndmask_b32_e32 v42, v43, v42, vcc
	v_cmp_eq_u32_e32 vcc, 8, v173
	s_nop 1
	v_cndmask_b32_e32 v41, v42, v41, vcc
	v_cmp_eq_u32_e32 vcc, 9, v173
	s_nop 1
	v_cndmask_b32_e32 v40, v41, v40, vcc
	v_cmp_eq_u32_e32 vcc, 10, v173
	s_nop 1
	v_cndmask_b32_e32 v39, v40, v39, vcc
	v_cmp_eq_u32_e32 vcc, 11, v173
	s_nop 1
	v_cndmask_b32_e32 v38, v39, v38, vcc
	v_cmp_eq_u32_e32 vcc, 12, v173
	v_and_b32_e32 v39, 15, v59
	s_nop 0
	v_cndmask_b32_e32 v37, v38, v37, vcc
	v_cmp_eq_u32_e32 vcc, 13, v173
	s_nop 1
	v_cndmask_b32_e32 v36, v37, v36, vcc
	v_cmp_eq_u32_e32 vcc, 14, v173
	s_nop 1
	v_cndmask_b32_e32 v35, v36, v35, vcc
	v_cmp_eq_u32_e32 vcc, 15, v173
	v_exp_f32_e32 v36, v12
	v_and_b32_e32 v12, 0xffffff00, v32
	v_cndmask_b32_e32 v38, v35, v34, vcc
	v_cmp_eq_u32_e32 vcc, 0, v39
	v_sub_f32_e32 v12, v12, v60
	v_mul_f32_e32 v12, 0x3fb8aa3b, v12
	v_cndmask_b32_e32 v33, 0, v33, vcc
	v_cmp_eq_u32_e32 vcc, 1, v39
	v_exp_f32_e32 v37, v12
	s_nop 0
	v_cndmask_b32_e32 v17, v33, v17, vcc
	v_cmp_eq_u32_e32 vcc, 2, v39
	v_sub_f32_e32 v33, v51, v60
	v_mul_f32_e32 v33, 0x3fb8aa3b, v33
	v_cndmask_b32_e32 v17, v17, v18, vcc
	v_cmp_eq_u32_e32 vcc, 3, v39
	v_sub_f32_e32 v18, v60, v60
	v_mul_f32_e32 v18, 0x3fb8aa3b, v18
	v_cndmask_b32_e32 v17, v17, v19, vcc
	v_cmp_eq_u32_e32 vcc, 4, v39
	v_sub_f32_e32 v19, v61, v60
	v_exp_f32_e32 v18, v18
	v_cndmask_b32_e32 v17, v17, v20, vcc
	v_cmp_eq_u32_e32 vcc, 5, v39
	v_mul_f32_e32 v19, 0x3fb8aa3b, v19
	v_sub_f32_e32 v20, v62, v60
	v_cndmask_b32_e32 v17, v17, v21, vcc
	v_exp_f32_e32 v19, v19
	v_mul_f32_e32 v20, 0x3fb8aa3b, v20
	v_sub_f32_e32 v21, v63, v60
	v_cmp_eq_u32_e32 vcc, 6, v39
	v_exp_f32_e32 v20, v20
	v_mul_f32_e32 v21, 0x3fb8aa3b, v21
	v_cndmask_b32_e32 v17, v17, v22, vcc
	v_cmp_eq_u32_e32 vcc, 7, v39
	v_exp_f32_e32 v21, v21
	v_add_f32_e32 v22, 0, v18
	v_cndmask_b32_e32 v17, v17, v23, vcc
	v_cmp_eq_u32_e32 vcc, 8, v39
	v_add_f32_e32 v22, v19, v22
	v_add_f32_e32 v22, v20, v22
	v_cndmask_b32_e32 v17, v17, v24, vcc
	v_cmp_eq_u32_e32 vcc, 9, v39
	v_sub_f32_e32 v23, v56, v60
	v_mul_f32_e32 v23, 0x3fb8aa3b, v23
	v_cndmask_b32_e32 v17, v17, v25, vcc
	v_cmp_eq_u32_e32 vcc, 10, v39
	v_sub_f32_e32 v24, v55, v60
	v_exp_f32_e32 v23, v23
	v_cndmask_b32_e32 v17, v17, v26, vcc
	v_add_f32_e32 v26, v21, v22
	v_sub_f32_e32 v22, v58, v60
	v_mul_f32_e32 v22, 0x3fb8aa3b, v22
	v_exp_f32_e32 v22, v22
	v_mul_f32_e32 v24, 0x3fb8aa3b, v24
	v_sub_f32_e32 v25, v54, v60
	v_exp_f32_e32 v24, v24
	v_mul_f32_e32 v25, 0x3fb8aa3b, v25
	v_cmp_eq_u32_e32 vcc, 11, v39
	v_exp_f32_e32 v25, v25
	v_add_f32_e32 v26, v22, v26
	v_cndmask_b32_e32 v17, v17, v27, vcc
	v_cmp_eq_u32_e32 vcc, 12, v39
	v_add_f32_e32 v26, v23, v26
	v_add_f32_e32 v26, v24, v26
	v_cndmask_b32_e32 v17, v17, v28, vcc
	v_cmp_eq_u32_e32 vcc, 13, v39
	v_sub_f32_e32 v27, v57, v60
	v_mul_f32_e32 v27, 0x3fb8aa3b, v27
	v_cndmask_b32_e32 v17, v17, v29, vcc
	v_cmp_eq_u32_e32 vcc, 14, v39
	v_sub_f32_e32 v28, v53, v60
	v_exp_f32_e32 v27, v27
	v_cndmask_b32_e32 v17, v17, v30, vcc
	v_add_f32_e32 v30, v25, v26
	v_sub_f32_e32 v26, v209, v60
	v_mul_f32_e32 v26, 0x3fb8aa3b, v26
	v_exp_f32_e32 v26, v26
	v_mul_f32_e32 v28, 0x3fb8aa3b, v28
	v_sub_f32_e32 v29, v52, v60
	v_exp_f32_e32 v28, v28
	v_mul_f32_e32 v29, 0x3fb8aa3b, v29
	v_exp_f32_e32 v29, v29
	v_exp_f32_e32 v34, v33
	v_sub_f32_e32 v33, v50, v60
	v_add_f32_e32 v30, v26, v30
	v_mul_f32_e32 v33, 0x3fb8aa3b, v33
	v_add_f32_e32 v30, v27, v30
	v_exp_f32_e32 v35, v33
	v_add_f32_e32 v30, v28, v30
	v_add_f32_e32 v30, v29, v30
	v_add_f32_e32 v12, v34, v30
	v_add_f32_e32 v12, v35, v12
	v_add_f32_e32 v12, v36, v12
	v_add_f32_e32 v30, v37, v12
	v_div_scale_f32 v32, s[6:7], v30, v30, 1.0
	v_rcp_f32_e32 v33, v32
	v_cmp_eq_u32_e32 vcc, 15, v39
	v_readlane_b32 s6, v255, 46
	s_lshl_b32 s6, s6, 4
	v_cndmask_b32_e32 v12, v17, v31, vcc
	v_fma_f32 v17, -v32, v33, 1.0
	v_fmac_f32_e32 v33, v17, v33
	v_div_scale_f32 v17, vcc, 1.0, v30, 1.0
	v_mul_f32_e32 v31, v17, v33
	v_lshl_add_u32 v12, v38, 7, v12
	v_fma_f32 v38, -v32, v31, v17
	v_fmac_f32_e32 v31, v38, v33
	v_fma_f32 v17, -v32, v31, v17
	v_div_fmas_f32 v17, v17, v33, v31
	v_div_fixup_f32 v30, v17, v30, 1.0
	v_lshlrev_b64 v[16:17], 9, v[176:177]
	s_ashr_i32 s7, s6, 31
	v_lshl_add_u64 v[32:33], s[94:95], 0, v[16:17]
	s_lshl_b64 s[6:7], s[6:7], 2
	v_lshl_add_u64 v[32:33], v[32:33], 0, s[6:7]
	v_lshl_add_u64 v[16:17], s[8:9], 0, v[16:17]
	v_lshl_add_u64 v[16:17], v[16:17], 0, s[6:7]
	global_store_dwordx4 v[32:33], v[12:15], off
	v_readlane_b32 s8, v255, 44
	v_readlane_b32 s9, v255, 45
	v_pk_mul_f32 v[12:13], v[18:19], v[30:31] op_sel_hi:[1,0]
	v_pk_mul_f32 v[14:15], v[20:21], v[30:31] op_sel_hi:[1,0]
	global_store_dwordx4 v[16:17], v[12:15], off
	global_store_dwordx4 v[32:33], v[8:11], off offset:16
	s_nop 1
	v_pk_mul_f32 v[8:9], v[22:23], v[30:31] op_sel_hi:[1,0]
	v_pk_mul_f32 v[10:11], v[24:25], v[30:31] op_sel_hi:[1,0]
	global_store_dwordx4 v[16:17], v[8:11], off offset:16
	global_store_dwordx4 v[32:33], v[4:7], off offset:32
	s_nop 1
	v_pk_mul_f32 v[4:5], v[26:27], v[30:31] op_sel_hi:[1,0]
	v_pk_mul_f32 v[6:7], v[28:29], v[30:31] op_sel_hi:[1,0]
	global_store_dwordx4 v[16:17], v[4:7], off offset:32
	global_store_dwordx4 v[32:33], v[0:3], off offset:48
	s_nop 1
	v_pk_mul_f32 v[0:1], v[34:35], v[30:31] op_sel_hi:[1,0]
	v_pk_mul_f32 v[2:3], v[36:37], v[30:31] op_sel_hi:[1,0]
	global_store_dwordx4 v[16:17], v[0:3], off offset:48
	s_branch .LBB0_696
